# v16 + SP2 LDS-DMA pieces issued before the A-fragment ds_reads in every GEMM K-loop
# speedup vs baseline: 1.0018x; 1.0018x over previous
.LBB0_390:
	s_add_u32 s1, s42, 0x100
	v_lshl_add_u64 v[142:143], s[40:41], 0, v[130:131]
	s_addc_u32 s24, s43, 0
	s_mov_b32 s25, -2
	s_mov_b64 s[42:43], 0
	s_add_u32 s14, s40, s42
	s_addc_u32 s15, s41, s43
	s_add_u32 s34, s14, 0x100
	s_addc_u32 s35, s15, 0
	s_add_u32 s44, s1, s42
	s_addc_u32 s45, s24, s43
	s_cmpk_eq_i32 s42, 0x700
	s_cselect_b64 vcc, -1, 0
	s_and_b64 s[14:15], vcc, exec
	s_cselect_b32 s15, s55, s35
	s_cselect_b32 s14, s54, s34
	s_cselect_b32 s35, s69, s45
	s_cselect_b32 s34, s68, s44
	s_add_i32 s44, 0, 0x11000
	v_add_u32_e32 v145, s44, v1
	s_add_i32 s45, 0, 0x15000
	ds_read_b128 v[146:149], v145
	ds_read_b128 v[150:153], v145 offset:1024
	ds_read_b128 v[154:157], v145 offset:2048
	ds_read_b128 v[158:161], v145 offset:3072
	v_add_u32_e32 v145, s45, v1
	ds_read_b128 v[162:165], v145
	ds_read_b128 v[166:169], v145 offset:1024
	ds_read_b128 v[170:173], v145 offset:2048
	ds_read_b128 v[174:177], v145 offset:3072
	v_cndmask_b32_e32 v193, v131, v141, vcc
	v_cndmask_b32_e32 v192, v130, v140, vcc
	v_lshl_add_u64 v[220:221], v[142:143], 0, s[42:43]
	v_lshl_add_u64 v[222:223], v[220:221], 0, s[6:7]
	s_add_i32 m0, s28, 0xd000
	ds_read_b128 v[178:181], v144 offset:4096
	ds_read_b128 v[182:185], v144 offset:5120
	ds_read_b128 v[196:199], v144 offset:6144
	ds_read_b128 v[200:203], v144 offset:7168
	ds_read_b128 v[204:207], v144 offset:8192
	ds_read_b128 v[208:211], v144 offset:9216
	ds_read_b128 v[212:215], v144 offset:10240
	ds_read_b128 v[216:219], v144 offset:11264
	global_load_lds_dwordx4 v[222:223], off
	v_lshl_add_u64 v[220:221], v[220:221], 0, s[8:9]
	s_add_i32 m0, s28, 0xf000
	s_nop 0
	global_load_lds_dwordx4 v[220:221], off
	s_waitcnt vmcnt(8)
	s_waitcnt lgkmcnt(0)
	s_barrier
	s_setprio 1
	s_waitcnt lgkmcnt(0)
	v_mfma_f32_16x16x32_bf16 v[126:129], v[146:149], v[178:181], 0
	v_mfma_f32_16x16x32_bf16 v[122:125], v[154:157], v[178:181], 0
	v_mfma_f32_16x16x32_bf16 v[110:113], v[146:149], v[196:199], 0
	v_mfma_f32_16x16x32_bf16 v[106:109], v[154:157], v[196:199], 0
	v_mfma_f32_16x16x32_bf16 v[94:97], v[146:149], v[204:207], 0
	v_mfma_f32_16x16x32_bf16 v[90:93], v[154:157], v[204:207], 0
	v_mfma_f32_16x16x32_bf16 v[78:81], v[146:149], v[212:215], 0
	v_mfma_f32_16x16x32_bf16 v[74:77], v[154:157], v[212:215], 0
	v_mfma_f32_16x16x32_bf16 v[126:129], v[150:153], v[182:185], v[126:129]
	v_mfma_f32_16x16x32_bf16 v[122:125], v[158:161], v[182:185], v[122:125]
	v_mfma_f32_16x16x32_bf16 v[110:113], v[150:153], v[200:203], v[110:113]
	v_mfma_f32_16x16x32_bf16 v[106:109], v[158:161], v[200:203], v[106:109]
	v_mfma_f32_16x16x32_bf16 v[94:97], v[150:153], v[208:211], v[94:97]
	v_mfma_f32_16x16x32_bf16 v[90:93], v[158:161], v[208:211], v[90:93]
	v_mfma_f32_16x16x32_bf16 v[78:81], v[150:153], v[216:219], v[78:81]
	v_mfma_f32_16x16x32_bf16 v[74:77], v[158:161], v[216:219], v[74:77]
	s_setprio 0
	s_setprio 1
	v_mfma_f32_16x16x32_bf16 v[118:121], v[162:165], v[178:181], 0
	v_mfma_f32_16x16x32_bf16 v[114:117], v[170:173], v[178:181], 0
	v_mfma_f32_16x16x32_bf16 v[102:105], v[162:165], v[196:199], 0
	v_mfma_f32_16x16x32_bf16 v[98:101], v[170:173], v[196:199], 0
	v_mfma_f32_16x16x32_bf16 v[86:89], v[162:165], v[204:207], 0
	v_mfma_f32_16x16x32_bf16 v[82:85], v[170:173], v[204:207], 0
	v_mfma_f32_16x16x32_bf16 v[70:73], v[162:165], v[212:215], 0
	v_mfma_f32_16x16x32_bf16 v[66:69], v[170:173], v[212:215], 0
	v_mfma_f32_16x16x32_bf16 v[118:121], v[166:169], v[182:185], v[118:121]
	v_mfma_f32_16x16x32_bf16 v[114:117], v[174:177], v[182:185], v[114:117]
	v_mfma_f32_16x16x32_bf16 v[102:105], v[166:169], v[200:203], v[102:105]
	v_mfma_f32_16x16x32_bf16 v[98:101], v[174:177], v[200:203], v[98:101]
	v_mfma_f32_16x16x32_bf16 v[86:89], v[166:169], v[208:211], v[86:89]
	v_mfma_f32_16x16x32_bf16 v[82:85], v[174:177], v[208:211], v[82:85]
	v_mfma_f32_16x16x32_bf16 v[70:73], v[166:169], v[216:219], v[70:73]
	v_mfma_f32_16x16x32_bf16 v[66:69], v[174:177], v[216:219], v[66:69]
	s_setprio 0
	s_barrier
	s_add_i32 s44, s44, s12
	v_lshl_add_u64 v[220:221], s[34:35], 0, v[186:187]
	s_mov_b32 m0, s44
	global_load_lds_dwordx4 v186, s[34:35]
	v_lshl_add_u64 v[222:223], v[220:221], 0, s[82:83]
	s_add_i32 m0, s44, 0x2000
	s_add_i32 s34, s45, s12
	global_load_lds_dwordx4 v[222:223], off
	v_lshl_add_u64 v[222:223], v[220:221], 0, s[64:65]
	s_mov_b32 m0, s34
	v_lshl_add_u64 v[192:193], s[14:15], 0, v[192:193]
	global_load_lds_dwordx4 v[222:223], off
	v_lshl_add_u64 v[222:223], v[220:221], 0, s[86:87]
	s_add_i32 m0, s34, 0x2000
	s_nop 0
	global_load_lds_dwordx4 v[222:223], off
	s_mov_b32 m0, s29
	v_lshl_add_u64 v[222:223], v[192:193], 0, s[82:83]
	global_load_lds_dwordx4 v[192:193], off
	s_mov_b32 m0, s47
	s_nop 0
	global_load_lds_dwordx4 v[222:223], off
	ds_read_b128 v[178:181], v144 offset:20480
	ds_read_b128 v[182:185], v144 offset:21504
	ds_read_b128 v[196:199], v144 offset:22528
	ds_read_b128 v[200:203], v144 offset:23552
	ds_read_b128 v[204:207], v144 offset:24576
	ds_read_b128 v[208:211], v144 offset:25600
	ds_read_b128 v[212:215], v144 offset:26624
	ds_read_b128 v[216:219], v144 offset:27648
	s_waitcnt vmcnt(8)
	s_waitcnt lgkmcnt(0)
	s_barrier
	s_setprio 1
	s_waitcnt lgkmcnt(0)
	v_mfma_f32_16x16x32_bf16 v[62:65], v[146:149], v[178:181], 0
	v_mfma_f32_16x16x32_bf16 v[58:61], v[154:157], v[178:181], 0
	v_mfma_f32_16x16x32_bf16 v[46:49], v[146:149], v[196:199], 0
	v_mfma_f32_16x16x32_bf16 v[42:45], v[154:157], v[196:199], 0
	v_mfma_f32_16x16x32_bf16 v[30:33], v[146:149], v[204:207], 0
	v_mfma_f32_16x16x32_bf16 v[26:29], v[154:157], v[204:207], 0
	v_mfma_f32_16x16x32_bf16 v[14:17], v[146:149], v[212:215], 0
	v_mfma_f32_16x16x32_bf16 v[10:13], v[154:157], v[212:215], 0
	v_mfma_f32_16x16x32_bf16 v[62:65], v[150:153], v[182:185], v[62:65]
	v_mfma_f32_16x16x32_bf16 v[58:61], v[158:161], v[182:185], v[58:61]
	v_mfma_f32_16x16x32_bf16 v[46:49], v[150:153], v[200:203], v[46:49]
	v_mfma_f32_16x16x32_bf16 v[42:45], v[158:161], v[200:203], v[42:45]
	v_mfma_f32_16x16x32_bf16 v[30:33], v[150:153], v[208:211], v[30:33]
	v_mfma_f32_16x16x32_bf16 v[26:29], v[158:161], v[208:211], v[26:29]
	v_mfma_f32_16x16x32_bf16 v[14:17], v[150:153], v[216:219], v[14:17]
	v_mfma_f32_16x16x32_bf16 v[10:13], v[158:161], v[216:219], v[10:13]
	s_setprio 0
	s_setprio 1
	v_mfma_f32_16x16x32_bf16 v[54:57], v[162:165], v[178:181], 0
	v_mfma_f32_16x16x32_bf16 v[50:53], v[170:173], v[178:181], 0
	v_mfma_f32_16x16x32_bf16 v[38:41], v[162:165], v[196:199], 0
	v_mfma_f32_16x16x32_bf16 v[34:37], v[170:173], v[196:199], 0
	v_mfma_f32_16x16x32_bf16 v[22:25], v[162:165], v[204:207], 0
	v_mfma_f32_16x16x32_bf16 v[18:21], v[170:173], v[204:207], 0
	v_mfma_f32_16x16x32_bf16 v[6:9], v[162:165], v[212:215], 0
	v_mfma_f32_16x16x32_bf16 v[2:5], v[170:173], v[212:215], 0
	v_mfma_f32_16x16x32_bf16 v[54:57], v[166:169], v[182:185], v[54:57]
	v_mfma_f32_16x16x32_bf16 v[50:53], v[174:177], v[182:185], v[50:53]
	v_mfma_f32_16x16x32_bf16 v[38:41], v[166:169], v[200:203], v[38:41]
	v_mfma_f32_16x16x32_bf16 v[34:37], v[174:177], v[200:203], v[34:37]
	v_mfma_f32_16x16x32_bf16 v[22:25], v[166:169], v[208:211], v[22:25]
	v_mfma_f32_16x16x32_bf16 v[18:21], v[174:177], v[208:211], v[18:21]
	v_mfma_f32_16x16x32_bf16 v[6:9], v[166:169], v[216:219], v[6:9]
	v_mfma_f32_16x16x32_bf16 v[2:5], v[174:177], v[216:219], v[2:5]
	s_setprio 0
	s_barrier
	s_add_i32 s14, 0, 0x19000
	v_add_u32_e32 v145, s14, v1
	s_add_i32 s15, 0, 0x1d000
	ds_read_b128 v[146:149], v145
	ds_read_b128 v[150:153], v145 offset:1024
	ds_read_b128 v[154:157], v145 offset:2048
	ds_read_b128 v[158:161], v145 offset:3072
	v_add_u32_e32 v145, s15, v1
	ds_read_b128 v[162:165], v145
	ds_read_b128 v[166:169], v145 offset:1024
	ds_read_b128 v[170:173], v145 offset:2048
	ds_read_b128 v[174:177], v145 offset:3072
	s_mov_b32 m0, s60
	v_lshl_add_u64 v[222:223], v[192:193], 0, s[64:65]
	ds_read_b128 v[178:181], v144 offset:36864
	ds_read_b128 v[182:185], v144 offset:37888
	ds_read_b128 v[196:199], v144 offset:38912
	ds_read_b128 v[200:203], v144 offset:39936
	ds_read_b128 v[204:207], v144 offset:40960
	ds_read_b128 v[208:211], v144 offset:41984
	ds_read_b128 v[212:215], v144 offset:43008
	ds_read_b128 v[216:219], v144 offset:44032
	global_load_lds_dwordx4 v[222:223], off
	v_lshl_add_u64 v[222:223], v[192:193], 0, s[86:87]
	s_mov_b32 m0, s61
	s_nop 0
	global_load_lds_dwordx4 v[222:223], off
	s_waitcnt vmcnt(8)
	s_waitcnt lgkmcnt(0)
	s_barrier
	s_setprio 1
	s_waitcnt lgkmcnt(0)
	v_mfma_f32_16x16x32_bf16 v[126:129], v[146:149], v[178:181], v[126:129]
	v_mfma_f32_16x16x32_bf16 v[122:125], v[154:157], v[178:181], v[122:125]
	v_mfma_f32_16x16x32_bf16 v[110:113], v[146:149], v[196:199], v[110:113]
	v_mfma_f32_16x16x32_bf16 v[106:109], v[154:157], v[196:199], v[106:109]
	v_mfma_f32_16x16x32_bf16 v[94:97], v[146:149], v[204:207], v[94:97]
	v_mfma_f32_16x16x32_bf16 v[90:93], v[154:157], v[204:207], v[90:93]
	v_mfma_f32_16x16x32_bf16 v[78:81], v[146:149], v[212:215], v[78:81]
	v_mfma_f32_16x16x32_bf16 v[74:77], v[154:157], v[212:215], v[74:77]
	v_mfma_f32_16x16x32_bf16 v[126:129], v[150:153], v[182:185], v[126:129]
	v_mfma_f32_16x16x32_bf16 v[122:125], v[158:161], v[182:185], v[122:125]
	v_mfma_f32_16x16x32_bf16 v[110:113], v[150:153], v[200:203], v[110:113]
	v_mfma_f32_16x16x32_bf16 v[106:109], v[158:161], v[200:203], v[106:109]
	v_mfma_f32_16x16x32_bf16 v[94:97], v[150:153], v[208:211], v[94:97]
	v_mfma_f32_16x16x32_bf16 v[90:93], v[158:161], v[208:211], v[90:93]
	v_mfma_f32_16x16x32_bf16 v[78:81], v[150:153], v[216:219], v[78:81]
	v_mfma_f32_16x16x32_bf16 v[74:77], v[158:161], v[216:219], v[74:77]
	s_setprio 0
	s_setprio 1
	v_mfma_f32_16x16x32_bf16 v[118:121], v[162:165], v[178:181], v[118:121]
	v_mfma_f32_16x16x32_bf16 v[114:117], v[170:173], v[178:181], v[114:117]
	v_mfma_f32_16x16x32_bf16 v[102:105], v[162:165], v[196:199], v[102:105]
	v_mfma_f32_16x16x32_bf16 v[98:101], v[170:173], v[196:199], v[98:101]
	v_mfma_f32_16x16x32_bf16 v[86:89], v[162:165], v[204:207], v[86:89]
	v_mfma_f32_16x16x32_bf16 v[82:85], v[170:173], v[204:207], v[82:85]
	v_mfma_f32_16x16x32_bf16 v[70:73], v[162:165], v[212:215], v[70:73]
	v_mfma_f32_16x16x32_bf16 v[66:69], v[170:173], v[212:215], v[66:69]
	v_mfma_f32_16x16x32_bf16 v[118:121], v[166:169], v[182:185], v[118:121]
	v_mfma_f32_16x16x32_bf16 v[114:117], v[174:177], v[182:185], v[114:117]
	v_mfma_f32_16x16x32_bf16 v[102:105], v[166:169], v[200:203], v[102:105]
	v_mfma_f32_16x16x32_bf16 v[98:101], v[174:177], v[200:203], v[98:101]
	v_mfma_f32_16x16x32_bf16 v[86:89], v[166:169], v[208:211], v[86:89]
	v_mfma_f32_16x16x32_bf16 v[82:85], v[174:177], v[208:211], v[82:85]
	v_mfma_f32_16x16x32_bf16 v[70:73], v[166:169], v[216:219], v[70:73]
	v_mfma_f32_16x16x32_bf16 v[66:69], v[174:177], v[216:219], v[66:69]
	s_setprio 0
	s_barrier
	s_add_i32 s14, s14, s12
	v_lshl_add_u64 v[222:223], v[220:221], 0, s[92:93]
	s_mov_b32 m0, s14
	global_load_lds_dwordx4 v[222:223], off
	v_lshl_add_u64 v[222:223], v[220:221], 0, s[4:5]
	s_add_i32 m0, s14, 0x2000
	s_add_i32 s14, s15, s12
	global_load_lds_dwordx4 v[222:223], off
	v_lshl_add_u64 v[222:223], v[220:221], 0, s[6:7]
	s_mov_b32 m0, s14
	v_lshl_add_u64 v[220:221], v[220:221], 0, s[8:9]
	global_load_lds_dwordx4 v[222:223], off
	s_add_i32 m0, s14, 0x2000
	s_nop 0
	global_load_lds_dwordx4 v[220:221], off
	v_lshl_add_u64 v[220:221], v[192:193], 0, s[92:93]
	s_mov_b32 m0, s76
	v_lshl_add_u64 v[192:193], v[192:193], 0, s[4:5]
	global_load_lds_dwordx4 v[220:221], off
	s_mov_b32 m0, s77
	s_nop 0
	global_load_lds_dwordx4 v[192:193], off
	ds_read_b128 v[178:181], v144 offset:53248
	ds_read_b128 v[182:185], v144 offset:54272
	ds_read_b128 v[196:199], v144 offset:55296
	ds_read_b128 v[200:203], v144 offset:56320
	ds_read_b128 v[204:207], v144 offset:57344
	ds_read_b128 v[208:211], v144 offset:58368
	ds_read_b128 v[212:215], v144 offset:59392
	ds_read_b128 v[216:219], v144 offset:60416
	s_waitcnt vmcnt(8)
	s_waitcnt lgkmcnt(0)
	s_barrier
	s_setprio 1
	s_waitcnt lgkmcnt(0)
	v_mfma_f32_16x16x32_bf16 v[62:65], v[146:149], v[178:181], v[62:65]
	v_mfma_f32_16x16x32_bf16 v[58:61], v[154:157], v[178:181], v[58:61]
	v_mfma_f32_16x16x32_bf16 v[46:49], v[146:149], v[196:199], v[46:49]
	v_mfma_f32_16x16x32_bf16 v[42:45], v[154:157], v[196:199], v[42:45]
	v_mfma_f32_16x16x32_bf16 v[30:33], v[146:149], v[204:207], v[30:33]
	v_mfma_f32_16x16x32_bf16 v[26:29], v[154:157], v[204:207], v[26:29]
	v_mfma_f32_16x16x32_bf16 v[14:17], v[146:149], v[212:215], v[14:17]
	v_mfma_f32_16x16x32_bf16 v[10:13], v[154:157], v[212:215], v[10:13]
	v_mfma_f32_16x16x32_bf16 v[62:65], v[150:153], v[182:185], v[62:65]
	v_mfma_f32_16x16x32_bf16 v[58:61], v[158:161], v[182:185], v[58:61]
	v_mfma_f32_16x16x32_bf16 v[46:49], v[150:153], v[200:203], v[46:49]
	v_mfma_f32_16x16x32_bf16 v[42:45], v[158:161], v[200:203], v[42:45]
	v_mfma_f32_16x16x32_bf16 v[30:33], v[150:153], v[208:211], v[30:33]
	v_mfma_f32_16x16x32_bf16 v[26:29], v[158:161], v[208:211], v[26:29]
	v_mfma_f32_16x16x32_bf16 v[14:17], v[150:153], v[216:219], v[14:17]
	v_mfma_f32_16x16x32_bf16 v[10:13], v[158:161], v[216:219], v[10:13]
	s_setprio 0
	s_setprio 1
	v_mfma_f32_16x16x32_bf16 v[54:57], v[162:165], v[178:181], v[54:57]
	v_mfma_f32_16x16x32_bf16 v[50:53], v[170:173], v[178:181], v[50:53]
	v_mfma_f32_16x16x32_bf16 v[38:41], v[162:165], v[196:199], v[38:41]
	v_mfma_f32_16x16x32_bf16 v[34:37], v[170:173], v[196:199], v[34:37]
	v_mfma_f32_16x16x32_bf16 v[22:25], v[162:165], v[204:207], v[22:25]
	v_mfma_f32_16x16x32_bf16 v[18:21], v[170:173], v[204:207], v[18:21]
	v_mfma_f32_16x16x32_bf16 v[6:9], v[162:165], v[212:215], v[6:9]
	v_mfma_f32_16x16x32_bf16 v[2:5], v[170:173], v[212:215], v[2:5]
	v_mfma_f32_16x16x32_bf16 v[54:57], v[166:169], v[182:185], v[54:57]
	v_mfma_f32_16x16x32_bf16 v[50:53], v[174:177], v[182:185], v[50:53]
	v_mfma_f32_16x16x32_bf16 v[38:41], v[166:169], v[200:203], v[38:41]
	v_mfma_f32_16x16x32_bf16 v[34:37], v[174:177], v[200:203], v[34:37]
	v_mfma_f32_16x16x32_bf16 v[22:25], v[166:169], v[208:211], v[22:25]
	v_mfma_f32_16x16x32_bf16 v[18:21], v[174:177], v[208:211], v[18:21]
	v_mfma_f32_16x16x32_bf16 v[6:9], v[166:169], v[216:219], v[6:9]
	v_mfma_f32_16x16x32_bf16 v[2:5], v[174:177], v[216:219], v[2:5]
	s_setprio 0
	s_barrier
	s_add_i32 s25, s25, 2
	s_add_u32 s42, s42, 0x100
	s_addc_u32 s43, s43, 0
.LBB0_391:
	s_add_u32 s14, s40, s42
	s_addc_u32 s15, s41, s43
	s_add_u32 s34, s14, 0x100
	s_addc_u32 s35, s15, 0
	s_add_u32 s44, s1, s42
	s_addc_u32 s45, s24, s43
	s_cmpk_eq_i32 s42, 0x700
	s_cselect_b64 vcc, -1, 0
	s_and_b64 s[14:15], vcc, exec
	s_cselect_b32 s15, s55, s35
	s_cselect_b32 s14, s54, s34
	s_cselect_b32 s35, s69, s45
	s_cselect_b32 s34, s68, s44
	s_add_i32 s44, 0, 0x11000
	v_add_u32_e32 v145, s44, v1
	s_add_i32 s45, 0, 0x15000
	ds_read_b128 v[146:149], v145
	ds_read_b128 v[150:153], v145 offset:1024
	ds_read_b128 v[154:157], v145 offset:2048
	ds_read_b128 v[158:161], v145 offset:3072
	v_add_u32_e32 v145, s45, v1
	ds_read_b128 v[162:165], v145
	ds_read_b128 v[166:169], v145 offset:1024
	ds_read_b128 v[170:173], v145 offset:2048
	ds_read_b128 v[174:177], v145 offset:3072
	v_cndmask_b32_e32 v193, v131, v141, vcc
	v_cndmask_b32_e32 v192, v130, v140, vcc
	v_lshl_add_u64 v[220:221], v[142:143], 0, s[42:43]
	v_lshl_add_u64 v[222:223], v[220:221], 0, s[6:7]
	s_add_i32 m0, s28, 0xd000
	ds_read_b128 v[178:181], v144 offset:4096
	ds_read_b128 v[182:185], v144 offset:5120
	ds_read_b128 v[196:199], v144 offset:6144
	ds_read_b128 v[200:203], v144 offset:7168
	ds_read_b128 v[204:207], v144 offset:8192
	ds_read_b128 v[208:211], v144 offset:9216
	ds_read_b128 v[212:215], v144 offset:10240
	ds_read_b128 v[216:219], v144 offset:11264
	global_load_lds_dwordx4 v[222:223], off
	v_lshl_add_u64 v[220:221], v[220:221], 0, s[8:9]
	s_add_i32 m0, s28, 0xf000
	s_nop 0
	global_load_lds_dwordx4 v[220:221], off
	s_waitcnt vmcnt(8)
	s_waitcnt lgkmcnt(0)
	s_barrier
	s_setprio 1
	s_waitcnt lgkmcnt(0)
	v_mfma_f32_16x16x32_bf16 v[126:129], v[146:149], v[178:181], v[126:129]
	v_mfma_f32_16x16x32_bf16 v[122:125], v[154:157], v[178:181], v[122:125]
	v_mfma_f32_16x16x32_bf16 v[110:113], v[146:149], v[196:199], v[110:113]
	v_mfma_f32_16x16x32_bf16 v[106:109], v[154:157], v[196:199], v[106:109]
	v_mfma_f32_16x16x32_bf16 v[94:97], v[146:149], v[204:207], v[94:97]
	v_mfma_f32_16x16x32_bf16 v[90:93], v[154:157], v[204:207], v[90:93]
	v_mfma_f32_16x16x32_bf16 v[78:81], v[146:149], v[212:215], v[78:81]
	v_mfma_f32_16x16x32_bf16 v[74:77], v[154:157], v[212:215], v[74:77]
	v_mfma_f32_16x16x32_bf16 v[126:129], v[150:153], v[182:185], v[126:129]
	v_mfma_f32_16x16x32_bf16 v[122:125], v[158:161], v[182:185], v[122:125]
	v_mfma_f32_16x16x32_bf16 v[110:113], v[150:153], v[200:203], v[110:113]
	v_mfma_f32_16x16x32_bf16 v[106:109], v[158:161], v[200:203], v[106:109]
	v_mfma_f32_16x16x32_bf16 v[94:97], v[150:153], v[208:211], v[94:97]
	v_mfma_f32_16x16x32_bf16 v[90:93], v[158:161], v[208:211], v[90:93]
	v_mfma_f32_16x16x32_bf16 v[78:81], v[150:153], v[216:219], v[78:81]
	v_mfma_f32_16x16x32_bf16 v[74:77], v[158:161], v[216:219], v[74:77]
	s_setprio 0
	s_setprio 1
	v_mfma_f32_16x16x32_bf16 v[118:121], v[162:165], v[178:181], v[118:121]
	v_mfma_f32_16x16x32_bf16 v[114:117], v[170:173], v[178:181], v[114:117]
	v_mfma_f32_16x16x32_bf16 v[102:105], v[162:165], v[196:199], v[102:105]
	v_mfma_f32_16x16x32_bf16 v[98:101], v[170:173], v[196:199], v[98:101]
	v_mfma_f32_16x16x32_bf16 v[86:89], v[162:165], v[204:207], v[86:89]
	v_mfma_f32_16x16x32_bf16 v[82:85], v[170:173], v[204:207], v[82:85]
	v_mfma_f32_16x16x32_bf16 v[70:73], v[162:165], v[212:215], v[70:73]
	v_mfma_f32_16x16x32_bf16 v[66:69], v[170:173], v[212:215], v[66:69]
	v_mfma_f32_16x16x32_bf16 v[118:121], v[166:169], v[182:185], v[118:121]
	v_mfma_f32_16x16x32_bf16 v[114:117], v[174:177], v[182:185], v[114:117]
	v_mfma_f32_16x16x32_bf16 v[102:105], v[166:169], v[200:203], v[102:105]
	v_mfma_f32_16x16x32_bf16 v[98:101], v[174:177], v[200:203], v[98:101]
	v_mfma_f32_16x16x32_bf16 v[86:89], v[166:169], v[208:211], v[86:89]
	v_mfma_f32_16x16x32_bf16 v[82:85], v[174:177], v[208:211], v[82:85]
	v_mfma_f32_16x16x32_bf16 v[70:73], v[166:169], v[216:219], v[70:73]
	v_mfma_f32_16x16x32_bf16 v[66:69], v[174:177], v[216:219], v[66:69]
	s_setprio 0
	s_barrier
	s_add_i32 s44, s44, s12
	v_lshl_add_u64 v[220:221], s[34:35], 0, v[186:187]
	s_mov_b32 m0, s44
	global_load_lds_dwordx4 v186, s[34:35]
	v_lshl_add_u64 v[222:223], v[220:221], 0, s[82:83]
	s_add_i32 m0, s44, 0x2000
	s_add_i32 s34, s45, s12
	global_load_lds_dwordx4 v[222:223], off
	v_lshl_add_u64 v[222:223], v[220:221], 0, s[64:65]
	s_mov_b32 m0, s34
	v_lshl_add_u64 v[192:193], s[14:15], 0, v[192:193]
	global_load_lds_dwordx4 v[222:223], off
	v_lshl_add_u64 v[222:223], v[220:221], 0, s[86:87]
	s_add_i32 m0, s34, 0x2000
	s_nop 0
	global_load_lds_dwordx4 v[222:223], off
	s_mov_b32 m0, s29
	v_lshl_add_u64 v[222:223], v[192:193], 0, s[82:83]
	global_load_lds_dwordx4 v[192:193], off
	s_mov_b32 m0, s47
	s_nop 0
	global_load_lds_dwordx4 v[222:223], off
	ds_read_b128 v[178:181], v144 offset:20480
	ds_read_b128 v[182:185], v144 offset:21504
	ds_read_b128 v[196:199], v144 offset:22528
	ds_read_b128 v[200:203], v144 offset:23552
	ds_read_b128 v[204:207], v144 offset:24576
	ds_read_b128 v[208:211], v144 offset:25600
	ds_read_b128 v[212:215], v144 offset:26624
	ds_read_b128 v[216:219], v144 offset:27648
	s_waitcnt vmcnt(8)
	s_waitcnt lgkmcnt(0)
	s_barrier
	s_setprio 1
	s_waitcnt lgkmcnt(0)
	v_mfma_f32_16x16x32_bf16 v[62:65], v[146:149], v[178:181], v[62:65]
	v_mfma_f32_16x16x32_bf16 v[58:61], v[154:157], v[178:181], v[58:61]
	v_mfma_f32_16x16x32_bf16 v[46:49], v[146:149], v[196:199], v[46:49]
	v_mfma_f32_16x16x32_bf16 v[42:45], v[154:157], v[196:199], v[42:45]
	v_mfma_f32_16x16x32_bf16 v[30:33], v[146:149], v[204:207], v[30:33]
	v_mfma_f32_16x16x32_bf16 v[26:29], v[154:157], v[204:207], v[26:29]
	v_mfma_f32_16x16x32_bf16 v[14:17], v[146:149], v[212:215], v[14:17]
	v_mfma_f32_16x16x32_bf16 v[10:13], v[154:157], v[212:215], v[10:13]
	v_mfma_f32_16x16x32_bf16 v[62:65], v[150:153], v[182:185], v[62:65]
	v_mfma_f32_16x16x32_bf16 v[58:61], v[158:161], v[182:185], v[58:61]
	v_mfma_f32_16x16x32_bf16 v[46:49], v[150:153], v[200:203], v[46:49]
	v_mfma_f32_16x16x32_bf16 v[42:45], v[158:161], v[200:203], v[42:45]
	v_mfma_f32_16x16x32_bf16 v[30:33], v[150:153], v[208:211], v[30:33]
	v_mfma_f32_16x16x32_bf16 v[26:29], v[158:161], v[208:211], v[26:29]
	v_mfma_f32_16x16x32_bf16 v[14:17], v[150:153], v[216:219], v[14:17]
	v_mfma_f32_16x16x32_bf16 v[10:13], v[158:161], v[216:219], v[10:13]
	s_setprio 0
	s_setprio 1
	v_mfma_f32_16x16x32_bf16 v[54:57], v[162:165], v[178:181], v[54:57]
	v_mfma_f32_16x16x32_bf16 v[50:53], v[170:173], v[178:181], v[50:53]
	v_mfma_f32_16x16x32_bf16 v[38:41], v[162:165], v[196:199], v[38:41]
	v_mfma_f32_16x16x32_bf16 v[34:37], v[170:173], v[196:199], v[34:37]
	v_mfma_f32_16x16x32_bf16 v[22:25], v[162:165], v[204:207], v[22:25]
	v_mfma_f32_16x16x32_bf16 v[18:21], v[170:173], v[204:207], v[18:21]
	v_mfma_f32_16x16x32_bf16 v[6:9], v[162:165], v[212:215], v[6:9]
	v_mfma_f32_16x16x32_bf16 v[2:5], v[170:173], v[212:215], v[2:5]
	v_mfma_f32_16x16x32_bf16 v[54:57], v[166:169], v[182:185], v[54:57]
	v_mfma_f32_16x16x32_bf16 v[50:53], v[174:177], v[182:185], v[50:53]
	v_mfma_f32_16x16x32_bf16 v[38:41], v[166:169], v[200:203], v[38:41]
	v_mfma_f32_16x16x32_bf16 v[34:37], v[174:177], v[200:203], v[34:37]
	v_mfma_f32_16x16x32_bf16 v[22:25], v[166:169], v[208:211], v[22:25]
	v_mfma_f32_16x16x32_bf16 v[18:21], v[174:177], v[208:211], v[18:21]
	v_mfma_f32_16x16x32_bf16 v[6:9], v[166:169], v[216:219], v[6:9]
	v_mfma_f32_16x16x32_bf16 v[2:5], v[174:177], v[216:219], v[2:5]
	s_setprio 0
	s_barrier
	s_add_i32 s14, 0, 0x19000
	v_add_u32_e32 v145, s14, v1
	s_add_i32 s15, 0, 0x1d000
	ds_read_b128 v[146:149], v145
	ds_read_b128 v[150:153], v145 offset:1024
	ds_read_b128 v[154:157], v145 offset:2048
	ds_read_b128 v[158:161], v145 offset:3072
	v_add_u32_e32 v145, s15, v1
	ds_read_b128 v[162:165], v145
	ds_read_b128 v[166:169], v145 offset:1024
	ds_read_b128 v[170:173], v145 offset:2048
	ds_read_b128 v[174:177], v145 offset:3072
	s_mov_b32 m0, s60
	v_lshl_add_u64 v[222:223], v[192:193], 0, s[64:65]
	ds_read_b128 v[178:181], v144 offset:36864
	ds_read_b128 v[182:185], v144 offset:37888
	ds_read_b128 v[196:199], v144 offset:38912
	ds_read_b128 v[200:203], v144 offset:39936
	ds_read_b128 v[204:207], v144 offset:40960
	ds_read_b128 v[208:211], v144 offset:41984
	ds_read_b128 v[212:215], v144 offset:43008
	ds_read_b128 v[216:219], v144 offset:44032
	global_load_lds_dwordx4 v[222:223], off
	v_lshl_add_u64 v[222:223], v[192:193], 0, s[86:87]
	s_mov_b32 m0, s61
	s_nop 0
	global_load_lds_dwordx4 v[222:223], off
	s_waitcnt vmcnt(8)
	s_waitcnt lgkmcnt(0)
	s_barrier
	s_setprio 1
	s_waitcnt lgkmcnt(0)
	v_mfma_f32_16x16x32_bf16 v[126:129], v[146:149], v[178:181], v[126:129]
	v_mfma_f32_16x16x32_bf16 v[122:125], v[154:157], v[178:181], v[122:125]
	v_mfma_f32_16x16x32_bf16 v[110:113], v[146:149], v[196:199], v[110:113]
	v_mfma_f32_16x16x32_bf16 v[106:109], v[154:157], v[196:199], v[106:109]
	v_mfma_f32_16x16x32_bf16 v[94:97], v[146:149], v[204:207], v[94:97]
	v_mfma_f32_16x16x32_bf16 v[90:93], v[154:157], v[204:207], v[90:93]
	v_mfma_f32_16x16x32_bf16 v[78:81], v[146:149], v[212:215], v[78:81]
	v_mfma_f32_16x16x32_bf16 v[74:77], v[154:157], v[212:215], v[74:77]
	v_mfma_f32_16x16x32_bf16 v[126:129], v[150:153], v[182:185], v[126:129]
	v_mfma_f32_16x16x32_bf16 v[122:125], v[158:161], v[182:185], v[122:125]
	v_mfma_f32_16x16x32_bf16 v[110:113], v[150:153], v[200:203], v[110:113]
	v_mfma_f32_16x16x32_bf16 v[106:109], v[158:161], v[200:203], v[106:109]
	v_mfma_f32_16x16x32_bf16 v[94:97], v[150:153], v[208:211], v[94:97]
	v_mfma_f32_16x16x32_bf16 v[90:93], v[158:161], v[208:211], v[90:93]
	v_mfma_f32_16x16x32_bf16 v[78:81], v[150:153], v[216:219], v[78:81]
	v_mfma_f32_16x16x32_bf16 v[74:77], v[158:161], v[216:219], v[74:77]
	s_setprio 0
	s_setprio 1
	v_mfma_f32_16x16x32_bf16 v[118:121], v[162:165], v[178:181], v[118:121]
	v_mfma_f32_16x16x32_bf16 v[114:117], v[170:173], v[178:181], v[114:117]
	v_mfma_f32_16x16x32_bf16 v[102:105], v[162:165], v[196:199], v[102:105]
	v_mfma_f32_16x16x32_bf16 v[98:101], v[170:173], v[196:199], v[98:101]
	v_mfma_f32_16x16x32_bf16 v[86:89], v[162:165], v[204:207], v[86:89]
	v_mfma_f32_16x16x32_bf16 v[82:85], v[170:173], v[204:207], v[82:85]
	v_mfma_f32_16x16x32_bf16 v[70:73], v[162:165], v[212:215], v[70:73]
	v_mfma_f32_16x16x32_bf16 v[66:69], v[170:173], v[212:215], v[66:69]
	v_mfma_f32_16x16x32_bf16 v[118:121], v[166:169], v[182:185], v[118:121]
	v_mfma_f32_16x16x32_bf16 v[114:117], v[174:177], v[182:185], v[114:117]
	v_mfma_f32_16x16x32_bf16 v[102:105], v[166:169], v[200:203], v[102:105]
	v_mfma_f32_16x16x32_bf16 v[98:101], v[174:177], v[200:203], v[98:101]
	v_mfma_f32_16x16x32_bf16 v[86:89], v[166:169], v[208:211], v[86:89]
	v_mfma_f32_16x16x32_bf16 v[82:85], v[174:177], v[208:211], v[82:85]
	v_mfma_f32_16x16x32_bf16 v[70:73], v[166:169], v[216:219], v[70:73]
	v_mfma_f32_16x16x32_bf16 v[66:69], v[174:177], v[216:219], v[66:69]
	s_setprio 0
	s_barrier
	s_add_i32 s14, s14, s12
	v_lshl_add_u64 v[222:223], v[220:221], 0, s[92:93]
	s_mov_b32 m0, s14
	global_load_lds_dwordx4 v[222:223], off
	v_lshl_add_u64 v[222:223], v[220:221], 0, s[4:5]
	s_add_i32 m0, s14, 0x2000
	s_add_i32 s14, s15, s12
	global_load_lds_dwordx4 v[222:223], off
	v_lshl_add_u64 v[222:223], v[220:221], 0, s[6:7]
	s_mov_b32 m0, s14
	v_lshl_add_u64 v[220:221], v[220:221], 0, s[8:9]
	global_load_lds_dwordx4 v[222:223], off
	s_add_i32 m0, s14, 0x2000
	s_nop 0
	global_load_lds_dwordx4 v[220:221], off
	v_lshl_add_u64 v[220:221], v[192:193], 0, s[92:93]
	s_mov_b32 m0, s76
	v_lshl_add_u64 v[192:193], v[192:193], 0, s[4:5]
	global_load_lds_dwordx4 v[220:221], off
	s_mov_b32 m0, s77
	s_nop 0
	global_load_lds_dwordx4 v[192:193], off
	ds_read_b128 v[178:181], v144 offset:53248
	ds_read_b128 v[182:185], v144 offset:54272
	ds_read_b128 v[196:199], v144 offset:55296
	ds_read_b128 v[200:203], v144 offset:56320
	ds_read_b128 v[204:207], v144 offset:57344
	ds_read_b128 v[208:211], v144 offset:58368
	ds_read_b128 v[212:215], v144 offset:59392
	ds_read_b128 v[216:219], v144 offset:60416
	s_waitcnt vmcnt(8)
	s_waitcnt lgkmcnt(0)
	s_barrier
	s_setprio 1
	s_waitcnt lgkmcnt(0)
	v_mfma_f32_16x16x32_bf16 v[62:65], v[146:149], v[178:181], v[62:65]
	v_mfma_f32_16x16x32_bf16 v[58:61], v[154:157], v[178:181], v[58:61]
	v_mfma_f32_16x16x32_bf16 v[46:49], v[146:149], v[196:199], v[46:49]
	v_mfma_f32_16x16x32_bf16 v[42:45], v[154:157], v[196:199], v[42:45]
	v_mfma_f32_16x16x32_bf16 v[30:33], v[146:149], v[204:207], v[30:33]
	v_mfma_f32_16x16x32_bf16 v[26:29], v[154:157], v[204:207], v[26:29]
	v_mfma_f32_16x16x32_bf16 v[14:17], v[146:149], v[212:215], v[14:17]
	v_mfma_f32_16x16x32_bf16 v[10:13], v[154:157], v[212:215], v[10:13]
	v_mfma_f32_16x16x32_bf16 v[62:65], v[150:153], v[182:185], v[62:65]
	v_mfma_f32_16x16x32_bf16 v[58:61], v[158:161], v[182:185], v[58:61]
	v_mfma_f32_16x16x32_bf16 v[46:49], v[150:153], v[200:203], v[46:49]
	v_mfma_f32_16x16x32_bf16 v[42:45], v[158:161], v[200:203], v[42:45]
	v_mfma_f32_16x16x32_bf16 v[30:33], v[150:153], v[208:211], v[30:33]
	v_mfma_f32_16x16x32_bf16 v[26:29], v[158:161], v[208:211], v[26:29]
	v_mfma_f32_16x16x32_bf16 v[14:17], v[150:153], v[216:219], v[14:17]
	v_mfma_f32_16x16x32_bf16 v[10:13], v[158:161], v[216:219], v[10:13]
	s_setprio 0
	s_setprio 1
	v_mfma_f32_16x16x32_bf16 v[54:57], v[162:165], v[178:181], v[54:57]
	v_mfma_f32_16x16x32_bf16 v[50:53], v[170:173], v[178:181], v[50:53]
	v_mfma_f32_16x16x32_bf16 v[38:41], v[162:165], v[196:199], v[38:41]
	v_mfma_f32_16x16x32_bf16 v[34:37], v[170:173], v[196:199], v[34:37]
	v_mfma_f32_16x16x32_bf16 v[22:25], v[162:165], v[204:207], v[22:25]
	v_mfma_f32_16x16x32_bf16 v[18:21], v[170:173], v[204:207], v[18:21]
	v_mfma_f32_16x16x32_bf16 v[6:9], v[162:165], v[212:215], v[6:9]
	v_mfma_f32_16x16x32_bf16 v[2:5], v[170:173], v[212:215], v[2:5]
	v_mfma_f32_16x16x32_bf16 v[54:57], v[166:169], v[182:185], v[54:57]
	v_mfma_f32_16x16x32_bf16 v[50:53], v[174:177], v[182:185], v[50:53]
	v_mfma_f32_16x16x32_bf16 v[38:41], v[166:169], v[200:203], v[38:41]
	v_mfma_f32_16x16x32_bf16 v[34:37], v[174:177], v[200:203], v[34:37]
	v_mfma_f32_16x16x32_bf16 v[22:25], v[166:169], v[208:211], v[22:25]
	v_mfma_f32_16x16x32_bf16 v[18:21], v[174:177], v[208:211], v[18:21]
	v_mfma_f32_16x16x32_bf16 v[6:9], v[166:169], v[216:219], v[6:9]
	v_mfma_f32_16x16x32_bf16 v[2:5], v[174:177], v[216:219], v[2:5]
	s_setprio 0
	s_barrier
	s_add_i32 s25, s25, 2
	s_add_u32 s42, s42, 0x100
	s_addc_u32 s43, s43, 0
	s_cmp_gt_u32 s25, 13
	s_cbranch_scc0 .LBB0_391
	s_and_b64 vcc, exec, s[50:51]
	s_cbranch_vccz .LBB0_394
	s_barrier

.LBB0_591:
	s_add_u32 s28, s42, s41
	s_addc_u32 s29, s43, 0
	s_add_u32 s49, s28, 0x100
	s_addc_u32 s85, s29, 0
	s_and_b64 s[24:25], s[14:15], exec
	s_cselect_b32 s24, s50, s49
	s_cselect_b32 s25, s51, s85
	s_add_u32 s41, s44, s41
	s_addc_u32 s49, s45, 0
	s_add_u32 s41, s41, 0x100
	s_addc_u32 s49, s49, 0
	s_add_i32 s85, 0, 0x11000
	v_add_u32_e32 v71, s85, v1
	ds_read_b128 v[72:75], v71
	ds_read_b128 v[76:79], v71 offset:1024
	ds_read_b128 v[80:83], v71 offset:2048
	ds_read_b128 v[84:87], v71 offset:3072
	s_and_b64 s[14:15], s[14:15], exec
	s_cselect_b32 s14, s52, s41
	s_cselect_b32 s15, s53, s49
	s_add_i32 s49, s85, s16
	s_add_i32 s85, 0, 0x19000
	s_add_i32 s41, s17, 0xf000
	s_add_i32 s90, s85, s16
	s_add_i32 m0, s17, 0xd000
	s_add_i32 s88, s49, 0x2000
	s_add_i32 s91, s90, 0x2000
	v_lshl_add_u64 v[120:121], s[28:29], 0, v[66:67]
	v_lshl_add_u64 v[122:123], v[120:121], 0, s[94:95]
	ds_read_b128 v[88:91], v70 offset:4096
	ds_read_b128 v[92:95], v70 offset:5120
	ds_read_b128 v[96:99], v70 offset:6144
	ds_read_b128 v[100:103], v70 offset:7168
	ds_read_b128 v[104:107], v70 offset:8192
	ds_read_b128 v[108:111], v70 offset:9216
	ds_read_b128 v[112:115], v70 offset:10240
	ds_read_b128 v[116:119], v70 offset:11264
	global_load_lds_dwordx4 v[122:123], off
	v_lshl_add_u64 v[120:121], v[120:121], 0, s[66:67]
	s_mov_b32 m0, s41
	s_nop 0
	global_load_lds_dwordx4 v[120:121], off
	s_waitcnt vmcnt(8)
	s_waitcnt lgkmcnt(0)
	s_barrier
	s_setprio 1
	s_waitcnt lgkmcnt(0)
	v_mfma_f32_16x16x32_bf16 v[62:65], v[72:75], v[88:91], v[62:65]
	v_mfma_f32_16x16x32_bf16 v[58:61], v[80:83], v[88:91], v[58:61]
	v_mfma_f32_16x16x32_bf16 v[54:57], v[72:75], v[96:99], v[54:57]
	v_mfma_f32_16x16x32_bf16 v[50:53], v[80:83], v[96:99], v[50:53]
	v_mfma_f32_16x16x32_bf16 v[46:49], v[72:75], v[104:107], v[46:49]
	v_mfma_f32_16x16x32_bf16 v[42:45], v[80:83], v[104:107], v[42:45]
	v_mfma_f32_16x16x32_bf16 v[38:41], v[72:75], v[112:115], v[38:41]
	v_mfma_f32_16x16x32_bf16 v[34:37], v[80:83], v[112:115], v[34:37]
	v_mfma_f32_16x16x32_bf16 v[62:65], v[76:79], v[92:95], v[62:65]
	v_mfma_f32_16x16x32_bf16 v[58:61], v[84:87], v[92:95], v[58:61]
	v_mfma_f32_16x16x32_bf16 v[54:57], v[76:79], v[100:103], v[54:57]
	v_mfma_f32_16x16x32_bf16 v[50:53], v[84:87], v[100:103], v[50:53]
	v_mfma_f32_16x16x32_bf16 v[46:49], v[76:79], v[108:111], v[46:49]
	v_mfma_f32_16x16x32_bf16 v[42:45], v[84:87], v[108:111], v[42:45]
	v_mfma_f32_16x16x32_bf16 v[38:41], v[76:79], v[116:119], v[38:41]
	v_mfma_f32_16x16x32_bf16 v[34:37], v[84:87], v[116:119], v[34:37]
	s_setprio 0
	s_setprio 1
	s_setprio 0
	s_barrier
	s_mov_b32 m0, s49
	v_lshl_add_u64 v[120:121], s[14:15], 0, v[186:187]
	global_load_lds_dwordx4 v186, s[14:15]
	v_lshl_add_u64 v[122:123], v[120:121], 0, s[0:1]
	s_mov_b32 m0, s88
	s_nop 0
	global_load_lds_dwordx4 v[122:123], off
	v_lshl_add_u64 v[122:123], v[120:121], 0, s[2:3]
	s_mov_b32 m0, s33
	s_nop 0
	global_load_lds_dwordx4 v[122:123], off
	v_lshl_add_u64 v[122:123], v[120:121], 0, s[18:19]
	s_mov_b32 m0, s34
	s_nop 0
	global_load_lds_dwordx4 v[122:123], off
	v_lshl_add_u64 v[122:123], s[24:25], 0, v[66:67]
	s_mov_b32 m0, s35
	v_lshl_add_u64 v[124:125], v[122:123], 0, s[20:21]
	global_load_lds_dwordx4 v[122:123], off
	s_mov_b32 m0, s59
	s_nop 0
	global_load_lds_dwordx4 v[124:125], off
	ds_read_b128 v[88:91], v70 offset:20480
	ds_read_b128 v[92:95], v70 offset:21504
	ds_read_b128 v[96:99], v70 offset:22528
	ds_read_b128 v[100:103], v70 offset:23552
	ds_read_b128 v[104:107], v70 offset:24576
	ds_read_b128 v[108:111], v70 offset:25600
	ds_read_b128 v[112:115], v70 offset:26624
	ds_read_b128 v[116:119], v70 offset:27648
	s_waitcnt vmcnt(8)
	s_waitcnt lgkmcnt(0)
	s_barrier
	s_setprio 1
	s_waitcnt lgkmcnt(0)
	v_mfma_f32_16x16x32_bf16 v[30:33], v[72:75], v[88:91], v[30:33]
	v_mfma_f32_16x16x32_bf16 v[26:29], v[80:83], v[88:91], v[26:29]
	v_mfma_f32_16x16x32_bf16 v[22:25], v[72:75], v[96:99], v[22:25]
	v_mfma_f32_16x16x32_bf16 v[18:21], v[80:83], v[96:99], v[18:21]
	v_mfma_f32_16x16x32_bf16 v[14:17], v[72:75], v[104:107], v[14:17]
	v_mfma_f32_16x16x32_bf16 v[10:13], v[80:83], v[104:107], v[10:13]
	v_mfma_f32_16x16x32_bf16 v[6:9], v[72:75], v[112:115], v[6:9]
	v_mfma_f32_16x16x32_bf16 v[2:5], v[80:83], v[112:115], v[2:5]
	v_mfma_f32_16x16x32_bf16 v[30:33], v[76:79], v[92:95], v[30:33]
	v_mfma_f32_16x16x32_bf16 v[26:29], v[84:87], v[92:95], v[26:29]
	v_mfma_f32_16x16x32_bf16 v[22:25], v[76:79], v[100:103], v[22:25]
	v_mfma_f32_16x16x32_bf16 v[18:21], v[84:87], v[100:103], v[18:21]
	v_mfma_f32_16x16x32_bf16 v[14:17], v[76:79], v[108:111], v[14:17]
	v_mfma_f32_16x16x32_bf16 v[10:13], v[84:87], v[108:111], v[10:13]
	v_mfma_f32_16x16x32_bf16 v[6:9], v[76:79], v[116:119], v[6:9]
	v_mfma_f32_16x16x32_bf16 v[2:5], v[84:87], v[116:119], v[2:5]
	s_setprio 0
	s_setprio 1
	s_setprio 0
	s_barrier
	v_add_u32_e32 v71, s85, v1
	ds_read_b128 v[72:75], v71
	ds_read_b128 v[76:79], v71 offset:1024
	ds_read_b128 v[80:83], v71 offset:2048
	ds_read_b128 v[84:87], v71 offset:3072
	s_mov_b32 m0, s60
	v_lshl_add_u64 v[124:125], v[122:123], 0, s[18:19]
	ds_read_b128 v[88:91], v70 offset:36864
	ds_read_b128 v[92:95], v70 offset:37888
	ds_read_b128 v[96:99], v70 offset:38912
	ds_read_b128 v[100:103], v70 offset:39936
	ds_read_b128 v[104:107], v70 offset:40960
	ds_read_b128 v[108:111], v70 offset:41984
	ds_read_b128 v[112:115], v70 offset:43008
	ds_read_b128 v[116:119], v70 offset:44032
	global_load_lds_dwordx4 v[124:125], off
	v_lshl_add_u64 v[124:125], v[122:123], 0, s[26:27]
	s_mov_b32 m0, s61
	s_nop 0
	global_load_lds_dwordx4 v[124:125], off
	s_waitcnt vmcnt(8)
	s_waitcnt lgkmcnt(0)
	s_barrier
	s_setprio 1
	s_waitcnt lgkmcnt(0)
	v_mfma_f32_16x16x32_bf16 v[62:65], v[72:75], v[88:91], v[62:65]
	v_mfma_f32_16x16x32_bf16 v[58:61], v[80:83], v[88:91], v[58:61]
	v_mfma_f32_16x16x32_bf16 v[54:57], v[72:75], v[96:99], v[54:57]
	v_mfma_f32_16x16x32_bf16 v[50:53], v[80:83], v[96:99], v[50:53]
	v_mfma_f32_16x16x32_bf16 v[46:49], v[72:75], v[104:107], v[46:49]
	v_mfma_f32_16x16x32_bf16 v[42:45], v[80:83], v[104:107], v[42:45]
	v_mfma_f32_16x16x32_bf16 v[38:41], v[72:75], v[112:115], v[38:41]
	v_mfma_f32_16x16x32_bf16 v[34:37], v[80:83], v[112:115], v[34:37]
	v_mfma_f32_16x16x32_bf16 v[62:65], v[76:79], v[92:95], v[62:65]
	v_mfma_f32_16x16x32_bf16 v[58:61], v[84:87], v[92:95], v[58:61]
	v_mfma_f32_16x16x32_bf16 v[54:57], v[76:79], v[100:103], v[54:57]
	v_mfma_f32_16x16x32_bf16 v[50:53], v[84:87], v[100:103], v[50:53]
	v_mfma_f32_16x16x32_bf16 v[46:49], v[76:79], v[108:111], v[46:49]
	v_mfma_f32_16x16x32_bf16 v[42:45], v[84:87], v[108:111], v[42:45]
	v_mfma_f32_16x16x32_bf16 v[38:41], v[76:79], v[116:119], v[38:41]
	v_mfma_f32_16x16x32_bf16 v[34:37], v[84:87], v[116:119], v[34:37]
	s_setprio 0
	s_setprio 1
	s_setprio 0
	s_barrier
	s_mov_b32 m0, s90
	v_lshl_add_u64 v[124:125], v[120:121], 0, s[92:93]
	global_load_lds_dwordx4 v[124:125], off
	v_lshl_add_u64 v[124:125], v[120:121], 0, s[12:13]
	s_mov_b32 m0, s91
	s_nop 0
	global_load_lds_dwordx4 v[124:125], off
	v_lshl_add_u64 v[124:125], v[120:121], 0, s[38:39]
	s_mov_b32 m0, s72
	v_lshl_add_u64 v[120:121], v[120:121], 0, s[94:95]
	global_load_lds_dwordx4 v[124:125], off
	s_mov_b32 m0, s73
	s_nop 0
	global_load_lds_dwordx4 v[120:121], off
	v_lshl_add_u64 v[120:121], v[122:123], 0, s[92:93]
	s_mov_b32 m0, s70
	s_nop 0
	global_load_lds_dwordx4 v[120:121], off
	v_lshl_add_u64 v[120:121], v[122:123], 0, s[30:31]
	s_mov_b32 m0, s71
	s_nop 0
	global_load_lds_dwordx4 v[120:121], off
	ds_read_b128 v[88:91], v70 offset:53248
	ds_read_b128 v[92:95], v70 offset:54272
	ds_read_b128 v[96:99], v70 offset:55296
	ds_read_b128 v[100:103], v70 offset:56320
	ds_read_b128 v[104:107], v70 offset:57344
	ds_read_b128 v[108:111], v70 offset:58368
	ds_read_b128 v[112:115], v70 offset:59392
	ds_read_b128 v[116:119], v70 offset:60416
	s_waitcnt vmcnt(8)
	s_waitcnt lgkmcnt(0)
	s_barrier
	s_setprio 1
	s_waitcnt lgkmcnt(0)
	v_mfma_f32_16x16x32_bf16 v[30:33], v[72:75], v[88:91], v[30:33]
	v_mfma_f32_16x16x32_bf16 v[26:29], v[80:83], v[88:91], v[26:29]
	v_mfma_f32_16x16x32_bf16 v[22:25], v[72:75], v[96:99], v[22:25]
	v_mfma_f32_16x16x32_bf16 v[18:21], v[80:83], v[96:99], v[18:21]
	v_mfma_f32_16x16x32_bf16 v[14:17], v[72:75], v[104:107], v[14:17]
	v_mfma_f32_16x16x32_bf16 v[10:13], v[80:83], v[104:107], v[10:13]
	v_mfma_f32_16x16x32_bf16 v[6:9], v[72:75], v[112:115], v[6:9]
	v_mfma_f32_16x16x32_bf16 v[2:5], v[80:83], v[112:115], v[2:5]
	v_mfma_f32_16x16x32_bf16 v[30:33], v[76:79], v[92:95], v[30:33]
	v_mfma_f32_16x16x32_bf16 v[26:29], v[84:87], v[92:95], v[26:29]
	v_mfma_f32_16x16x32_bf16 v[22:25], v[76:79], v[100:103], v[22:25]
	v_mfma_f32_16x16x32_bf16 v[18:21], v[84:87], v[100:103], v[18:21]
	v_mfma_f32_16x16x32_bf16 v[14:17], v[76:79], v[108:111], v[14:17]
	v_mfma_f32_16x16x32_bf16 v[10:13], v[84:87], v[108:111], v[10:13]
	v_mfma_f32_16x16x32_bf16 v[6:9], v[76:79], v[116:119], v[6:9]
	v_mfma_f32_16x16x32_bf16 v[2:5], v[84:87], v[116:119], v[2:5]
	s_setprio 0
	s_setprio 1
	s_setprio 0
	s_barrier
	s_movk_i32 s41, 0x100
	s_andn2_b64 vcc, exec, s[56:57]
	s_mov_b64 s[14:15], -1
	s_mov_b64 s[56:57], 0
	s_cbranch_vccz .LBB0_591
	s_mov_b64 s[0:1], 0x10000
	s_and_b64 vcc, exec, s[46:47]
	s_cbranch_vccz .LBB0_594
	s_barrier

.LBB0_616:
	s_add_u32 s53, s50, 0xfffe8080
	s_addc_u32 s71, s51, -1
	s_add_i32 s74, 0, 0x11000
	s_cmp_eq_u32 s52, 2
	s_cselect_b64 s[14:15], -1, 0
	s_and_b64 s[14:15], s[14:15], exec
	s_cselect_b32 s15, s45, s71
	s_cselect_b32 s14, s44, s53
	v_add_u32_e32 v137, s74, v1
	s_cselect_b32 s73, s47, s43
	s_cselect_b32 s72, s46, s35
	s_add_i32 s53, 0, 0x15000
	ds_read_b128 v[138:141], v137
	ds_read_b128 v[142:145], v137 offset:1024
	ds_read_b128 v[146:149], v137 offset:2048
	ds_read_b128 v[150:153], v137 offset:3072
	v_add_u32_e32 v137, s53, v1
	ds_read_b128 v[154:157], v137
	ds_read_b128 v[158:161], v137 offset:1024
	ds_read_b128 v[162:165], v137 offset:2048
	ds_read_b128 v[166:169], v137 offset:3072
	v_lshl_add_u64 v[192:193], s[50:51], 0, v[134:135]
	s_add_i32 m0, s25, 0xd000
	ds_read_b128 v[170:173], v136 offset:4096
	ds_read_b128 v[174:177], v136 offset:5120
	ds_read_b128 v[178:181], v136 offset:6144
	ds_read_b128 v[182:185], v136 offset:7168
	ds_read_b128 v[196:199], v136 offset:8192
	ds_read_b128 v[200:203], v136 offset:9216
	ds_read_b128 v[204:207], v136 offset:10240
	ds_read_b128 v[208:211], v136 offset:11264
	global_load_lds_dwordx4 v[192:193], off
	v_lshl_add_u64 v[192:193], v[192:193], 0, s[20:21]
	s_add_i32 m0, s25, 0xf000
	s_nop 0
	global_load_lds_dwordx4 v[192:193], off
	s_waitcnt vmcnt(8)
	s_waitcnt lgkmcnt(0)
	s_barrier
	s_setprio 1
	s_waitcnt lgkmcnt(0)
	v_mfma_f32_16x16x32_bf16 v[126:129], v[138:141], v[170:173], v[126:129]
	v_mfma_f32_16x16x32_bf16 v[122:125], v[146:149], v[170:173], v[122:125]
	v_mfma_f32_16x16x32_bf16 v[110:113], v[138:141], v[178:181], v[110:113]
	v_mfma_f32_16x16x32_bf16 v[106:109], v[146:149], v[178:181], v[106:109]
	v_mfma_f32_16x16x32_bf16 v[94:97], v[138:141], v[196:199], v[94:97]
	v_mfma_f32_16x16x32_bf16 v[90:93], v[146:149], v[196:199], v[90:93]
	v_mfma_f32_16x16x32_bf16 v[78:81], v[138:141], v[204:207], v[78:81]
	v_mfma_f32_16x16x32_bf16 v[74:77], v[146:149], v[204:207], v[74:77]
	v_mfma_f32_16x16x32_bf16 v[126:129], v[142:145], v[174:177], v[126:129]
	v_mfma_f32_16x16x32_bf16 v[122:125], v[150:153], v[174:177], v[122:125]
	v_mfma_f32_16x16x32_bf16 v[110:113], v[142:145], v[182:185], v[110:113]
	v_mfma_f32_16x16x32_bf16 v[106:109], v[150:153], v[182:185], v[106:109]
	v_mfma_f32_16x16x32_bf16 v[94:97], v[142:145], v[200:203], v[94:97]
	v_mfma_f32_16x16x32_bf16 v[90:93], v[150:153], v[200:203], v[90:93]
	v_mfma_f32_16x16x32_bf16 v[78:81], v[142:145], v[208:211], v[78:81]
	v_mfma_f32_16x16x32_bf16 v[74:77], v[150:153], v[208:211], v[74:77]
	s_setprio 0
	s_setprio 1
	v_mfma_f32_16x16x32_bf16 v[118:121], v[154:157], v[170:173], v[118:121]
	v_mfma_f32_16x16x32_bf16 v[114:117], v[162:165], v[170:173], v[114:117]
	v_mfma_f32_16x16x32_bf16 v[102:105], v[154:157], v[178:181], v[102:105]
	v_mfma_f32_16x16x32_bf16 v[98:101], v[162:165], v[178:181], v[98:101]
	v_mfma_f32_16x16x32_bf16 v[86:89], v[154:157], v[196:199], v[86:89]
	v_mfma_f32_16x16x32_bf16 v[82:85], v[162:165], v[196:199], v[82:85]
	v_mfma_f32_16x16x32_bf16 v[70:73], v[154:157], v[204:207], v[70:73]
	v_mfma_f32_16x16x32_bf16 v[66:69], v[162:165], v[204:207], v[66:69]
	v_mfma_f32_16x16x32_bf16 v[118:121], v[158:161], v[174:177], v[118:121]
	v_mfma_f32_16x16x32_bf16 v[114:117], v[166:169], v[174:177], v[114:117]
	v_mfma_f32_16x16x32_bf16 v[102:105], v[158:161], v[182:185], v[102:105]
	v_mfma_f32_16x16x32_bf16 v[98:101], v[166:169], v[182:185], v[98:101]
	v_mfma_f32_16x16x32_bf16 v[86:89], v[158:161], v[200:203], v[86:89]
	v_mfma_f32_16x16x32_bf16 v[82:85], v[166:169], v[200:203], v[82:85]
	v_mfma_f32_16x16x32_bf16 v[70:73], v[158:161], v[208:211], v[70:73]
	v_mfma_f32_16x16x32_bf16 v[66:69], v[166:169], v[208:211], v[66:69]
	s_setprio 0
	s_barrier
	s_add_i32 s71, s74, s24
	v_lshl_add_u64 v[192:193], s[72:73], 0, v[186:187]
	s_mov_b32 m0, s71
	global_load_lds_dwordx4 v186, s[72:73]
	v_lshl_add_u64 v[212:213], v[192:193], 0, s[20:21]
	s_add_i32 m0, s71, 0x2000
	s_add_i32 s53, s53, s24
	global_load_lds_dwordx4 v[212:213], off
	v_lshl_add_u64 v[212:213], v[192:193], 0, s[18:19]
	s_mov_b32 m0, s53
	s_nop 0
	global_load_lds_dwordx4 v[212:213], off
	v_lshl_add_u64 v[212:213], v[192:193], 0, s[22:23]
	s_add_i32 m0, s53, 0x2000
	s_nop 0
	global_load_lds_dwordx4 v[212:213], off
	v_lshl_add_u64 v[212:213], s[14:15], 0, v[130:131]
	s_mov_b32 m0, s28
	v_lshl_add_u64 v[214:215], v[212:213], 0, s[20:21]
	global_load_lds_dwordx4 v[212:213], off
	s_mov_b32 m0, s29
	s_nop 0
	global_load_lds_dwordx4 v[214:215], off
	ds_read_b128 v[170:173], v136 offset:20480
	ds_read_b128 v[174:177], v136 offset:21504
	ds_read_b128 v[178:181], v136 offset:22528
	ds_read_b128 v[182:185], v136 offset:23552
	ds_read_b128 v[196:199], v136 offset:24576
	ds_read_b128 v[200:203], v136 offset:25600
	ds_read_b128 v[204:207], v136 offset:26624
	ds_read_b128 v[208:211], v136 offset:27648
	s_waitcnt vmcnt(8)
	s_waitcnt lgkmcnt(0)
	s_barrier
	s_setprio 1
	s_waitcnt lgkmcnt(0)
	v_mfma_f32_16x16x32_bf16 v[62:65], v[138:141], v[170:173], v[62:65]
	v_mfma_f32_16x16x32_bf16 v[58:61], v[146:149], v[170:173], v[58:61]
	v_mfma_f32_16x16x32_bf16 v[46:49], v[138:141], v[178:181], v[46:49]
	v_mfma_f32_16x16x32_bf16 v[42:45], v[146:149], v[178:181], v[42:45]
	v_mfma_f32_16x16x32_bf16 v[30:33], v[138:141], v[196:199], v[30:33]
	v_mfma_f32_16x16x32_bf16 v[26:29], v[146:149], v[196:199], v[26:29]
	v_mfma_f32_16x16x32_bf16 v[14:17], v[138:141], v[204:207], v[14:17]
	v_mfma_f32_16x16x32_bf16 v[10:13], v[146:149], v[204:207], v[10:13]
	v_mfma_f32_16x16x32_bf16 v[62:65], v[142:145], v[174:177], v[62:65]
	v_mfma_f32_16x16x32_bf16 v[58:61], v[150:153], v[174:177], v[58:61]
	v_mfma_f32_16x16x32_bf16 v[46:49], v[142:145], v[182:185], v[46:49]
	v_mfma_f32_16x16x32_bf16 v[42:45], v[150:153], v[182:185], v[42:45]
	v_mfma_f32_16x16x32_bf16 v[30:33], v[142:145], v[200:203], v[30:33]
	v_mfma_f32_16x16x32_bf16 v[26:29], v[150:153], v[200:203], v[26:29]
	v_mfma_f32_16x16x32_bf16 v[14:17], v[142:145], v[208:211], v[14:17]
	v_mfma_f32_16x16x32_bf16 v[10:13], v[150:153], v[208:211], v[10:13]
	s_setprio 0
	s_setprio 1
	v_mfma_f32_16x16x32_bf16 v[54:57], v[154:157], v[170:173], v[54:57]
	v_mfma_f32_16x16x32_bf16 v[50:53], v[162:165], v[170:173], v[50:53]
	v_mfma_f32_16x16x32_bf16 v[38:41], v[154:157], v[178:181], v[38:41]
	v_mfma_f32_16x16x32_bf16 v[34:37], v[162:165], v[178:181], v[34:37]
	v_mfma_f32_16x16x32_bf16 v[22:25], v[154:157], v[196:199], v[22:25]
	v_mfma_f32_16x16x32_bf16 v[18:21], v[162:165], v[196:199], v[18:21]
	v_mfma_f32_16x16x32_bf16 v[6:9], v[154:157], v[204:207], v[6:9]
	v_mfma_f32_16x16x32_bf16 v[2:5], v[162:165], v[204:207], v[2:5]
	v_mfma_f32_16x16x32_bf16 v[54:57], v[158:161], v[174:177], v[54:57]
	v_mfma_f32_16x16x32_bf16 v[50:53], v[166:169], v[174:177], v[50:53]
	v_mfma_f32_16x16x32_bf16 v[38:41], v[158:161], v[182:185], v[38:41]
	v_mfma_f32_16x16x32_bf16 v[34:37], v[166:169], v[182:185], v[34:37]
	v_mfma_f32_16x16x32_bf16 v[22:25], v[158:161], v[200:203], v[22:25]
	v_mfma_f32_16x16x32_bf16 v[18:21], v[166:169], v[200:203], v[18:21]
	v_mfma_f32_16x16x32_bf16 v[6:9], v[158:161], v[208:211], v[6:9]
	v_mfma_f32_16x16x32_bf16 v[2:5], v[166:169], v[208:211], v[2:5]
	s_setprio 0
	s_barrier
	s_add_i32 s14, 0, 0x19000
	v_add_u32_e32 v137, s14, v1
	s_add_i32 s15, 0, 0x1d000
	ds_read_b128 v[138:141], v137
	ds_read_b128 v[142:145], v137 offset:1024
	ds_read_b128 v[146:149], v137 offset:2048
	ds_read_b128 v[150:153], v137 offset:3072
	v_add_u32_e32 v137, s15, v1
	ds_read_b128 v[154:157], v137
	ds_read_b128 v[158:161], v137 offset:1024
	ds_read_b128 v[162:165], v137 offset:2048
	ds_read_b128 v[166:169], v137 offset:3072
	s_mov_b32 m0, s33
	v_lshl_add_u64 v[214:215], v[212:213], 0, s[18:19]
	ds_read_b128 v[170:173], v136 offset:36864
	ds_read_b128 v[174:177], v136 offset:37888
	ds_read_b128 v[178:181], v136 offset:38912
	ds_read_b128 v[182:185], v136 offset:39936
	ds_read_b128 v[196:199], v136 offset:40960
	ds_read_b128 v[200:203], v136 offset:41984
	ds_read_b128 v[204:207], v136 offset:43008
	ds_read_b128 v[208:211], v136 offset:44032
	global_load_lds_dwordx4 v[214:215], off
	v_lshl_add_u64 v[214:215], v[212:213], 0, s[22:23]
	s_mov_b32 m0, s39
	s_nop 0
	global_load_lds_dwordx4 v[214:215], off
	s_waitcnt vmcnt(8)
	s_waitcnt lgkmcnt(0)
	s_barrier
	s_setprio 1
	s_waitcnt lgkmcnt(0)
	v_mfma_f32_16x16x32_bf16 v[126:129], v[138:141], v[170:173], v[126:129]
	v_mfma_f32_16x16x32_bf16 v[122:125], v[146:149], v[170:173], v[122:125]
	v_mfma_f32_16x16x32_bf16 v[110:113], v[138:141], v[178:181], v[110:113]
	v_mfma_f32_16x16x32_bf16 v[106:109], v[146:149], v[178:181], v[106:109]
	v_mfma_f32_16x16x32_bf16 v[94:97], v[138:141], v[196:199], v[94:97]
	v_mfma_f32_16x16x32_bf16 v[90:93], v[146:149], v[196:199], v[90:93]
	v_mfma_f32_16x16x32_bf16 v[78:81], v[138:141], v[204:207], v[78:81]
	v_mfma_f32_16x16x32_bf16 v[74:77], v[146:149], v[204:207], v[74:77]
	v_mfma_f32_16x16x32_bf16 v[126:129], v[142:145], v[174:177], v[126:129]
	v_mfma_f32_16x16x32_bf16 v[122:125], v[150:153], v[174:177], v[122:125]
	v_mfma_f32_16x16x32_bf16 v[110:113], v[142:145], v[182:185], v[110:113]
	v_mfma_f32_16x16x32_bf16 v[106:109], v[150:153], v[182:185], v[106:109]
	v_mfma_f32_16x16x32_bf16 v[94:97], v[142:145], v[200:203], v[94:97]
	v_mfma_f32_16x16x32_bf16 v[90:93], v[150:153], v[200:203], v[90:93]
	v_mfma_f32_16x16x32_bf16 v[78:81], v[142:145], v[208:211], v[78:81]
	v_mfma_f32_16x16x32_bf16 v[74:77], v[150:153], v[208:211], v[74:77]
	s_setprio 0
	s_setprio 1
	v_mfma_f32_16x16x32_bf16 v[118:121], v[154:157], v[170:173], v[118:121]
	v_mfma_f32_16x16x32_bf16 v[114:117], v[162:165], v[170:173], v[114:117]
	v_mfma_f32_16x16x32_bf16 v[102:105], v[154:157], v[178:181], v[102:105]
	v_mfma_f32_16x16x32_bf16 v[98:101], v[162:165], v[178:181], v[98:101]
	v_mfma_f32_16x16x32_bf16 v[86:89], v[154:157], v[196:199], v[86:89]
	v_mfma_f32_16x16x32_bf16 v[82:85], v[162:165], v[196:199], v[82:85]
	v_mfma_f32_16x16x32_bf16 v[70:73], v[154:157], v[204:207], v[70:73]
	v_mfma_f32_16x16x32_bf16 v[66:69], v[162:165], v[204:207], v[66:69]
	v_mfma_f32_16x16x32_bf16 v[118:121], v[158:161], v[174:177], v[118:121]
	v_mfma_f32_16x16x32_bf16 v[114:117], v[166:169], v[174:177], v[114:117]
	v_mfma_f32_16x16x32_bf16 v[102:105], v[158:161], v[182:185], v[102:105]
	v_mfma_f32_16x16x32_bf16 v[98:101], v[166:169], v[182:185], v[98:101]
	v_mfma_f32_16x16x32_bf16 v[86:89], v[158:161], v[200:203], v[86:89]
	v_mfma_f32_16x16x32_bf16 v[82:85], v[166:169], v[200:203], v[82:85]
	v_mfma_f32_16x16x32_bf16 v[70:73], v[158:161], v[208:211], v[70:73]
	v_mfma_f32_16x16x32_bf16 v[66:69], v[166:169], v[208:211], v[66:69]
	s_setprio 0
	s_barrier
	s_add_i32 s14, s14, s24
	v_lshl_add_u64 v[214:215], v[192:193], 0, s[92:93]
	s_mov_b32 m0, s14
	global_load_lds_dwordx4 v[214:215], off
	v_lshl_add_u64 v[214:215], v[192:193], 0, s[26:27]
	s_add_i32 m0, s14, 0x2000
	s_add_i32 s14, s15, s24
	global_load_lds_dwordx4 v[214:215], off
	v_lshl_add_u64 v[214:215], v[192:193], 0, s[30:31]
	s_mov_b32 m0, s14
	v_lshl_add_u64 v[192:193], v[192:193], 0, s[78:79]
	global_load_lds_dwordx4 v[214:215], off
	s_add_i32 m0, s14, 0x2000
	s_nop 0
	global_load_lds_dwordx4 v[192:193], off
	v_lshl_add_u64 v[192:193], v[212:213], 0, s[92:93]
	s_mov_b32 m0, s55
	s_nop 0
	global_load_lds_dwordx4 v[192:193], off
	v_lshl_add_u64 v[192:193], v[212:213], 0, s[26:27]
	s_mov_b32 m0, s56
	s_nop 0
	global_load_lds_dwordx4 v[192:193], off
	ds_read_b128 v[170:173], v136 offset:53248
	ds_read_b128 v[174:177], v136 offset:54272
	ds_read_b128 v[178:181], v136 offset:55296
	ds_read_b128 v[182:185], v136 offset:56320
	ds_read_b128 v[196:199], v136 offset:57344
	ds_read_b128 v[200:203], v136 offset:58368
	ds_read_b128 v[204:207], v136 offset:59392
	ds_read_b128 v[208:211], v136 offset:60416
	s_waitcnt vmcnt(8)
	s_waitcnt lgkmcnt(0)
	s_barrier
	s_setprio 1
	s_waitcnt lgkmcnt(0)
	v_mfma_f32_16x16x32_bf16 v[62:65], v[138:141], v[170:173], v[62:65]
	v_mfma_f32_16x16x32_bf16 v[58:61], v[146:149], v[170:173], v[58:61]
	v_mfma_f32_16x16x32_bf16 v[46:49], v[138:141], v[178:181], v[46:49]
	v_mfma_f32_16x16x32_bf16 v[42:45], v[146:149], v[178:181], v[42:45]
	v_mfma_f32_16x16x32_bf16 v[30:33], v[138:141], v[196:199], v[30:33]
	v_mfma_f32_16x16x32_bf16 v[26:29], v[146:149], v[196:199], v[26:29]
	v_mfma_f32_16x16x32_bf16 v[14:17], v[138:141], v[204:207], v[14:17]
	v_mfma_f32_16x16x32_bf16 v[10:13], v[146:149], v[204:207], v[10:13]
	v_mfma_f32_16x16x32_bf16 v[62:65], v[142:145], v[174:177], v[62:65]
	v_mfma_f32_16x16x32_bf16 v[58:61], v[150:153], v[174:177], v[58:61]
	v_mfma_f32_16x16x32_bf16 v[46:49], v[142:145], v[182:185], v[46:49]
	v_mfma_f32_16x16x32_bf16 v[42:45], v[150:153], v[182:185], v[42:45]
	v_mfma_f32_16x16x32_bf16 v[30:33], v[142:145], v[200:203], v[30:33]
	v_mfma_f32_16x16x32_bf16 v[26:29], v[150:153], v[200:203], v[26:29]
	v_mfma_f32_16x16x32_bf16 v[14:17], v[142:145], v[208:211], v[14:17]
	v_mfma_f32_16x16x32_bf16 v[10:13], v[150:153], v[208:211], v[10:13]
	s_setprio 0
	s_setprio 1
	v_mfma_f32_16x16x32_bf16 v[54:57], v[154:157], v[170:173], v[54:57]
	v_mfma_f32_16x16x32_bf16 v[50:53], v[162:165], v[170:173], v[50:53]
	v_mfma_f32_16x16x32_bf16 v[38:41], v[154:157], v[178:181], v[38:41]
	v_mfma_f32_16x16x32_bf16 v[34:37], v[162:165], v[178:181], v[34:37]
	v_mfma_f32_16x16x32_bf16 v[22:25], v[154:157], v[196:199], v[22:25]
	v_mfma_f32_16x16x32_bf16 v[18:21], v[162:165], v[196:199], v[18:21]
	v_mfma_f32_16x16x32_bf16 v[6:9], v[154:157], v[204:207], v[6:9]
	v_mfma_f32_16x16x32_bf16 v[2:5], v[162:165], v[204:207], v[2:5]
	v_mfma_f32_16x16x32_bf16 v[54:57], v[158:161], v[174:177], v[54:57]
	v_mfma_f32_16x16x32_bf16 v[50:53], v[166:169], v[174:177], v[50:53]
	v_mfma_f32_16x16x32_bf16 v[38:41], v[158:161], v[182:185], v[38:41]
	v_mfma_f32_16x16x32_bf16 v[34:37], v[166:169], v[182:185], v[34:37]
	v_mfma_f32_16x16x32_bf16 v[22:25], v[158:161], v[200:203], v[22:25]
	v_mfma_f32_16x16x32_bf16 v[18:21], v[166:169], v[200:203], v[18:21]
	v_mfma_f32_16x16x32_bf16 v[6:9], v[158:161], v[208:211], v[6:9]
	v_mfma_f32_16x16x32_bf16 v[2:5], v[166:169], v[208:211], v[2:5]
	s_setprio 0
	s_barrier
	s_add_i32 s52, s52, 2
	s_add_u32 s35, s35, 0x100
	s_addc_u32 s43, s43, 0
	s_add_u32 s50, s50, 0x100
	s_addc_u32 s51, s51, 0
	s_cmp_gt_u32 s52, 3
	s_cbranch_scc0 .LBB0_616
	s_and_b64 vcc, exec, s[40:41]
	s_cbranch_vccz .LBB0_619
	s_barrier

.LBB0_643:
	s_add_i32 s35, s96, 0x100
	s_and_b64 s[14:15], s[44:45], exec
	s_cselect_b32 s14, 0, s35
	s_cselect_b32 s15, 0, 0
	s_add_i32 s50, 0, 0x11000
	s_add_i32 s51, 0, 0x15000
	v_add_u32_e32 v150, s50, v40
	v_add_u32_e32 v166, s51, v40
	ds_read_b128 v[42:45], v150
	ds_read_b128 v[46:49], v150 offset:1024
	ds_read_b128 v[146:149], v150 offset:2048
	ds_read_b128 v[150:153], v150 offset:3072
	ds_read_b128 v[154:157], v166
	ds_read_b128 v[158:161], v166 offset:1024
	ds_read_b128 v[162:165], v166 offset:2048
	ds_read_b128 v[166:169], v166 offset:3072
	s_add_i32 s45, 0, 0x19000
	s_add_i32 s44, 0, 0x1d000
	s_add_i32 s49, s50, s1
	s_add_i32 s47, s51, s1
	s_add_i32 s35, s45, s1
	s_add_i32 s51, s44, s1
	s_add_i32 m0, s3, 0xd000
	s_add_i32 s53, s3, 0xf000
	s_add_i32 s48, s49, 0x2000
	s_add_i32 s46, s47, 0x2000
	s_add_i32 s52, s35, 0x2000
	s_add_i32 s50, s51, 0x2000
	v_lshl_add_u64 v[192:193], v[36:37], 0, s[96:97]
	v_lshl_add_u64 v[212:213], v[192:193], 0, s[60:61]
	ds_read_b128 v[170:173], v41 offset:4096
	ds_read_b128 v[174:177], v41 offset:5120
	ds_read_b128 v[178:181], v41 offset:6144
	ds_read_b128 v[182:185], v41 offset:7168
	ds_read_b128 v[196:199], v41 offset:8192
	ds_read_b128 v[200:203], v41 offset:9216
	ds_read_b128 v[204:207], v41 offset:10240
	ds_read_b128 v[208:211], v41 offset:11264
	global_load_lds_dwordx4 v[212:213], off
	v_lshl_add_u64 v[192:193], v[192:193], 0, s[30:31]
	s_mov_b32 m0, s53
	s_nop 0
	global_load_lds_dwordx4 v[192:193], off
	s_waitcnt vmcnt(8)
	s_waitcnt lgkmcnt(0)
	s_barrier
	s_setprio 1
	s_waitcnt lgkmcnt(0)
	v_mfma_f32_16x16x32_bf16 v[142:145], v[42:45], v[170:173], v[142:145]
	v_mfma_f32_16x16x32_bf16 v[138:141], v[146:149], v[170:173], v[138:141]
	v_mfma_f32_16x16x32_bf16 v[126:129], v[42:45], v[178:181], v[126:129]
	v_mfma_f32_16x16x32_bf16 v[122:125], v[146:149], v[178:181], v[122:125]
	v_mfma_f32_16x16x32_bf16 v[110:113], v[42:45], v[196:199], v[110:113]
	v_mfma_f32_16x16x32_bf16 v[106:109], v[146:149], v[196:199], v[106:109]
	v_mfma_f32_16x16x32_bf16 v[94:97], v[42:45], v[204:207], v[94:97]
	v_mfma_f32_16x16x32_bf16 v[90:93], v[146:149], v[204:207], v[90:93]
	v_mfma_f32_16x16x32_bf16 v[142:145], v[46:49], v[174:177], v[142:145]
	v_mfma_f32_16x16x32_bf16 v[138:141], v[150:153], v[174:177], v[138:141]
	v_mfma_f32_16x16x32_bf16 v[126:129], v[46:49], v[182:185], v[126:129]
	v_mfma_f32_16x16x32_bf16 v[122:125], v[150:153], v[182:185], v[122:125]
	v_mfma_f32_16x16x32_bf16 v[110:113], v[46:49], v[200:203], v[110:113]
	v_mfma_f32_16x16x32_bf16 v[106:109], v[150:153], v[200:203], v[106:109]
	v_mfma_f32_16x16x32_bf16 v[94:97], v[46:49], v[208:211], v[94:97]
	v_mfma_f32_16x16x32_bf16 v[90:93], v[150:153], v[208:211], v[90:93]
	s_setprio 0
	s_setprio 1
	v_mfma_f32_16x16x32_bf16 v[134:137], v[154:157], v[170:173], v[134:137]
	v_mfma_f32_16x16x32_bf16 v[130:133], v[162:165], v[170:173], v[130:133]
	v_mfma_f32_16x16x32_bf16 v[118:121], v[154:157], v[178:181], v[118:121]
	v_mfma_f32_16x16x32_bf16 v[114:117], v[162:165], v[178:181], v[114:117]
	v_mfma_f32_16x16x32_bf16 v[102:105], v[154:157], v[196:199], v[102:105]
	v_mfma_f32_16x16x32_bf16 v[98:101], v[162:165], v[196:199], v[98:101]
	v_mfma_f32_16x16x32_bf16 v[86:89], v[154:157], v[204:207], v[86:89]
	v_mfma_f32_16x16x32_bf16 v[82:85], v[162:165], v[204:207], v[82:85]
	v_mfma_f32_16x16x32_bf16 v[134:137], v[158:161], v[174:177], v[134:137]
	v_mfma_f32_16x16x32_bf16 v[130:133], v[166:169], v[174:177], v[130:133]
	v_mfma_f32_16x16x32_bf16 v[118:121], v[158:161], v[182:185], v[118:121]
	v_mfma_f32_16x16x32_bf16 v[114:117], v[166:169], v[182:185], v[114:117]
	v_mfma_f32_16x16x32_bf16 v[102:105], v[158:161], v[200:203], v[102:105]
	v_mfma_f32_16x16x32_bf16 v[98:101], v[166:169], v[200:203], v[98:101]
	v_mfma_f32_16x16x32_bf16 v[86:89], v[158:161], v[208:211], v[86:89]
	v_mfma_f32_16x16x32_bf16 v[82:85], v[166:169], v[208:211], v[82:85]
	s_setprio 0
	s_barrier
	s_mov_b32 m0, s49
	v_lshl_add_u64 v[192:193], v[34:35], 0, s[14:15]
	global_load_lds_dwordx4 v[192:193], off
	v_lshl_add_u64 v[212:213], v[192:193], 0, s[54:55]
	s_mov_b32 m0, s48
	s_nop 0
	global_load_lds_dwordx4 v[212:213], off
	v_lshl_add_u64 v[212:213], v[192:193], 0, s[56:57]
	s_mov_b32 m0, s47
	s_nop 0
	global_load_lds_dwordx4 v[212:213], off
	v_lshl_add_u64 v[212:213], v[192:193], 0, s[18:19]
	s_mov_b32 m0, s46
	s_nop 0
	global_load_lds_dwordx4 v[212:213], off
	v_lshl_add_u64 v[212:213], v[36:37], 0, s[14:15]
	s_mov_b32 m0, s24
	v_lshl_add_u64 v[214:215], v[212:213], 0, s[54:55]
	global_load_lds_dwordx4 v[212:213], off
	s_mov_b32 m0, s25
	s_nop 0
	global_load_lds_dwordx4 v[214:215], off
	ds_read_b128 v[170:173], v41 offset:20480
	ds_read_b128 v[174:177], v41 offset:21504
	ds_read_b128 v[178:181], v41 offset:22528
	ds_read_b128 v[182:185], v41 offset:23552
	ds_read_b128 v[196:199], v41 offset:24576
	ds_read_b128 v[200:203], v41 offset:25600
	ds_read_b128 v[204:207], v41 offset:26624
	ds_read_b128 v[208:211], v41 offset:27648
	s_waitcnt vmcnt(8)
	s_waitcnt lgkmcnt(0)
	s_barrier
	s_setprio 1
	s_waitcnt lgkmcnt(0)
	v_mfma_f32_16x16x32_bf16 v[78:81], v[42:45], v[170:173], v[78:81]
	v_mfma_f32_16x16x32_bf16 v[74:77], v[146:149], v[170:173], v[74:77]
	v_mfma_f32_16x16x32_bf16 v[62:65], v[42:45], v[178:181], v[62:65]
	v_mfma_f32_16x16x32_bf16 v[58:61], v[146:149], v[178:181], v[58:61]
	v_mfma_f32_16x16x32_bf16 v[30:33], v[42:45], v[196:199], v[30:33]
	v_mfma_f32_16x16x32_bf16 v[26:29], v[146:149], v[196:199], v[26:29]
	v_mfma_f32_16x16x32_bf16 v[14:17], v[42:45], v[204:207], v[14:17]
	v_mfma_f32_16x16x32_bf16 v[10:13], v[146:149], v[204:207], v[10:13]
	v_mfma_f32_16x16x32_bf16 v[78:81], v[46:49], v[174:177], v[78:81]
	v_mfma_f32_16x16x32_bf16 v[74:77], v[150:153], v[174:177], v[74:77]
	v_mfma_f32_16x16x32_bf16 v[62:65], v[46:49], v[182:185], v[62:65]
	v_mfma_f32_16x16x32_bf16 v[58:61], v[150:153], v[182:185], v[58:61]
	v_mfma_f32_16x16x32_bf16 v[30:33], v[46:49], v[200:203], v[30:33]
	v_mfma_f32_16x16x32_bf16 v[26:29], v[150:153], v[200:203], v[26:29]
	v_mfma_f32_16x16x32_bf16 v[14:17], v[46:49], v[208:211], v[14:17]
	v_mfma_f32_16x16x32_bf16 v[10:13], v[150:153], v[208:211], v[10:13]
	s_setprio 0
	s_setprio 1
	v_mfma_f32_16x16x32_bf16 v[54:57], v[154:157], v[178:181], v[54:57]
	v_mfma_f32_16x16x32_bf16 v[50:53], v[162:165], v[178:181], v[50:53]
	v_mfma_f32_16x16x32_bf16 v[22:25], v[154:157], v[196:199], v[22:25]
	v_mfma_f32_16x16x32_bf16 v[18:21], v[162:165], v[196:199], v[18:21]
	v_mfma_f32_16x16x32_bf16 v[6:9], v[154:157], v[204:207], v[6:9]
	v_mfma_f32_16x16x32_bf16 v[2:5], v[162:165], v[204:207], v[2:5]
	v_mfma_f32_16x16x32_bf16 v[42:45], v[154:157], v[170:173], v[70:73]
	v_mfma_f32_16x16x32_bf16 v[46:49], v[162:165], v[170:173], v[66:69]
	v_mfma_f32_16x16x32_bf16 v[54:57], v[158:161], v[182:185], v[54:57]
	v_mfma_f32_16x16x32_bf16 v[50:53], v[166:169], v[182:185], v[50:53]
	v_mfma_f32_16x16x32_bf16 v[22:25], v[158:161], v[200:203], v[22:25]
	v_mfma_f32_16x16x32_bf16 v[18:21], v[166:169], v[200:203], v[18:21]
	v_mfma_f32_16x16x32_bf16 v[6:9], v[158:161], v[208:211], v[6:9]
	v_mfma_f32_16x16x32_bf16 v[2:5], v[166:169], v[208:211], v[2:5]
	v_mfma_f32_16x16x32_bf16 v[42:45], v[158:161], v[174:177], v[42:45]
	v_mfma_f32_16x16x32_bf16 v[46:49], v[166:169], v[174:177], v[46:49]
	s_setprio 0
	s_barrier
	v_add_u32_e32 v150, s45, v40
	v_add_u32_e32 v166, s44, v40
	ds_read_b128 v[66:69], v150
	ds_read_b128 v[70:73], v150 offset:1024
	ds_read_b128 v[146:149], v150 offset:2048
	ds_read_b128 v[150:153], v150 offset:3072
	ds_read_b128 v[154:157], v166
	ds_read_b128 v[158:161], v166 offset:1024
	ds_read_b128 v[162:165], v166 offset:2048
	ds_read_b128 v[166:169], v166 offset:3072
	s_mov_b32 m0, s28
	v_lshl_add_u64 v[214:215], v[212:213], 0, s[56:57]
	ds_read_b128 v[170:173], v41 offset:36864
	ds_read_b128 v[174:177], v41 offset:37888
	ds_read_b128 v[178:181], v41 offset:38912
	ds_read_b128 v[182:185], v41 offset:39936
	ds_read_b128 v[196:199], v41 offset:40960
	ds_read_b128 v[200:203], v41 offset:41984
	ds_read_b128 v[204:207], v41 offset:43008
	ds_read_b128 v[208:211], v41 offset:44032
	global_load_lds_dwordx4 v[214:215], off
	v_lshl_add_u64 v[214:215], v[212:213], 0, s[18:19]
	s_mov_b32 m0, s29
	s_nop 0
	global_load_lds_dwordx4 v[214:215], off
	s_waitcnt vmcnt(8)
	s_waitcnt lgkmcnt(0)
	s_barrier
	s_setprio 1
	s_waitcnt lgkmcnt(0)
	v_mfma_f32_16x16x32_bf16 v[142:145], v[66:69], v[170:173], v[142:145]
	v_mfma_f32_16x16x32_bf16 v[138:141], v[146:149], v[170:173], v[138:141]
	v_mfma_f32_16x16x32_bf16 v[126:129], v[66:69], v[178:181], v[126:129]
	v_mfma_f32_16x16x32_bf16 v[122:125], v[146:149], v[178:181], v[122:125]
	v_mfma_f32_16x16x32_bf16 v[110:113], v[66:69], v[196:199], v[110:113]
	v_mfma_f32_16x16x32_bf16 v[106:109], v[146:149], v[196:199], v[106:109]
	v_mfma_f32_16x16x32_bf16 v[94:97], v[66:69], v[204:207], v[94:97]
	v_mfma_f32_16x16x32_bf16 v[90:93], v[146:149], v[204:207], v[90:93]
	v_mfma_f32_16x16x32_bf16 v[142:145], v[70:73], v[174:177], v[142:145]
	v_mfma_f32_16x16x32_bf16 v[138:141], v[150:153], v[174:177], v[138:141]
	v_mfma_f32_16x16x32_bf16 v[126:129], v[70:73], v[182:185], v[126:129]
	v_mfma_f32_16x16x32_bf16 v[122:125], v[150:153], v[182:185], v[122:125]
	v_mfma_f32_16x16x32_bf16 v[110:113], v[70:73], v[200:203], v[110:113]
	v_mfma_f32_16x16x32_bf16 v[106:109], v[150:153], v[200:203], v[106:109]
	v_mfma_f32_16x16x32_bf16 v[94:97], v[70:73], v[208:211], v[94:97]
	v_mfma_f32_16x16x32_bf16 v[90:93], v[150:153], v[208:211], v[90:93]
	s_setprio 0
	s_setprio 1
	v_mfma_f32_16x16x32_bf16 v[134:137], v[154:157], v[170:173], v[134:137]
	v_mfma_f32_16x16x32_bf16 v[130:133], v[162:165], v[170:173], v[130:133]
	v_mfma_f32_16x16x32_bf16 v[118:121], v[154:157], v[178:181], v[118:121]
	v_mfma_f32_16x16x32_bf16 v[114:117], v[162:165], v[178:181], v[114:117]
	v_mfma_f32_16x16x32_bf16 v[102:105], v[154:157], v[196:199], v[102:105]
	v_mfma_f32_16x16x32_bf16 v[98:101], v[162:165], v[196:199], v[98:101]
	v_mfma_f32_16x16x32_bf16 v[86:89], v[154:157], v[204:207], v[86:89]
	v_mfma_f32_16x16x32_bf16 v[82:85], v[162:165], v[204:207], v[82:85]
	v_mfma_f32_16x16x32_bf16 v[134:137], v[158:161], v[174:177], v[134:137]
	v_mfma_f32_16x16x32_bf16 v[130:133], v[166:169], v[174:177], v[130:133]
	v_mfma_f32_16x16x32_bf16 v[118:121], v[158:161], v[182:185], v[118:121]
	v_mfma_f32_16x16x32_bf16 v[114:117], v[166:169], v[182:185], v[114:117]
	v_mfma_f32_16x16x32_bf16 v[102:105], v[158:161], v[200:203], v[102:105]
	v_mfma_f32_16x16x32_bf16 v[98:101], v[166:169], v[200:203], v[98:101]
	v_mfma_f32_16x16x32_bf16 v[86:89], v[158:161], v[208:211], v[86:89]
	v_mfma_f32_16x16x32_bf16 v[82:85], v[166:169], v[208:211], v[82:85]
	s_setprio 0
	s_barrier
	s_mov_b32 m0, s35
	v_lshl_add_u64 v[214:215], v[192:193], 0, s[92:93]
	global_load_lds_dwordx4 v[214:215], off
	v_lshl_add_u64 v[214:215], v[192:193], 0, s[58:59]
	s_mov_b32 m0, s52
	s_nop 0
	global_load_lds_dwordx4 v[214:215], off
	v_lshl_add_u64 v[214:215], v[192:193], 0, s[60:61]
	s_mov_b32 m0, s51
	v_lshl_add_u64 v[192:193], v[192:193], 0, s[30:31]
	global_load_lds_dwordx4 v[214:215], off
	s_mov_b32 m0, s50
	s_nop 0
	global_load_lds_dwordx4 v[192:193], off
	v_lshl_add_u64 v[192:193], v[212:213], 0, s[92:93]
	s_mov_b32 m0, s33
	s_nop 0
	global_load_lds_dwordx4 v[192:193], off
	v_lshl_add_u64 v[192:193], v[212:213], 0, s[58:59]
	s_mov_b32 m0, s34
	s_nop 0
	global_load_lds_dwordx4 v[192:193], off
	ds_read_b128 v[170:173], v41 offset:53248
	ds_read_b128 v[174:177], v41 offset:54272
	ds_read_b128 v[178:181], v41 offset:55296
	ds_read_b128 v[182:185], v41 offset:56320
	ds_read_b128 v[196:199], v41 offset:57344
	ds_read_b128 v[200:203], v41 offset:58368
	ds_read_b128 v[204:207], v41 offset:59392
	ds_read_b128 v[208:211], v41 offset:60416
	s_waitcnt vmcnt(8)
	s_waitcnt lgkmcnt(0)
	s_barrier
	s_setprio 1
	s_waitcnt lgkmcnt(0)
	v_mfma_f32_16x16x32_bf16 v[78:81], v[66:69], v[170:173], v[78:81]
	v_mfma_f32_16x16x32_bf16 v[74:77], v[146:149], v[170:173], v[74:77]
	v_mfma_f32_16x16x32_bf16 v[62:65], v[66:69], v[178:181], v[62:65]
	v_mfma_f32_16x16x32_bf16 v[58:61], v[146:149], v[178:181], v[58:61]
	v_mfma_f32_16x16x32_bf16 v[30:33], v[66:69], v[196:199], v[30:33]
	v_mfma_f32_16x16x32_bf16 v[26:29], v[146:149], v[196:199], v[26:29]
	v_mfma_f32_16x16x32_bf16 v[14:17], v[66:69], v[204:207], v[14:17]
	v_mfma_f32_16x16x32_bf16 v[10:13], v[146:149], v[204:207], v[10:13]
	v_mfma_f32_16x16x32_bf16 v[78:81], v[70:73], v[174:177], v[78:81]
	v_mfma_f32_16x16x32_bf16 v[74:77], v[150:153], v[174:177], v[74:77]
	v_mfma_f32_16x16x32_bf16 v[62:65], v[70:73], v[182:185], v[62:65]
	v_mfma_f32_16x16x32_bf16 v[58:61], v[150:153], v[182:185], v[58:61]
	v_mfma_f32_16x16x32_bf16 v[30:33], v[70:73], v[200:203], v[30:33]
	v_mfma_f32_16x16x32_bf16 v[26:29], v[150:153], v[200:203], v[26:29]
	v_mfma_f32_16x16x32_bf16 v[14:17], v[70:73], v[208:211], v[14:17]
	v_mfma_f32_16x16x32_bf16 v[10:13], v[150:153], v[208:211], v[10:13]
	s_setprio 0
	s_setprio 1
	v_mfma_f32_16x16x32_bf16 v[42:45], v[154:157], v[170:173], v[42:45]
	v_mfma_f32_16x16x32_bf16 v[70:73], v[158:161], v[174:177], v[42:45]
	v_mfma_f32_16x16x32_bf16 v[42:45], v[162:165], v[170:173], v[46:49]
	v_mfma_f32_16x16x32_bf16 v[66:69], v[166:169], v[174:177], v[42:45]
	v_mfma_f32_16x16x32_bf16 v[42:45], v[154:157], v[178:181], v[54:57]
	v_mfma_f32_16x16x32_bf16 v[54:57], v[158:161], v[182:185], v[42:45]
	v_mfma_f32_16x16x32_bf16 v[42:45], v[162:165], v[178:181], v[50:53]
	v_mfma_f32_16x16x32_bf16 v[22:25], v[154:157], v[196:199], v[22:25]
	v_mfma_f32_16x16x32_bf16 v[18:21], v[162:165], v[196:199], v[18:21]
	v_mfma_f32_16x16x32_bf16 v[6:9], v[154:157], v[204:207], v[6:9]
	v_mfma_f32_16x16x32_bf16 v[2:5], v[162:165], v[204:207], v[2:5]
	v_mfma_f32_16x16x32_bf16 v[50:53], v[166:169], v[182:185], v[42:45]
	v_mfma_f32_16x16x32_bf16 v[22:25], v[158:161], v[200:203], v[22:25]
	v_mfma_f32_16x16x32_bf16 v[18:21], v[166:169], v[200:203], v[18:21]
	v_mfma_f32_16x16x32_bf16 v[6:9], v[158:161], v[208:211], v[6:9]
	v_mfma_f32_16x16x32_bf16 v[2:5], v[166:169], v[208:211], v[2:5]
	s_setprio 0
	s_barrier
	s_andn2_b64 vcc, exec, s[42:43]
	s_mov_b64 s[44:45], -1
	s_mov_b64 s[42:43], 0
	s_movk_i32 s96, 0x100
	s_cbranch_vccz .LBB0_643
	s_cmpk_lt_u32 s2, 0x100
	s_cbranch_scc0 .LBB0_646
	s_barrier

.LBB0_896:
	s_add_i32 s73, s73, 2
	s_add_u32 s75, s50, 0x80
	s_addc_u32 vcc_lo, s51, 0
	s_and_b64 s[28:29], exec, s[28:29]
	s_cselect_b32 s29, s77, vcc_lo
	s_cselect_b32 s28, s76, s75
	s_add_i32 s75, 0, 0x11000
	v_add_u32_e32 v131, s75, v166
	s_add_i32 vcc_lo, 0, 0x15000
	ds_read_b128 v[146:149], v131
	ds_read_b128 v[150:153], v131 offset:1024
	ds_read_b128 v[154:157], v131 offset:2048
	ds_read_b128 v[158:161], v131 offset:3072
	v_add_u32_e32 v131, vcc_lo, v166
	ds_read_b128 v[170:173], v131
	ds_read_b128 v[174:177], v131 offset:1024
	ds_read_b128 v[178:181], v131 offset:2048
	ds_read_b128 v[182:185], v131 offset:3072
	v_lshl_add_u64 v[162:163], s[50:51], 0, v[134:135]
	s_add_i32 m0, s33, 0xd000
	ds_read_b128 v[196:199], v167 offset:4096
	ds_read_b128 v[200:203], v167 offset:5120
	ds_read_b128 v[204:207], v167 offset:6144
	ds_read_b128 v[208:211], v167 offset:7168
	ds_read_b128 v[212:215], v167 offset:8192
	ds_read_b128 v[216:219], v167 offset:9216
	ds_read_b128 v[220:223], v167 offset:10240
	ds_read_b128 v[240:243], v167 offset:11264
	global_load_lds_dwordx4 v[162:163], off
	v_lshl_add_u64 v[162:163], s[50:51], 0, v[136:137]
	s_add_i32 m0, s33, 0xf000
	s_nop 0
	global_load_lds_dwordx4 v[162:163], off
	s_waitcnt vmcnt(8)
	s_waitcnt lgkmcnt(0)
	s_barrier
	s_setprio 1
	s_waitcnt lgkmcnt(0)
	v_mfma_f32_16x16x32_bf16 v[126:129], v[146:149], v[196:199], v[126:129]
	v_mfma_f32_16x16x32_bf16 v[122:125], v[154:157], v[196:199], v[122:125]
	v_mfma_f32_16x16x32_bf16 v[118:121], v[146:149], v[204:207], v[118:121]
	v_mfma_f32_16x16x32_bf16 v[114:117], v[154:157], v[204:207], v[114:117]
	v_mfma_f32_16x16x32_bf16 v[110:113], v[146:149], v[212:215], v[110:113]
	v_mfma_f32_16x16x32_bf16 v[106:109], v[154:157], v[212:215], v[106:109]
	v_mfma_f32_16x16x32_bf16 v[102:105], v[146:149], v[220:223], v[102:105]
	v_mfma_f32_16x16x32_bf16 v[98:101], v[154:157], v[220:223], v[98:101]
	v_mfma_f32_16x16x32_bf16 v[126:129], v[150:153], v[200:203], v[126:129]
	v_mfma_f32_16x16x32_bf16 v[122:125], v[158:161], v[200:203], v[122:125]
	v_mfma_f32_16x16x32_bf16 v[118:121], v[150:153], v[208:211], v[118:121]
	v_mfma_f32_16x16x32_bf16 v[114:117], v[158:161], v[208:211], v[114:117]
	v_mfma_f32_16x16x32_bf16 v[110:113], v[150:153], v[216:219], v[110:113]
	v_mfma_f32_16x16x32_bf16 v[106:109], v[158:161], v[216:219], v[106:109]
	v_mfma_f32_16x16x32_bf16 v[102:105], v[150:153], v[240:243], v[102:105]
	v_mfma_f32_16x16x32_bf16 v[98:101], v[158:161], v[240:243], v[98:101]
	s_setprio 0
	s_setprio 1
	v_mfma_f32_16x16x32_bf16 v[94:97], v[170:173], v[196:199], v[94:97]
	v_mfma_f32_16x16x32_bf16 v[90:93], v[178:181], v[196:199], v[90:93]
	v_mfma_f32_16x16x32_bf16 v[86:89], v[170:173], v[204:207], v[86:89]
	v_mfma_f32_16x16x32_bf16 v[82:85], v[178:181], v[204:207], v[82:85]
	v_mfma_f32_16x16x32_bf16 v[78:81], v[170:173], v[212:215], v[78:81]
	v_mfma_f32_16x16x32_bf16 v[74:77], v[178:181], v[212:215], v[74:77]
	v_mfma_f32_16x16x32_bf16 v[70:73], v[170:173], v[220:223], v[70:73]
	v_mfma_f32_16x16x32_bf16 v[66:69], v[178:181], v[220:223], v[66:69]
	v_mfma_f32_16x16x32_bf16 v[94:97], v[174:177], v[200:203], v[94:97]
	v_mfma_f32_16x16x32_bf16 v[90:93], v[182:185], v[200:203], v[90:93]
	v_mfma_f32_16x16x32_bf16 v[86:89], v[174:177], v[208:211], v[86:89]
	v_mfma_f32_16x16x32_bf16 v[82:85], v[182:185], v[208:211], v[82:85]
	v_mfma_f32_16x16x32_bf16 v[78:81], v[174:177], v[216:219], v[78:81]
	v_mfma_f32_16x16x32_bf16 v[74:77], v[182:185], v[216:219], v[74:77]
	v_mfma_f32_16x16x32_bf16 v[70:73], v[174:177], v[240:243], v[70:73]
	v_mfma_f32_16x16x32_bf16 v[66:69], v[182:185], v[240:243], v[66:69]
	s_setprio 0
	s_barrier
	s_add_i32 s75, s75, s13
	v_lshl_add_u64 v[192:193], s[0:1], 0, v[186:187]
	s_mov_b32 m0, s75
	global_load_lds_dwordx4 v186, s[0:1]
	v_lshl_add_u64 v[224:225], v[192:193], 0, s[58:59]
	s_add_i32 m0, s75, 0x2000
	s_add_i32 s0, vcc_lo, s13
	global_load_lds_dwordx4 v[224:225], off
	v_lshl_add_u64 v[244:245], v[224:225], 0, s[58:59]
	s_mov_b32 m0, s0
	v_lshl_add_u64 v[246:247], v[244:245], 0, s[58:59]
	global_load_lds_dwordx4 v[244:245], off
	s_add_i32 m0, s0, 0x2000
	v_lshl_add_u64 v[248:249], s[28:29], 0, v[144:145]
	global_load_lds_dwordx4 v[246:247], off
	s_mov_b32 m0, s16
	v_lshl_add_u64 v[250:251], v[248:249], 0, s[56:57]
	global_load_lds_dwordx4 v[248:249], off
	s_mov_b32 m0, s17
	s_nop 0
	global_load_lds_dwordx4 v[250:251], off
	ds_read_b128 v[196:199], v167 offset:20480
	ds_read_b128 v[200:203], v167 offset:21504
	ds_read_b128 v[204:207], v167 offset:22528
	ds_read_b128 v[208:211], v167 offset:23552
	ds_read_b128 v[212:215], v167 offset:24576
	ds_read_b128 v[216:219], v167 offset:25600
	ds_read_b128 v[220:223], v167 offset:26624
	ds_read_b128 v[240:243], v167 offset:27648
	s_waitcnt vmcnt(8)
	s_waitcnt lgkmcnt(0)
	s_barrier
	s_setprio 1
	s_waitcnt lgkmcnt(0)
	v_mfma_f32_16x16x32_bf16 v[62:65], v[146:149], v[196:199], v[62:65]
	v_mfma_f32_16x16x32_bf16 v[58:61], v[154:157], v[196:199], v[58:61]
	v_mfma_f32_16x16x32_bf16 v[54:57], v[146:149], v[204:207], v[54:57]
	v_mfma_f32_16x16x32_bf16 v[50:53], v[154:157], v[204:207], v[50:53]
	v_mfma_f32_16x16x32_bf16 v[46:49], v[146:149], v[212:215], v[46:49]
	v_mfma_f32_16x16x32_bf16 v[42:45], v[154:157], v[212:215], v[42:45]
	v_mfma_f32_16x16x32_bf16 v[38:41], v[146:149], v[220:223], v[38:41]
	v_mfma_f32_16x16x32_bf16 v[34:37], v[154:157], v[220:223], v[34:37]
	v_mfma_f32_16x16x32_bf16 v[62:65], v[150:153], v[200:203], v[62:65]
	v_mfma_f32_16x16x32_bf16 v[58:61], v[158:161], v[200:203], v[58:61]
	v_mfma_f32_16x16x32_bf16 v[54:57], v[150:153], v[208:211], v[54:57]
	v_mfma_f32_16x16x32_bf16 v[50:53], v[158:161], v[208:211], v[50:53]
	v_mfma_f32_16x16x32_bf16 v[46:49], v[150:153], v[216:219], v[46:49]
	v_mfma_f32_16x16x32_bf16 v[42:45], v[158:161], v[216:219], v[42:45]
	v_mfma_f32_16x16x32_bf16 v[38:41], v[150:153], v[240:243], v[38:41]
	v_mfma_f32_16x16x32_bf16 v[34:37], v[158:161], v[240:243], v[34:37]
	s_setprio 0
	s_setprio 1
	v_mfma_f32_16x16x32_bf16 v[30:33], v[170:173], v[196:199], v[30:33]
	v_mfma_f32_16x16x32_bf16 v[26:29], v[178:181], v[196:199], v[26:29]
	v_mfma_f32_16x16x32_bf16 v[22:25], v[170:173], v[204:207], v[22:25]
	v_mfma_f32_16x16x32_bf16 v[18:21], v[178:181], v[204:207], v[18:21]
	v_mfma_f32_16x16x32_bf16 v[14:17], v[170:173], v[212:215], v[14:17]
	v_mfma_f32_16x16x32_bf16 v[10:13], v[178:181], v[212:215], v[10:13]
	v_mfma_f32_16x16x32_bf16 v[6:9], v[170:173], v[220:223], v[6:9]
	v_mfma_f32_16x16x32_bf16 v[2:5], v[178:181], v[220:223], v[2:5]
	v_mfma_f32_16x16x32_bf16 v[30:33], v[174:177], v[200:203], v[30:33]
	v_mfma_f32_16x16x32_bf16 v[26:29], v[182:185], v[200:203], v[26:29]
	v_mfma_f32_16x16x32_bf16 v[22:25], v[174:177], v[208:211], v[22:25]
	v_mfma_f32_16x16x32_bf16 v[18:21], v[182:185], v[208:211], v[18:21]
	v_mfma_f32_16x16x32_bf16 v[14:17], v[174:177], v[216:219], v[14:17]
	v_mfma_f32_16x16x32_bf16 v[10:13], v[182:185], v[216:219], v[10:13]
	v_mfma_f32_16x16x32_bf16 v[6:9], v[174:177], v[240:243], v[6:9]
	v_mfma_f32_16x16x32_bf16 v[2:5], v[182:185], v[240:243], v[2:5]
	s_setprio 0
	s_barrier
	s_add_i32 s0, 0, 0x19000
	v_add_u32_e32 v131, s0, v166
	s_add_i32 s1, 0, 0x1d000
	ds_read_b128 v[144:147], v131
	ds_read_b128 v[148:151], v131 offset:1024
	ds_read_b128 v[152:155], v131 offset:2048
	ds_read_b128 v[156:159], v131 offset:3072
	v_add_u32_e32 v131, s1, v166
	ds_read_b128 v[160:163], v131
	ds_read_b128 v[170:173], v131 offset:1024
	ds_read_b128 v[174:177], v131 offset:2048
	ds_read_b128 v[178:181], v131 offset:3072
	s_mov_b32 m0, s54
	v_lshl_add_u64 v[240:241], v[248:249], 0, s[68:69]
	ds_read_b128 v[182:185], v167 offset:36864
	ds_read_b128 v[196:199], v167 offset:37888
	ds_read_b128 v[200:203], v167 offset:38912
	ds_read_b128 v[204:207], v167 offset:39936
	ds_read_b128 v[208:211], v167 offset:40960
	ds_read_b128 v[212:215], v167 offset:41984
	ds_read_b128 v[216:219], v167 offset:43008
	ds_read_b128 v[220:223], v167 offset:44032
	global_load_lds_dwordx4 v[240:241], off
	v_lshl_add_u64 v[240:241], v[248:249], 0, s[46:47]
	s_mov_b32 m0, s55
	s_nop 0
	global_load_lds_dwordx4 v[240:241], off
	s_waitcnt vmcnt(8)
	s_waitcnt lgkmcnt(0)
	s_barrier
	s_setprio 1
	s_waitcnt lgkmcnt(0)
	v_mfma_f32_16x16x32_bf16 v[126:129], v[144:147], v[182:185], v[126:129]
	v_mfma_f32_16x16x32_bf16 v[122:125], v[152:155], v[182:185], v[122:125]
	v_mfma_f32_16x16x32_bf16 v[118:121], v[144:147], v[200:203], v[118:121]
	v_mfma_f32_16x16x32_bf16 v[114:117], v[152:155], v[200:203], v[114:117]
	v_mfma_f32_16x16x32_bf16 v[110:113], v[144:147], v[208:211], v[110:113]
	v_mfma_f32_16x16x32_bf16 v[106:109], v[152:155], v[208:211], v[106:109]
	v_mfma_f32_16x16x32_bf16 v[102:105], v[144:147], v[216:219], v[102:105]
	v_mfma_f32_16x16x32_bf16 v[98:101], v[152:155], v[216:219], v[98:101]
	v_mfma_f32_16x16x32_bf16 v[126:129], v[148:151], v[196:199], v[126:129]
	v_mfma_f32_16x16x32_bf16 v[122:125], v[156:159], v[196:199], v[122:125]
	v_mfma_f32_16x16x32_bf16 v[118:121], v[148:151], v[204:207], v[118:121]
	v_mfma_f32_16x16x32_bf16 v[114:117], v[156:159], v[204:207], v[114:117]
	v_mfma_f32_16x16x32_bf16 v[110:113], v[148:151], v[212:215], v[110:113]
	v_mfma_f32_16x16x32_bf16 v[106:109], v[156:159], v[212:215], v[106:109]
	v_mfma_f32_16x16x32_bf16 v[102:105], v[148:151], v[220:223], v[102:105]
	v_mfma_f32_16x16x32_bf16 v[98:101], v[156:159], v[220:223], v[98:101]
	s_setprio 0
	s_setprio 1
	v_mfma_f32_16x16x32_bf16 v[94:97], v[160:163], v[182:185], v[94:97]
	v_mfma_f32_16x16x32_bf16 v[90:93], v[174:177], v[182:185], v[90:93]
	v_mfma_f32_16x16x32_bf16 v[86:89], v[160:163], v[200:203], v[86:89]
	v_mfma_f32_16x16x32_bf16 v[82:85], v[174:177], v[200:203], v[82:85]
	v_mfma_f32_16x16x32_bf16 v[78:81], v[160:163], v[208:211], v[78:81]
	v_mfma_f32_16x16x32_bf16 v[74:77], v[174:177], v[208:211], v[74:77]
	v_mfma_f32_16x16x32_bf16 v[70:73], v[160:163], v[216:219], v[70:73]
	v_mfma_f32_16x16x32_bf16 v[66:69], v[174:177], v[216:219], v[66:69]
	v_mfma_f32_16x16x32_bf16 v[94:97], v[170:173], v[196:199], v[94:97]
	v_mfma_f32_16x16x32_bf16 v[90:93], v[178:181], v[196:199], v[90:93]
	v_mfma_f32_16x16x32_bf16 v[86:89], v[170:173], v[204:207], v[86:89]
	v_mfma_f32_16x16x32_bf16 v[82:85], v[178:181], v[204:207], v[82:85]
	v_mfma_f32_16x16x32_bf16 v[78:81], v[170:173], v[212:215], v[78:81]
	v_mfma_f32_16x16x32_bf16 v[74:77], v[178:181], v[212:215], v[74:77]
	v_mfma_f32_16x16x32_bf16 v[70:73], v[170:173], v[220:223], v[70:73]
	v_mfma_f32_16x16x32_bf16 v[66:69], v[178:181], v[220:223], v[66:69]
	s_setprio 0
	s_barrier
	s_add_i32 s0, s0, s13
	v_lshl_add_u64 v[192:193], v[192:193], 0, s[92:93]
	s_mov_b32 m0, s0
	global_load_lds_dwordx4 v[192:193], off
	v_lshl_add_u64 v[192:193], v[224:225], 0, s[92:93]
	s_add_i32 m0, s0, 0x2000
	s_add_i32 s0, s1, s13
	global_load_lds_dwordx4 v[192:193], off
	v_lshl_add_u64 v[192:193], v[244:245], 0, s[92:93]
	s_mov_b32 m0, s0
	s_nop 0
	global_load_lds_dwordx4 v[192:193], off
	v_lshl_add_u64 v[192:193], v[246:247], 0, s[92:93]
	s_add_i32 m0, s0, 0x2000
	s_nop 0
	global_load_lds_dwordx4 v[192:193], off
	v_lshl_add_u64 v[192:193], v[248:249], 0, s[92:93]
	s_mov_b32 m0, s90
	s_nop 0
	global_load_lds_dwordx4 v[192:193], off
	v_lshl_add_u64 v[192:193], v[250:251], 0, s[92:93]
	s_mov_b32 m0, s91
	s_nop 0
	global_load_lds_dwordx4 v[192:193], off
	ds_read_b128 v[182:185], v167 offset:53248
	ds_read_b128 v[196:199], v167 offset:54272
	ds_read_b128 v[200:203], v167 offset:55296
	ds_read_b128 v[204:207], v167 offset:56320
	ds_read_b128 v[208:211], v167 offset:57344
	ds_read_b128 v[212:215], v167 offset:58368
	ds_read_b128 v[216:219], v167 offset:59392
	ds_read_b128 v[220:223], v167 offset:60416
	s_waitcnt vmcnt(8)
	s_waitcnt lgkmcnt(0)
	s_barrier
	s_setprio 1
	s_waitcnt lgkmcnt(0)
	v_mfma_f32_16x16x32_bf16 v[62:65], v[144:147], v[182:185], v[62:65]
	v_mfma_f32_16x16x32_bf16 v[58:61], v[152:155], v[182:185], v[58:61]
	v_mfma_f32_16x16x32_bf16 v[54:57], v[144:147], v[200:203], v[54:57]
	v_mfma_f32_16x16x32_bf16 v[50:53], v[152:155], v[200:203], v[50:53]
	v_mfma_f32_16x16x32_bf16 v[46:49], v[144:147], v[208:211], v[46:49]
	v_mfma_f32_16x16x32_bf16 v[42:45], v[152:155], v[208:211], v[42:45]
	v_mfma_f32_16x16x32_bf16 v[38:41], v[144:147], v[216:219], v[38:41]
	v_mfma_f32_16x16x32_bf16 v[34:37], v[152:155], v[216:219], v[34:37]
	v_mfma_f32_16x16x32_bf16 v[62:65], v[148:151], v[196:199], v[62:65]
	v_mfma_f32_16x16x32_bf16 v[58:61], v[156:159], v[196:199], v[58:61]
	v_mfma_f32_16x16x32_bf16 v[54:57], v[148:151], v[204:207], v[54:57]
	v_mfma_f32_16x16x32_bf16 v[50:53], v[156:159], v[204:207], v[50:53]
	v_mfma_f32_16x16x32_bf16 v[46:49], v[148:151], v[212:215], v[46:49]
	v_mfma_f32_16x16x32_bf16 v[42:45], v[156:159], v[212:215], v[42:45]
	v_mfma_f32_16x16x32_bf16 v[38:41], v[148:151], v[220:223], v[38:41]
	v_mfma_f32_16x16x32_bf16 v[34:37], v[156:159], v[220:223], v[34:37]
	s_setprio 0
	s_setprio 1
	v_mfma_f32_16x16x32_bf16 v[30:33], v[160:163], v[182:185], v[30:33]
	v_mfma_f32_16x16x32_bf16 v[26:29], v[174:177], v[182:185], v[26:29]
	v_mfma_f32_16x16x32_bf16 v[22:25], v[160:163], v[200:203], v[22:25]
	v_mfma_f32_16x16x32_bf16 v[18:21], v[174:177], v[200:203], v[18:21]
	v_mfma_f32_16x16x32_bf16 v[14:17], v[160:163], v[208:211], v[14:17]
	v_mfma_f32_16x16x32_bf16 v[10:13], v[174:177], v[208:211], v[10:13]
	v_mfma_f32_16x16x32_bf16 v[6:9], v[160:163], v[216:219], v[6:9]
	v_mfma_f32_16x16x32_bf16 v[2:5], v[174:177], v[216:219], v[2:5]
	v_mfma_f32_16x16x32_bf16 v[30:33], v[170:173], v[196:199], v[30:33]
	v_mfma_f32_16x16x32_bf16 v[26:29], v[178:181], v[196:199], v[26:29]
	v_mfma_f32_16x16x32_bf16 v[22:25], v[170:173], v[204:207], v[22:25]
	v_mfma_f32_16x16x32_bf16 v[18:21], v[178:181], v[204:207], v[18:21]
	v_mfma_f32_16x16x32_bf16 v[14:17], v[170:173], v[212:215], v[14:17]
	v_mfma_f32_16x16x32_bf16 v[10:13], v[178:181], v[212:215], v[10:13]
	v_mfma_f32_16x16x32_bf16 v[6:9], v[170:173], v[220:223], v[6:9]
	v_mfma_f32_16x16x32_bf16 v[2:5], v[178:181], v[220:223], v[2:5]
	s_setprio 0
	s_barrier
	s_add_u32 s48, s48, 0x100
	s_addc_u32 s49, s49, 0
	s_add_u32 s50, s50, 0x100
	s_addc_u32 s51, s51, 0
	s_cmp_ge_i32 s73, s35
	s_cbranch_scc1 .LBB0_899

.LBB0_1110:
	s_add_u32 s24, s54, 0x100
	v_lshl_add_u64 v[140:141], s[52:53], 0, v[138:139]
	s_addc_u32 s25, s55, 0
	s_mov_b32 s43, -2
	s_mov_b64 s[54:55], 0
	s_add_u32 s14, s52, s54
	s_addc_u32 s15, s53, s55
	s_add_u32 s45, s14, 0x100
	s_addc_u32 s73, s15, 0
	s_add_u32 s74, s24, s54
	s_addc_u32 s75, s25, s55
	s_cmpk_eq_i32 s54, 0x700
	s_cselect_b64 vcc, -1, 0
	s_and_b64 s[14:15], vcc, exec
	s_cselect_b32 s15, s47, s73
	s_cselect_b32 s14, s46, s45
	s_cselect_b32 s75, s49, s75
	s_cselect_b32 s74, s48, s74
	s_add_i32 s45, 0, 0x11000
	v_add_u32_e32 v131, s45, v1
	s_add_i32 s73, 0, 0x15000
	ds_read_b128 v[144:147], v131
	ds_read_b128 v[148:151], v131 offset:1024
	ds_read_b128 v[152:155], v131 offset:2048
	ds_read_b128 v[156:159], v131 offset:3072
	v_add_u32_e32 v131, s73, v1
	ds_read_b128 v[160:163], v131
	ds_read_b128 v[164:167], v131 offset:1024
	ds_read_b128 v[168:171], v131 offset:2048
	ds_read_b128 v[172:175], v131 offset:3072
	v_cndmask_b32_e32 v185, v139, v137, vcc
	v_cndmask_b32_e32 v184, v138, v136, vcc
	v_lshl_add_u64 v[192:193], v[140:141], 0, s[54:55]
	v_lshl_add_u64 v[220:221], v[192:193], 0, s[6:7]
	s_add_i32 m0, s29, 0xd000
	ds_read_b128 v[176:179], v142 offset:4096
	ds_read_b128 v[180:183], v142 offset:5120
	ds_read_b128 v[196:199], v142 offset:6144
	ds_read_b128 v[200:203], v142 offset:7168
	ds_read_b128 v[204:207], v142 offset:8192
	ds_read_b128 v[208:211], v142 offset:9216
	ds_read_b128 v[212:215], v142 offset:10240
	ds_read_b128 v[216:219], v142 offset:11264
	global_load_lds_dwordx4 v[220:221], off
	v_lshl_add_u64 v[192:193], v[192:193], 0, s[8:9]
	s_add_i32 m0, s29, 0xf000
	s_nop 0
	global_load_lds_dwordx4 v[192:193], off
	s_waitcnt vmcnt(8)
	s_waitcnt lgkmcnt(0)
	s_barrier
	s_setprio 1
	s_waitcnt lgkmcnt(0)
	v_mfma_f32_16x16x32_bf16 v[126:129], v[144:147], v[176:179], 0
	v_mfma_f32_16x16x32_bf16 v[122:125], v[152:155], v[176:179], 0
	v_mfma_f32_16x16x32_bf16 v[110:113], v[144:147], v[196:199], 0
	v_mfma_f32_16x16x32_bf16 v[106:109], v[152:155], v[196:199], 0
	v_mfma_f32_16x16x32_bf16 v[94:97], v[144:147], v[204:207], 0
	v_mfma_f32_16x16x32_bf16 v[90:93], v[152:155], v[204:207], 0
	v_mfma_f32_16x16x32_bf16 v[78:81], v[144:147], v[212:215], 0
	v_mfma_f32_16x16x32_bf16 v[74:77], v[152:155], v[212:215], 0
	v_mfma_f32_16x16x32_bf16 v[126:129], v[148:151], v[180:183], v[126:129]
	v_mfma_f32_16x16x32_bf16 v[122:125], v[156:159], v[180:183], v[122:125]
	v_mfma_f32_16x16x32_bf16 v[110:113], v[148:151], v[200:203], v[110:113]
	v_mfma_f32_16x16x32_bf16 v[106:109], v[156:159], v[200:203], v[106:109]
	v_mfma_f32_16x16x32_bf16 v[94:97], v[148:151], v[208:211], v[94:97]
	v_mfma_f32_16x16x32_bf16 v[90:93], v[156:159], v[208:211], v[90:93]
	v_mfma_f32_16x16x32_bf16 v[78:81], v[148:151], v[216:219], v[78:81]
	v_mfma_f32_16x16x32_bf16 v[74:77], v[156:159], v[216:219], v[74:77]
	s_setprio 0
	s_setprio 1
	v_mfma_f32_16x16x32_bf16 v[118:121], v[160:163], v[176:179], 0
	v_mfma_f32_16x16x32_bf16 v[114:117], v[168:171], v[176:179], 0
	v_mfma_f32_16x16x32_bf16 v[102:105], v[160:163], v[196:199], 0
	v_mfma_f32_16x16x32_bf16 v[98:101], v[168:171], v[196:199], 0
	v_mfma_f32_16x16x32_bf16 v[86:89], v[160:163], v[204:207], 0
	v_mfma_f32_16x16x32_bf16 v[82:85], v[168:171], v[204:207], 0
	v_mfma_f32_16x16x32_bf16 v[70:73], v[160:163], v[212:215], 0
	v_mfma_f32_16x16x32_bf16 v[66:69], v[168:171], v[212:215], 0
	v_mfma_f32_16x16x32_bf16 v[118:121], v[164:167], v[180:183], v[118:121]
	v_mfma_f32_16x16x32_bf16 v[114:117], v[172:175], v[180:183], v[114:117]
	v_mfma_f32_16x16x32_bf16 v[102:105], v[164:167], v[200:203], v[102:105]
	v_mfma_f32_16x16x32_bf16 v[98:101], v[172:175], v[200:203], v[98:101]
	v_mfma_f32_16x16x32_bf16 v[86:89], v[164:167], v[208:211], v[86:89]
	v_mfma_f32_16x16x32_bf16 v[82:85], v[172:175], v[208:211], v[82:85]
	v_mfma_f32_16x16x32_bf16 v[70:73], v[164:167], v[216:219], v[70:73]
	v_mfma_f32_16x16x32_bf16 v[66:69], v[172:175], v[216:219], v[66:69]
	s_setprio 0
	s_barrier
	s_add_i32 s45, s45, s2
	v_lshl_add_u64 v[192:193], s[74:75], 0, v[186:187]
	s_mov_b32 m0, s45
	global_load_lds_dwordx4 v186, s[74:75]
	v_lshl_add_u64 v[220:221], v[192:193], 0, s[82:83]
	s_add_i32 m0, s45, 0x2000
	s_add_i32 s45, s73, s2
	global_load_lds_dwordx4 v[220:221], off
	v_lshl_add_u64 v[220:221], v[192:193], 0, s[64:65]
	s_mov_b32 m0, s45
	v_lshl_add_u64 v[184:185], s[14:15], 0, v[184:185]
	global_load_lds_dwordx4 v[220:221], off
	v_lshl_add_u64 v[220:221], v[192:193], 0, s[86:87]
	s_add_i32 m0, s45, 0x2000
	s_nop 0
	global_load_lds_dwordx4 v[220:221], off
	s_mov_b32 m0, s33
	v_lshl_add_u64 v[220:221], v[184:185], 0, s[82:83]
	global_load_lds_dwordx4 v[184:185], off
	s_mov_b32 m0, s34
	s_nop 0
	global_load_lds_dwordx4 v[220:221], off
	ds_read_b128 v[176:179], v142 offset:20480
	ds_read_b128 v[180:183], v142 offset:21504
	ds_read_b128 v[196:199], v142 offset:22528
	ds_read_b128 v[200:203], v142 offset:23552
	ds_read_b128 v[204:207], v142 offset:24576
	ds_read_b128 v[208:211], v142 offset:25600
	ds_read_b128 v[212:215], v142 offset:26624
	ds_read_b128 v[216:219], v142 offset:27648
	s_waitcnt vmcnt(8)
	s_waitcnt lgkmcnt(0)
	s_barrier
	s_setprio 1
	s_waitcnt lgkmcnt(0)
	v_mfma_f32_16x16x32_bf16 v[62:65], v[144:147], v[176:179], 0
	v_mfma_f32_16x16x32_bf16 v[58:61], v[152:155], v[176:179], 0
	v_mfma_f32_16x16x32_bf16 v[46:49], v[144:147], v[196:199], 0
	v_mfma_f32_16x16x32_bf16 v[42:45], v[152:155], v[196:199], 0
	v_mfma_f32_16x16x32_bf16 v[30:33], v[144:147], v[204:207], 0
	v_mfma_f32_16x16x32_bf16 v[26:29], v[152:155], v[204:207], 0
	v_mfma_f32_16x16x32_bf16 v[14:17], v[144:147], v[212:215], 0
	v_mfma_f32_16x16x32_bf16 v[10:13], v[152:155], v[212:215], 0
	v_mfma_f32_16x16x32_bf16 v[62:65], v[148:151], v[180:183], v[62:65]
	v_mfma_f32_16x16x32_bf16 v[58:61], v[156:159], v[180:183], v[58:61]
	v_mfma_f32_16x16x32_bf16 v[46:49], v[148:151], v[200:203], v[46:49]
	v_mfma_f32_16x16x32_bf16 v[42:45], v[156:159], v[200:203], v[42:45]
	v_mfma_f32_16x16x32_bf16 v[30:33], v[148:151], v[208:211], v[30:33]
	v_mfma_f32_16x16x32_bf16 v[26:29], v[156:159], v[208:211], v[26:29]
	v_mfma_f32_16x16x32_bf16 v[14:17], v[148:151], v[216:219], v[14:17]
	v_mfma_f32_16x16x32_bf16 v[10:13], v[156:159], v[216:219], v[10:13]
	s_setprio 0
	s_setprio 1
	v_mfma_f32_16x16x32_bf16 v[54:57], v[160:163], v[176:179], 0
	v_mfma_f32_16x16x32_bf16 v[50:53], v[168:171], v[176:179], 0
	v_mfma_f32_16x16x32_bf16 v[38:41], v[160:163], v[196:199], 0
	v_mfma_f32_16x16x32_bf16 v[34:37], v[168:171], v[196:199], 0
	v_mfma_f32_16x16x32_bf16 v[22:25], v[160:163], v[204:207], 0
	v_mfma_f32_16x16x32_bf16 v[18:21], v[168:171], v[204:207], 0
	v_mfma_f32_16x16x32_bf16 v[6:9], v[160:163], v[212:215], 0
	v_mfma_f32_16x16x32_bf16 v[2:5], v[168:171], v[212:215], 0
	v_mfma_f32_16x16x32_bf16 v[54:57], v[164:167], v[180:183], v[54:57]
	v_mfma_f32_16x16x32_bf16 v[50:53], v[172:175], v[180:183], v[50:53]
	v_mfma_f32_16x16x32_bf16 v[38:41], v[164:167], v[200:203], v[38:41]
	v_mfma_f32_16x16x32_bf16 v[34:37], v[172:175], v[200:203], v[34:37]
	v_mfma_f32_16x16x32_bf16 v[22:25], v[164:167], v[208:211], v[22:25]
	v_mfma_f32_16x16x32_bf16 v[18:21], v[172:175], v[208:211], v[18:21]
	v_mfma_f32_16x16x32_bf16 v[6:9], v[164:167], v[216:219], v[6:9]
	v_mfma_f32_16x16x32_bf16 v[2:5], v[172:175], v[216:219], v[2:5]
	s_setprio 0
	s_barrier
	s_add_i32 s14, 0, 0x19000
	v_add_u32_e32 v131, s14, v1
	s_add_i32 s15, 0, 0x1d000
	ds_read_b128 v[144:147], v131
	ds_read_b128 v[148:151], v131 offset:1024
	ds_read_b128 v[152:155], v131 offset:2048
	ds_read_b128 v[156:159], v131 offset:3072
	v_add_u32_e32 v131, s15, v1
	ds_read_b128 v[160:163], v131
	ds_read_b128 v[164:167], v131 offset:1024
	ds_read_b128 v[168:171], v131 offset:2048
	ds_read_b128 v[172:175], v131 offset:3072
	s_mov_b32 m0, s35
	v_lshl_add_u64 v[220:221], v[184:185], 0, s[64:65]
	ds_read_b128 v[176:179], v142 offset:36864
	ds_read_b128 v[180:183], v142 offset:37888
	ds_read_b128 v[196:199], v142 offset:38912
	ds_read_b128 v[200:203], v142 offset:39936
	ds_read_b128 v[204:207], v142 offset:40960
	ds_read_b128 v[208:211], v142 offset:41984
	ds_read_b128 v[212:215], v142 offset:43008
	ds_read_b128 v[216:219], v142 offset:44032
	global_load_lds_dwordx4 v[220:221], off
	v_lshl_add_u64 v[220:221], v[184:185], 0, s[86:87]
	s_mov_b32 m0, s56
	s_nop 0
	global_load_lds_dwordx4 v[220:221], off
	s_waitcnt vmcnt(8)
	s_waitcnt lgkmcnt(0)
	s_barrier
	s_setprio 1
	s_waitcnt lgkmcnt(0)
	v_mfma_f32_16x16x32_bf16 v[126:129], v[144:147], v[176:179], v[126:129]
	v_mfma_f32_16x16x32_bf16 v[122:125], v[152:155], v[176:179], v[122:125]
	v_mfma_f32_16x16x32_bf16 v[110:113], v[144:147], v[196:199], v[110:113]
	v_mfma_f32_16x16x32_bf16 v[106:109], v[152:155], v[196:199], v[106:109]
	v_mfma_f32_16x16x32_bf16 v[94:97], v[144:147], v[204:207], v[94:97]
	v_mfma_f32_16x16x32_bf16 v[90:93], v[152:155], v[204:207], v[90:93]
	v_mfma_f32_16x16x32_bf16 v[78:81], v[144:147], v[212:215], v[78:81]
	v_mfma_f32_16x16x32_bf16 v[74:77], v[152:155], v[212:215], v[74:77]
	v_mfma_f32_16x16x32_bf16 v[126:129], v[148:151], v[180:183], v[126:129]
	v_mfma_f32_16x16x32_bf16 v[122:125], v[156:159], v[180:183], v[122:125]
	v_mfma_f32_16x16x32_bf16 v[110:113], v[148:151], v[200:203], v[110:113]
	v_mfma_f32_16x16x32_bf16 v[106:109], v[156:159], v[200:203], v[106:109]
	v_mfma_f32_16x16x32_bf16 v[94:97], v[148:151], v[208:211], v[94:97]
	v_mfma_f32_16x16x32_bf16 v[90:93], v[156:159], v[208:211], v[90:93]
	v_mfma_f32_16x16x32_bf16 v[78:81], v[148:151], v[216:219], v[78:81]
	v_mfma_f32_16x16x32_bf16 v[74:77], v[156:159], v[216:219], v[74:77]
	s_setprio 0
	s_setprio 1
	v_mfma_f32_16x16x32_bf16 v[118:121], v[160:163], v[176:179], v[118:121]
	v_mfma_f32_16x16x32_bf16 v[114:117], v[168:171], v[176:179], v[114:117]
	v_mfma_f32_16x16x32_bf16 v[102:105], v[160:163], v[196:199], v[102:105]
	v_mfma_f32_16x16x32_bf16 v[98:101], v[168:171], v[196:199], v[98:101]
	v_mfma_f32_16x16x32_bf16 v[86:89], v[160:163], v[204:207], v[86:89]
	v_mfma_f32_16x16x32_bf16 v[82:85], v[168:171], v[204:207], v[82:85]
	v_mfma_f32_16x16x32_bf16 v[70:73], v[160:163], v[212:215], v[70:73]
	v_mfma_f32_16x16x32_bf16 v[66:69], v[168:171], v[212:215], v[66:69]
	v_mfma_f32_16x16x32_bf16 v[118:121], v[164:167], v[180:183], v[118:121]
	v_mfma_f32_16x16x32_bf16 v[114:117], v[172:175], v[180:183], v[114:117]
	v_mfma_f32_16x16x32_bf16 v[102:105], v[164:167], v[200:203], v[102:105]
	v_mfma_f32_16x16x32_bf16 v[98:101], v[172:175], v[200:203], v[98:101]
	v_mfma_f32_16x16x32_bf16 v[86:89], v[164:167], v[208:211], v[86:89]
	v_mfma_f32_16x16x32_bf16 v[82:85], v[172:175], v[208:211], v[82:85]
	v_mfma_f32_16x16x32_bf16 v[70:73], v[164:167], v[216:219], v[70:73]
	v_mfma_f32_16x16x32_bf16 v[66:69], v[172:175], v[216:219], v[66:69]
	s_setprio 0
	s_barrier
	s_add_i32 s14, s14, s2
	v_lshl_add_u64 v[220:221], v[192:193], 0, s[92:93]
	s_mov_b32 m0, s14
	global_load_lds_dwordx4 v[220:221], off
	v_lshl_add_u64 v[220:221], v[192:193], 0, s[4:5]
	s_add_i32 m0, s14, 0x2000
	s_add_i32 s14, s15, s2
	global_load_lds_dwordx4 v[220:221], off
	v_lshl_add_u64 v[220:221], v[192:193], 0, s[6:7]
	s_mov_b32 m0, s14
	v_lshl_add_u64 v[192:193], v[192:193], 0, s[8:9]
	global_load_lds_dwordx4 v[220:221], off
	s_add_i32 m0, s14, 0x2000
	s_nop 0
	global_load_lds_dwordx4 v[192:193], off
	v_lshl_add_u64 v[192:193], v[184:185], 0, s[92:93]
	s_mov_b32 m0, s59
	v_lshl_add_u64 v[184:185], v[184:185], 0, s[4:5]
	global_load_lds_dwordx4 v[192:193], off
	s_mov_b32 m0, s60
	s_nop 0
	global_load_lds_dwordx4 v[184:185], off
	ds_read_b128 v[176:179], v142 offset:53248
	ds_read_b128 v[180:183], v142 offset:54272
	ds_read_b128 v[196:199], v142 offset:55296
	ds_read_b128 v[200:203], v142 offset:56320
	ds_read_b128 v[204:207], v142 offset:57344
	ds_read_b128 v[208:211], v142 offset:58368
	ds_read_b128 v[212:215], v142 offset:59392
	ds_read_b128 v[216:219], v142 offset:60416
	s_waitcnt vmcnt(8)
	s_waitcnt lgkmcnt(0)
	s_barrier
	s_setprio 1
	s_waitcnt lgkmcnt(0)
	v_mfma_f32_16x16x32_bf16 v[62:65], v[144:147], v[176:179], v[62:65]
	v_mfma_f32_16x16x32_bf16 v[58:61], v[152:155], v[176:179], v[58:61]
	v_mfma_f32_16x16x32_bf16 v[46:49], v[144:147], v[196:199], v[46:49]
	v_mfma_f32_16x16x32_bf16 v[42:45], v[152:155], v[196:199], v[42:45]
	v_mfma_f32_16x16x32_bf16 v[30:33], v[144:147], v[204:207], v[30:33]
	v_mfma_f32_16x16x32_bf16 v[26:29], v[152:155], v[204:207], v[26:29]
	v_mfma_f32_16x16x32_bf16 v[14:17], v[144:147], v[212:215], v[14:17]
	v_mfma_f32_16x16x32_bf16 v[10:13], v[152:155], v[212:215], v[10:13]
	v_mfma_f32_16x16x32_bf16 v[62:65], v[148:151], v[180:183], v[62:65]
	v_mfma_f32_16x16x32_bf16 v[58:61], v[156:159], v[180:183], v[58:61]
	v_mfma_f32_16x16x32_bf16 v[46:49], v[148:151], v[200:203], v[46:49]
	v_mfma_f32_16x16x32_bf16 v[42:45], v[156:159], v[200:203], v[42:45]
	v_mfma_f32_16x16x32_bf16 v[30:33], v[148:151], v[208:211], v[30:33]
	v_mfma_f32_16x16x32_bf16 v[26:29], v[156:159], v[208:211], v[26:29]
	v_mfma_f32_16x16x32_bf16 v[14:17], v[148:151], v[216:219], v[14:17]
	v_mfma_f32_16x16x32_bf16 v[10:13], v[156:159], v[216:219], v[10:13]
	s_setprio 0
	s_setprio 1
	v_mfma_f32_16x16x32_bf16 v[54:57], v[160:163], v[176:179], v[54:57]
	v_mfma_f32_16x16x32_bf16 v[50:53], v[168:171], v[176:179], v[50:53]
	v_mfma_f32_16x16x32_bf16 v[38:41], v[160:163], v[196:199], v[38:41]
	v_mfma_f32_16x16x32_bf16 v[34:37], v[168:171], v[196:199], v[34:37]
	v_mfma_f32_16x16x32_bf16 v[22:25], v[160:163], v[204:207], v[22:25]
	v_mfma_f32_16x16x32_bf16 v[18:21], v[168:171], v[204:207], v[18:21]
	v_mfma_f32_16x16x32_bf16 v[6:9], v[160:163], v[212:215], v[6:9]
	v_mfma_f32_16x16x32_bf16 v[2:5], v[168:171], v[212:215], v[2:5]
	v_mfma_f32_16x16x32_bf16 v[54:57], v[164:167], v[180:183], v[54:57]
	v_mfma_f32_16x16x32_bf16 v[50:53], v[172:175], v[180:183], v[50:53]
	v_mfma_f32_16x16x32_bf16 v[38:41], v[164:167], v[200:203], v[38:41]
	v_mfma_f32_16x16x32_bf16 v[34:37], v[172:175], v[200:203], v[34:37]
	v_mfma_f32_16x16x32_bf16 v[22:25], v[164:167], v[208:211], v[22:25]
	v_mfma_f32_16x16x32_bf16 v[18:21], v[172:175], v[208:211], v[18:21]
	v_mfma_f32_16x16x32_bf16 v[6:9], v[164:167], v[216:219], v[6:9]
	v_mfma_f32_16x16x32_bf16 v[2:5], v[172:175], v[216:219], v[2:5]
	s_setprio 0
	s_barrier
	s_add_i32 s43, s43, 2
	s_add_u32 s54, s54, 0x100
	s_addc_u32 s55, s55, 0
.LBB0_1111:
	s_add_u32 s14, s52, s54
	s_addc_u32 s15, s53, s55
	s_add_u32 s45, s14, 0x100
	s_addc_u32 s73, s15, 0
	s_add_u32 s74, s24, s54
	s_addc_u32 s75, s25, s55
	s_cmpk_eq_i32 s54, 0x700
	s_cselect_b64 vcc, -1, 0
	s_and_b64 s[14:15], vcc, exec
	s_cselect_b32 s15, s47, s73
	s_cselect_b32 s14, s46, s45
	s_cselect_b32 s75, s49, s75
	s_cselect_b32 s74, s48, s74
	s_add_i32 s45, 0, 0x11000
	v_add_u32_e32 v131, s45, v1
	s_add_i32 s73, 0, 0x15000
	ds_read_b128 v[144:147], v131
	ds_read_b128 v[148:151], v131 offset:1024
	ds_read_b128 v[152:155], v131 offset:2048
	ds_read_b128 v[156:159], v131 offset:3072
	v_add_u32_e32 v131, s73, v1
	ds_read_b128 v[160:163], v131
	ds_read_b128 v[164:167], v131 offset:1024
	ds_read_b128 v[168:171], v131 offset:2048
	ds_read_b128 v[172:175], v131 offset:3072
	v_cndmask_b32_e32 v185, v139, v137, vcc
	v_cndmask_b32_e32 v184, v138, v136, vcc
	v_lshl_add_u64 v[192:193], v[140:141], 0, s[54:55]
	v_lshl_add_u64 v[220:221], v[192:193], 0, s[6:7]
	s_add_i32 m0, s29, 0xd000
	ds_read_b128 v[176:179], v142 offset:4096
	ds_read_b128 v[180:183], v142 offset:5120
	ds_read_b128 v[196:199], v142 offset:6144
	ds_read_b128 v[200:203], v142 offset:7168
	ds_read_b128 v[204:207], v142 offset:8192
	ds_read_b128 v[208:211], v142 offset:9216
	ds_read_b128 v[212:215], v142 offset:10240
	ds_read_b128 v[216:219], v142 offset:11264
	global_load_lds_dwordx4 v[220:221], off
	v_lshl_add_u64 v[192:193], v[192:193], 0, s[8:9]
	s_add_i32 m0, s29, 0xf000
	s_nop 0
	global_load_lds_dwordx4 v[192:193], off
	s_waitcnt vmcnt(8)
	s_waitcnt lgkmcnt(0)
	s_barrier
	s_setprio 1
	s_waitcnt lgkmcnt(0)
	v_mfma_f32_16x16x32_bf16 v[126:129], v[144:147], v[176:179], v[126:129]
	v_mfma_f32_16x16x32_bf16 v[122:125], v[152:155], v[176:179], v[122:125]
	v_mfma_f32_16x16x32_bf16 v[110:113], v[144:147], v[196:199], v[110:113]
	v_mfma_f32_16x16x32_bf16 v[106:109], v[152:155], v[196:199], v[106:109]
	v_mfma_f32_16x16x32_bf16 v[94:97], v[144:147], v[204:207], v[94:97]
	v_mfma_f32_16x16x32_bf16 v[90:93], v[152:155], v[204:207], v[90:93]
	v_mfma_f32_16x16x32_bf16 v[78:81], v[144:147], v[212:215], v[78:81]
	v_mfma_f32_16x16x32_bf16 v[74:77], v[152:155], v[212:215], v[74:77]
	v_mfma_f32_16x16x32_bf16 v[126:129], v[148:151], v[180:183], v[126:129]
	v_mfma_f32_16x16x32_bf16 v[122:125], v[156:159], v[180:183], v[122:125]
	v_mfma_f32_16x16x32_bf16 v[110:113], v[148:151], v[200:203], v[110:113]
	v_mfma_f32_16x16x32_bf16 v[106:109], v[156:159], v[200:203], v[106:109]
	v_mfma_f32_16x16x32_bf16 v[94:97], v[148:151], v[208:211], v[94:97]
	v_mfma_f32_16x16x32_bf16 v[90:93], v[156:159], v[208:211], v[90:93]
	v_mfma_f32_16x16x32_bf16 v[78:81], v[148:151], v[216:219], v[78:81]
	v_mfma_f32_16x16x32_bf16 v[74:77], v[156:159], v[216:219], v[74:77]
	s_setprio 0
	s_setprio 1
	v_mfma_f32_16x16x32_bf16 v[118:121], v[160:163], v[176:179], v[118:121]
	v_mfma_f32_16x16x32_bf16 v[114:117], v[168:171], v[176:179], v[114:117]
	v_mfma_f32_16x16x32_bf16 v[102:105], v[160:163], v[196:199], v[102:105]
	v_mfma_f32_16x16x32_bf16 v[98:101], v[168:171], v[196:199], v[98:101]
	v_mfma_f32_16x16x32_bf16 v[86:89], v[160:163], v[204:207], v[86:89]
	v_mfma_f32_16x16x32_bf16 v[82:85], v[168:171], v[204:207], v[82:85]
	v_mfma_f32_16x16x32_bf16 v[70:73], v[160:163], v[212:215], v[70:73]
	v_mfma_f32_16x16x32_bf16 v[66:69], v[168:171], v[212:215], v[66:69]
	v_mfma_f32_16x16x32_bf16 v[118:121], v[164:167], v[180:183], v[118:121]
	v_mfma_f32_16x16x32_bf16 v[114:117], v[172:175], v[180:183], v[114:117]
	v_mfma_f32_16x16x32_bf16 v[102:105], v[164:167], v[200:203], v[102:105]
	v_mfma_f32_16x16x32_bf16 v[98:101], v[172:175], v[200:203], v[98:101]
	v_mfma_f32_16x16x32_bf16 v[86:89], v[164:167], v[208:211], v[86:89]
	v_mfma_f32_16x16x32_bf16 v[82:85], v[172:175], v[208:211], v[82:85]
	v_mfma_f32_16x16x32_bf16 v[70:73], v[164:167], v[216:219], v[70:73]
	v_mfma_f32_16x16x32_bf16 v[66:69], v[172:175], v[216:219], v[66:69]
	s_setprio 0
	s_barrier
	s_add_i32 s45, s45, s2
	v_lshl_add_u64 v[192:193], s[74:75], 0, v[186:187]
	s_mov_b32 m0, s45
	global_load_lds_dwordx4 v186, s[74:75]
	v_lshl_add_u64 v[220:221], v[192:193], 0, s[82:83]
	s_add_i32 m0, s45, 0x2000
	s_add_i32 s45, s73, s2
	global_load_lds_dwordx4 v[220:221], off
	v_lshl_add_u64 v[220:221], v[192:193], 0, s[64:65]
	s_mov_b32 m0, s45
	v_lshl_add_u64 v[184:185], s[14:15], 0, v[184:185]
	global_load_lds_dwordx4 v[220:221], off
	v_lshl_add_u64 v[220:221], v[192:193], 0, s[86:87]
	s_add_i32 m0, s45, 0x2000
	s_nop 0
	global_load_lds_dwordx4 v[220:221], off
	s_mov_b32 m0, s33
	v_lshl_add_u64 v[220:221], v[184:185], 0, s[82:83]
	global_load_lds_dwordx4 v[184:185], off
	s_mov_b32 m0, s34
	s_nop 0
	global_load_lds_dwordx4 v[220:221], off
	ds_read_b128 v[176:179], v142 offset:20480
	ds_read_b128 v[180:183], v142 offset:21504
	ds_read_b128 v[196:199], v142 offset:22528
	ds_read_b128 v[200:203], v142 offset:23552
	ds_read_b128 v[204:207], v142 offset:24576
	ds_read_b128 v[208:211], v142 offset:25600
	ds_read_b128 v[212:215], v142 offset:26624
	ds_read_b128 v[216:219], v142 offset:27648
	s_waitcnt vmcnt(8)
	s_waitcnt lgkmcnt(0)
	s_barrier
	s_setprio 1
	s_waitcnt lgkmcnt(0)
	v_mfma_f32_16x16x32_bf16 v[62:65], v[144:147], v[176:179], v[62:65]
	v_mfma_f32_16x16x32_bf16 v[58:61], v[152:155], v[176:179], v[58:61]
	v_mfma_f32_16x16x32_bf16 v[46:49], v[144:147], v[196:199], v[46:49]
	v_mfma_f32_16x16x32_bf16 v[42:45], v[152:155], v[196:199], v[42:45]
	v_mfma_f32_16x16x32_bf16 v[30:33], v[144:147], v[204:207], v[30:33]
	v_mfma_f32_16x16x32_bf16 v[26:29], v[152:155], v[204:207], v[26:29]
	v_mfma_f32_16x16x32_bf16 v[14:17], v[144:147], v[212:215], v[14:17]
	v_mfma_f32_16x16x32_bf16 v[10:13], v[152:155], v[212:215], v[10:13]
	v_mfma_f32_16x16x32_bf16 v[62:65], v[148:151], v[180:183], v[62:65]
	v_mfma_f32_16x16x32_bf16 v[58:61], v[156:159], v[180:183], v[58:61]
	v_mfma_f32_16x16x32_bf16 v[46:49], v[148:151], v[200:203], v[46:49]
	v_mfma_f32_16x16x32_bf16 v[42:45], v[156:159], v[200:203], v[42:45]
	v_mfma_f32_16x16x32_bf16 v[30:33], v[148:151], v[208:211], v[30:33]
	v_mfma_f32_16x16x32_bf16 v[26:29], v[156:159], v[208:211], v[26:29]
	v_mfma_f32_16x16x32_bf16 v[14:17], v[148:151], v[216:219], v[14:17]
	v_mfma_f32_16x16x32_bf16 v[10:13], v[156:159], v[216:219], v[10:13]
	s_setprio 0
	s_setprio 1
	v_mfma_f32_16x16x32_bf16 v[54:57], v[160:163], v[176:179], v[54:57]
	v_mfma_f32_16x16x32_bf16 v[50:53], v[168:171], v[176:179], v[50:53]
	v_mfma_f32_16x16x32_bf16 v[38:41], v[160:163], v[196:199], v[38:41]
	v_mfma_f32_16x16x32_bf16 v[34:37], v[168:171], v[196:199], v[34:37]
	v_mfma_f32_16x16x32_bf16 v[22:25], v[160:163], v[204:207], v[22:25]
	v_mfma_f32_16x16x32_bf16 v[18:21], v[168:171], v[204:207], v[18:21]
	v_mfma_f32_16x16x32_bf16 v[6:9], v[160:163], v[212:215], v[6:9]
	v_mfma_f32_16x16x32_bf16 v[2:5], v[168:171], v[212:215], v[2:5]
	v_mfma_f32_16x16x32_bf16 v[54:57], v[164:167], v[180:183], v[54:57]
	v_mfma_f32_16x16x32_bf16 v[50:53], v[172:175], v[180:183], v[50:53]
	v_mfma_f32_16x16x32_bf16 v[38:41], v[164:167], v[200:203], v[38:41]
	v_mfma_f32_16x16x32_bf16 v[34:37], v[172:175], v[200:203], v[34:37]
	v_mfma_f32_16x16x32_bf16 v[22:25], v[164:167], v[208:211], v[22:25]
	v_mfma_f32_16x16x32_bf16 v[18:21], v[172:175], v[208:211], v[18:21]
	v_mfma_f32_16x16x32_bf16 v[6:9], v[164:167], v[216:219], v[6:9]
	v_mfma_f32_16x16x32_bf16 v[2:5], v[172:175], v[216:219], v[2:5]
	s_setprio 0
	s_barrier
	s_add_i32 s14, 0, 0x19000
	v_add_u32_e32 v131, s14, v1
	s_add_i32 s15, 0, 0x1d000
	ds_read_b128 v[144:147], v131
	ds_read_b128 v[148:151], v131 offset:1024
	ds_read_b128 v[152:155], v131 offset:2048
	ds_read_b128 v[156:159], v131 offset:3072
	v_add_u32_e32 v131, s15, v1
	ds_read_b128 v[160:163], v131
	ds_read_b128 v[164:167], v131 offset:1024
	ds_read_b128 v[168:171], v131 offset:2048
	ds_read_b128 v[172:175], v131 offset:3072
	s_mov_b32 m0, s35
	v_lshl_add_u64 v[220:221], v[184:185], 0, s[64:65]
	ds_read_b128 v[176:179], v142 offset:36864
	ds_read_b128 v[180:183], v142 offset:37888
	ds_read_b128 v[196:199], v142 offset:38912
	ds_read_b128 v[200:203], v142 offset:39936
	ds_read_b128 v[204:207], v142 offset:40960
	ds_read_b128 v[208:211], v142 offset:41984
	ds_read_b128 v[212:215], v142 offset:43008
	ds_read_b128 v[216:219], v142 offset:44032
	global_load_lds_dwordx4 v[220:221], off
	v_lshl_add_u64 v[220:221], v[184:185], 0, s[86:87]
	s_mov_b32 m0, s56
	s_nop 0
	global_load_lds_dwordx4 v[220:221], off
	s_waitcnt vmcnt(8)
	s_waitcnt lgkmcnt(0)
	s_barrier
	s_setprio 1
	s_waitcnt lgkmcnt(0)
	v_mfma_f32_16x16x32_bf16 v[126:129], v[144:147], v[176:179], v[126:129]
	v_mfma_f32_16x16x32_bf16 v[122:125], v[152:155], v[176:179], v[122:125]
	v_mfma_f32_16x16x32_bf16 v[110:113], v[144:147], v[196:199], v[110:113]
	v_mfma_f32_16x16x32_bf16 v[106:109], v[152:155], v[196:199], v[106:109]
	v_mfma_f32_16x16x32_bf16 v[94:97], v[144:147], v[204:207], v[94:97]
	v_mfma_f32_16x16x32_bf16 v[90:93], v[152:155], v[204:207], v[90:93]
	v_mfma_f32_16x16x32_bf16 v[78:81], v[144:147], v[212:215], v[78:81]
	v_mfma_f32_16x16x32_bf16 v[74:77], v[152:155], v[212:215], v[74:77]
	v_mfma_f32_16x16x32_bf16 v[126:129], v[148:151], v[180:183], v[126:129]
	v_mfma_f32_16x16x32_bf16 v[122:125], v[156:159], v[180:183], v[122:125]
	v_mfma_f32_16x16x32_bf16 v[110:113], v[148:151], v[200:203], v[110:113]
	v_mfma_f32_16x16x32_bf16 v[106:109], v[156:159], v[200:203], v[106:109]
	v_mfma_f32_16x16x32_bf16 v[94:97], v[148:151], v[208:211], v[94:97]
	v_mfma_f32_16x16x32_bf16 v[90:93], v[156:159], v[208:211], v[90:93]
	v_mfma_f32_16x16x32_bf16 v[78:81], v[148:151], v[216:219], v[78:81]
	v_mfma_f32_16x16x32_bf16 v[74:77], v[156:159], v[216:219], v[74:77]
	s_setprio 0
	s_setprio 1
	v_mfma_f32_16x16x32_bf16 v[118:121], v[160:163], v[176:179], v[118:121]
	v_mfma_f32_16x16x32_bf16 v[114:117], v[168:171], v[176:179], v[114:117]
	v_mfma_f32_16x16x32_bf16 v[102:105], v[160:163], v[196:199], v[102:105]
	v_mfma_f32_16x16x32_bf16 v[98:101], v[168:171], v[196:199], v[98:101]
	v_mfma_f32_16x16x32_bf16 v[86:89], v[160:163], v[204:207], v[86:89]
	v_mfma_f32_16x16x32_bf16 v[82:85], v[168:171], v[204:207], v[82:85]
	v_mfma_f32_16x16x32_bf16 v[70:73], v[160:163], v[212:215], v[70:73]
	v_mfma_f32_16x16x32_bf16 v[66:69], v[168:171], v[212:215], v[66:69]
	v_mfma_f32_16x16x32_bf16 v[118:121], v[164:167], v[180:183], v[118:121]
	v_mfma_f32_16x16x32_bf16 v[114:117], v[172:175], v[180:183], v[114:117]
	v_mfma_f32_16x16x32_bf16 v[102:105], v[164:167], v[200:203], v[102:105]
	v_mfma_f32_16x16x32_bf16 v[98:101], v[172:175], v[200:203], v[98:101]
	v_mfma_f32_16x16x32_bf16 v[86:89], v[164:167], v[208:211], v[86:89]
	v_mfma_f32_16x16x32_bf16 v[82:85], v[172:175], v[208:211], v[82:85]
	v_mfma_f32_16x16x32_bf16 v[70:73], v[164:167], v[216:219], v[70:73]
	v_mfma_f32_16x16x32_bf16 v[66:69], v[172:175], v[216:219], v[66:69]
	s_setprio 0
	s_barrier
	s_add_i32 s14, s14, s2
	v_lshl_add_u64 v[220:221], v[192:193], 0, s[92:93]
	s_mov_b32 m0, s14
	global_load_lds_dwordx4 v[220:221], off
	v_lshl_add_u64 v[220:221], v[192:193], 0, s[4:5]
	s_add_i32 m0, s14, 0x2000
	s_add_i32 s14, s15, s2
	global_load_lds_dwordx4 v[220:221], off
	v_lshl_add_u64 v[220:221], v[192:193], 0, s[6:7]
	s_mov_b32 m0, s14
	v_lshl_add_u64 v[192:193], v[192:193], 0, s[8:9]
	global_load_lds_dwordx4 v[220:221], off
	s_add_i32 m0, s14, 0x2000
	s_nop 0
	global_load_lds_dwordx4 v[192:193], off
	v_lshl_add_u64 v[192:193], v[184:185], 0, s[92:93]
	s_mov_b32 m0, s59
	v_lshl_add_u64 v[184:185], v[184:185], 0, s[4:5]
	global_load_lds_dwordx4 v[192:193], off
	s_mov_b32 m0, s60
	s_nop 0
	global_load_lds_dwordx4 v[184:185], off
	ds_read_b128 v[176:179], v142 offset:53248
	ds_read_b128 v[180:183], v142 offset:54272
	ds_read_b128 v[196:199], v142 offset:55296
	ds_read_b128 v[200:203], v142 offset:56320
	ds_read_b128 v[204:207], v142 offset:57344
	ds_read_b128 v[208:211], v142 offset:58368
	ds_read_b128 v[212:215], v142 offset:59392
	ds_read_b128 v[216:219], v142 offset:60416
	s_waitcnt vmcnt(8)
	s_waitcnt lgkmcnt(0)
	s_barrier
	s_setprio 1
	s_waitcnt lgkmcnt(0)
	v_mfma_f32_16x16x32_bf16 v[62:65], v[144:147], v[176:179], v[62:65]
	v_mfma_f32_16x16x32_bf16 v[58:61], v[152:155], v[176:179], v[58:61]
	v_mfma_f32_16x16x32_bf16 v[46:49], v[144:147], v[196:199], v[46:49]
	v_mfma_f32_16x16x32_bf16 v[42:45], v[152:155], v[196:199], v[42:45]
	v_mfma_f32_16x16x32_bf16 v[30:33], v[144:147], v[204:207], v[30:33]
	v_mfma_f32_16x16x32_bf16 v[26:29], v[152:155], v[204:207], v[26:29]
	v_mfma_f32_16x16x32_bf16 v[14:17], v[144:147], v[212:215], v[14:17]
	v_mfma_f32_16x16x32_bf16 v[10:13], v[152:155], v[212:215], v[10:13]
	v_mfma_f32_16x16x32_bf16 v[62:65], v[148:151], v[180:183], v[62:65]
	v_mfma_f32_16x16x32_bf16 v[58:61], v[156:159], v[180:183], v[58:61]
	v_mfma_f32_16x16x32_bf16 v[46:49], v[148:151], v[200:203], v[46:49]
	v_mfma_f32_16x16x32_bf16 v[42:45], v[156:159], v[200:203], v[42:45]
	v_mfma_f32_16x16x32_bf16 v[30:33], v[148:151], v[208:211], v[30:33]
	v_mfma_f32_16x16x32_bf16 v[26:29], v[156:159], v[208:211], v[26:29]
	v_mfma_f32_16x16x32_bf16 v[14:17], v[148:151], v[216:219], v[14:17]
	v_mfma_f32_16x16x32_bf16 v[10:13], v[156:159], v[216:219], v[10:13]
	s_setprio 0
	s_setprio 1
	v_mfma_f32_16x16x32_bf16 v[54:57], v[160:163], v[176:179], v[54:57]
	v_mfma_f32_16x16x32_bf16 v[50:53], v[168:171], v[176:179], v[50:53]
	v_mfma_f32_16x16x32_bf16 v[38:41], v[160:163], v[196:199], v[38:41]
	v_mfma_f32_16x16x32_bf16 v[34:37], v[168:171], v[196:199], v[34:37]
	v_mfma_f32_16x16x32_bf16 v[22:25], v[160:163], v[204:207], v[22:25]
	v_mfma_f32_16x16x32_bf16 v[18:21], v[168:171], v[204:207], v[18:21]
	v_mfma_f32_16x16x32_bf16 v[6:9], v[160:163], v[212:215], v[6:9]
	v_mfma_f32_16x16x32_bf16 v[2:5], v[168:171], v[212:215], v[2:5]
	v_mfma_f32_16x16x32_bf16 v[54:57], v[164:167], v[180:183], v[54:57]
	v_mfma_f32_16x16x32_bf16 v[50:53], v[172:175], v[180:183], v[50:53]
	v_mfma_f32_16x16x32_bf16 v[38:41], v[164:167], v[200:203], v[38:41]
	v_mfma_f32_16x16x32_bf16 v[34:37], v[172:175], v[200:203], v[34:37]
	v_mfma_f32_16x16x32_bf16 v[22:25], v[164:167], v[208:211], v[22:25]
	v_mfma_f32_16x16x32_bf16 v[18:21], v[172:175], v[208:211], v[18:21]
	v_mfma_f32_16x16x32_bf16 v[6:9], v[164:167], v[216:219], v[6:9]
	v_mfma_f32_16x16x32_bf16 v[2:5], v[172:175], v[216:219], v[2:5]
	s_setprio 0
	s_barrier
	s_add_i32 s43, s43, 2
	s_add_u32 s54, s54, 0x100
	s_addc_u32 s55, s55, 0
	s_cmp_gt_u32 s43, 13
	s_cbranch_scc0 .LBB0_1111
	s_and_b64 vcc, exec, s[40:41]
	s_cbranch_vccz .LBB0_1114
	s_barrier

.LBB0_1338:
	s_add_u32 s1, s72, 0x100
	s_addc_u32 s2, s73, 0
	s_add_u32 s14, s70, 0x80
	v_mov_b32_e32 v59, v187
	v_mov_b32_e32 v65, v187
	s_addc_u32 s15, s71, 0
	v_lshl_add_u64 v[74:75], s[14:15], 0, v[64:65]
	v_lshl_add_u64 v[76:77], s[14:15], 0, v[58:59]
	s_mov_b32 s34, -2
	s_mov_b64 s[40:41], 0
	s_add_u32 s14, s70, s40
	s_addc_u32 s15, s71, s41
	s_add_u32 s35, s14, 0x100
	s_addc_u32 s55, s15, 0
	s_add_u32 s61, s1, s40
	s_addc_u32 s69, s2, s41
	s_cmpk_eq_i32 s40, 0x700
	s_cselect_b64 vcc, -1, 0
	s_and_b64 s[14:15], vcc, exec
	s_cselect_b32 s15, s59, s55
	s_cselect_b32 s14, s58, s35
	s_cselect_b32 s73, s57, s69
	s_cselect_b32 s72, s56, s61
	s_add_i32 s35, 0, 0x11000
	v_add_u32_e32 v63, s35, v165
	s_add_i32 s55, 0, 0x15000
	ds_read_b128 v[78:81], v63
	ds_read_b128 v[154:157], v63 offset:1024
	ds_read_b128 v[158:161], v63 offset:2048
	ds_read_b128 v[172:175], v63 offset:3072
	v_add_u32_e32 v63, s55, v165
	ds_read_b128 v[176:179], v63
	ds_read_b128 v[180:183], v63 offset:1024
	ds_read_b128 v[196:199], v63 offset:2048
	ds_read_b128 v[200:203], v63 offset:3072
	v_cndmask_b32_e32 v186, v62, v171, vcc
	v_cndmask_b32_e32 v184, v60, v170, vcc
	v_cndmask_b32_e32 v59, v58, v168, vcc
	v_cndmask_b32_e32 v61, v64, v169, vcc
	v_lshl_add_u64 v[192:193], v[76:77], 0, s[40:41]
	s_add_i32 m0, s24, 0xd000
	ds_read_b128 v[204:207], v166 offset:4096
	ds_read_b128 v[208:211], v166 offset:5120
	ds_read_b128 v[212:215], v166 offset:6144
	ds_read_b128 v[216:219], v166 offset:7168
	ds_read_b128 v[220:223], v166 offset:8192
	ds_read_b128 v[240:243], v166 offset:9216
	ds_read_b128 v[244:247], v166 offset:10240
	ds_read_b128 v[248:251], v166 offset:11264
	global_load_lds_dwordx4 v[192:193], off
	v_lshl_add_u64 v[192:193], v[74:75], 0, s[40:41]
	s_add_i32 m0, s24, 0xf000
	s_nop 0
	global_load_lds_dwordx4 v[192:193], off
	s_waitcnt vmcnt(8)
	s_waitcnt lgkmcnt(0)
	s_barrier
	s_setprio 1
	s_waitcnt lgkmcnt(0)
	v_mfma_f32_16x16x32_bf16 v[142:145], v[78:81], v[204:207], 0
	v_mfma_f32_16x16x32_bf16 v[134:137], v[158:161], v[204:207], 0
	v_mfma_f32_16x16x32_bf16 v[126:129], v[78:81], v[212:215], 0
	v_mfma_f32_16x16x32_bf16 v[118:121], v[158:161], v[212:215], 0
	v_mfma_f32_16x16x32_bf16 v[110:113], v[78:81], v[220:223], 0
	v_mfma_f32_16x16x32_bf16 v[102:105], v[158:161], v[220:223], 0
	v_mfma_f32_16x16x32_bf16 v[94:97], v[78:81], v[244:247], 0
	v_mfma_f32_16x16x32_bf16 v[86:89], v[158:161], v[244:247], 0
	v_mfma_f32_16x16x32_bf16 v[142:145], v[154:157], v[208:211], v[142:145]
	v_mfma_f32_16x16x32_bf16 v[134:137], v[172:175], v[208:211], v[134:137]
	v_mfma_f32_16x16x32_bf16 v[126:129], v[154:157], v[216:219], v[126:129]
	v_mfma_f32_16x16x32_bf16 v[118:121], v[172:175], v[216:219], v[118:121]
	v_mfma_f32_16x16x32_bf16 v[110:113], v[154:157], v[240:243], v[110:113]
	v_mfma_f32_16x16x32_bf16 v[102:105], v[172:175], v[240:243], v[102:105]
	v_mfma_f32_16x16x32_bf16 v[94:97], v[154:157], v[248:251], v[94:97]
	v_mfma_f32_16x16x32_bf16 v[86:89], v[172:175], v[248:251], v[86:89]
	s_setprio 0
	s_setprio 1
	v_mfma_f32_16x16x32_bf16 v[138:141], v[176:179], v[204:207], 0
	v_mfma_f32_16x16x32_bf16 v[130:133], v[196:199], v[204:207], 0
	v_mfma_f32_16x16x32_bf16 v[122:125], v[176:179], v[212:215], 0
	v_mfma_f32_16x16x32_bf16 v[114:117], v[196:199], v[212:215], 0
	v_mfma_f32_16x16x32_bf16 v[106:109], v[176:179], v[220:223], 0
	v_mfma_f32_16x16x32_bf16 v[98:101], v[196:199], v[220:223], 0
	v_mfma_f32_16x16x32_bf16 v[90:93], v[176:179], v[244:247], 0
	v_mfma_f32_16x16x32_bf16 v[82:85], v[196:199], v[244:247], 0
	v_mfma_f32_16x16x32_bf16 v[138:141], v[180:183], v[208:211], v[138:141]
	v_mfma_f32_16x16x32_bf16 v[130:133], v[200:203], v[208:211], v[130:133]
	v_mfma_f32_16x16x32_bf16 v[122:125], v[180:183], v[216:219], v[122:125]
	v_mfma_f32_16x16x32_bf16 v[114:117], v[200:203], v[216:219], v[114:117]
	v_mfma_f32_16x16x32_bf16 v[106:109], v[180:183], v[240:243], v[106:109]
	v_mfma_f32_16x16x32_bf16 v[98:101], v[200:203], v[240:243], v[98:101]
	v_mfma_f32_16x16x32_bf16 v[90:93], v[180:183], v[248:251], v[90:93]
	v_mfma_f32_16x16x32_bf16 v[82:85], v[200:203], v[248:251], v[82:85]
	s_setprio 0
	s_barrier
	s_add_i32 s35, s35, s17
	v_lshl_add_u64 v[192:193], s[72:73], 0, v[148:149]
	s_mov_b32 m0, s35
	global_load_lds_dwordx4 v[192:193], off
	v_lshl_add_u64 v[224:225], v[192:193], 0, s[82:83]
	s_add_i32 m0, s35, 0x2000
	s_add_i32 s35, s55, s17
	global_load_lds_dwordx4 v[224:225], off
	v_lshl_add_u64 v[224:225], v[192:193], 0, s[64:65]
	s_mov_b32 m0, s35
	v_mov_b32_e32 v185, v187
	global_load_lds_dwordx4 v[224:225], off
	v_lshl_add_u64 v[224:225], v[192:193], 0, s[86:87]
	s_add_i32 m0, s35, 0x2000
	s_nop 0
	global_load_lds_dwordx4 v[224:225], off
	s_mov_b32 m0, s25
	v_lshl_add_u64 v[224:225], s[14:15], 0, v[186:187]
	global_load_lds_dwordx4 v186, s[14:15]
	s_mov_b32 m0, s28
	s_nop 0
	global_load_lds_dwordx4 v184, s[14:15]
	ds_read_b128 v[204:207], v166 offset:20480
	ds_read_b128 v[208:211], v166 offset:21504
	ds_read_b128 v[212:215], v166 offset:22528
	ds_read_b128 v[216:219], v166 offset:23552
	ds_read_b128 v[220:223], v166 offset:24576
	ds_read_b128 v[240:243], v166 offset:25600
	ds_read_b128 v[244:247], v166 offset:26624
	ds_read_b128 v[248:251], v166 offset:27648
	s_waitcnt vmcnt(8)
	s_waitcnt lgkmcnt(0)
	v_lshl_add_u64 v[184:185], s[14:15], 0, v[184:185]
	s_barrier
	s_cmp_lg_u64 s[38:39], 0
	s_cbranch_scc1 .Lup_tokskip
	v_lshlrev_b32_e32 v2, 10, v2
	v_lshlrev_b32_e32 v3, 10, v3
	v_lshlrev_b32_e32 v5, 10, v5
	v_lshlrev_b32_e32 v4, 10, v4
	v_add_lshl_u32 v168, v5, v164, 1
	v_add_lshl_u32 v170, v3, v164, 1
	v_add_lshl_u32 v171, v2, v164, 1
	v_add_lshl_u32 v169, v4, v164, 1
.Lup_tokskip:
	s_setprio 1
	s_waitcnt lgkmcnt(0)
	v_mfma_f32_16x16x32_bf16 v[70:73], v[78:81], v[204:207], 0
	v_mfma_f32_16x16x32_bf16 v[54:57], v[158:161], v[204:207], 0
	v_mfma_f32_16x16x32_bf16 v[46:49], v[78:81], v[212:215], 0
	v_mfma_f32_16x16x32_bf16 v[38:41], v[158:161], v[212:215], 0
	v_mfma_f32_16x16x32_bf16 v[30:33], v[78:81], v[220:223], 0
	v_mfma_f32_16x16x32_bf16 v[22:25], v[158:161], v[220:223], 0
	v_mfma_f32_16x16x32_bf16 v[14:17], v[78:81], v[244:247], 0
	v_mfma_f32_16x16x32_bf16 v[6:9], v[158:161], v[244:247], 0
	v_mfma_f32_16x16x32_bf16 v[70:73], v[154:157], v[208:211], v[70:73]
	v_mfma_f32_16x16x32_bf16 v[54:57], v[172:175], v[208:211], v[54:57]
	v_mfma_f32_16x16x32_bf16 v[46:49], v[154:157], v[216:219], v[46:49]
	v_mfma_f32_16x16x32_bf16 v[38:41], v[172:175], v[216:219], v[38:41]
	v_mfma_f32_16x16x32_bf16 v[30:33], v[154:157], v[240:243], v[30:33]
	v_mfma_f32_16x16x32_bf16 v[22:25], v[172:175], v[240:243], v[22:25]
	v_mfma_f32_16x16x32_bf16 v[14:17], v[154:157], v[248:251], v[14:17]
	v_mfma_f32_16x16x32_bf16 v[6:9], v[172:175], v[248:251], v[6:9]
	s_setprio 0
	s_setprio 1
	v_mfma_f32_16x16x32_bf16 v[66:69], v[176:179], v[204:207], 0
	v_mfma_f32_16x16x32_bf16 v[50:53], v[196:199], v[204:207], 0
	v_mfma_f32_16x16x32_bf16 v[42:45], v[176:179], v[212:215], 0
	v_mfma_f32_16x16x32_bf16 v[34:37], v[196:199], v[212:215], 0
	v_mfma_f32_16x16x32_bf16 v[26:29], v[176:179], v[220:223], 0
	v_mfma_f32_16x16x32_bf16 v[18:21], v[196:199], v[220:223], 0
	v_mfma_f32_16x16x32_bf16 v[10:13], v[176:179], v[244:247], 0
	v_mfma_f32_16x16x32_bf16 v[2:5], v[196:199], v[244:247], 0
	v_mfma_f32_16x16x32_bf16 v[66:69], v[180:183], v[208:211], v[66:69]
	v_mfma_f32_16x16x32_bf16 v[50:53], v[200:203], v[208:211], v[50:53]
	v_mfma_f32_16x16x32_bf16 v[42:45], v[180:183], v[216:219], v[42:45]
	v_mfma_f32_16x16x32_bf16 v[34:37], v[200:203], v[216:219], v[34:37]
	v_mfma_f32_16x16x32_bf16 v[26:29], v[180:183], v[240:243], v[26:29]
	v_mfma_f32_16x16x32_bf16 v[18:21], v[200:203], v[240:243], v[18:21]
	v_mfma_f32_16x16x32_bf16 v[10:13], v[180:183], v[248:251], v[10:13]
	v_mfma_f32_16x16x32_bf16 v[2:5], v[200:203], v[248:251], v[2:5]
	s_setprio 0
	s_barrier
	s_add_i32 s35, 0, 0x19000
	v_add_u32_e32 v63, s35, v165
	s_add_i32 s55, 0, 0x1d000
	ds_read_b128 v[78:81], v63
	ds_read_b128 v[154:157], v63 offset:1024
	ds_read_b128 v[158:161], v63 offset:2048
	ds_read_b128 v[172:175], v63 offset:3072
	v_add_u32_e32 v63, s55, v165
	ds_read_b128 v[176:179], v63
	ds_read_b128 v[180:183], v63 offset:1024
	ds_read_b128 v[196:199], v63 offset:2048
	ds_read_b128 v[200:203], v63 offset:3072
	s_mov_b32 m0, s29
	ds_read_b128 v[204:207], v166 offset:36864
	ds_read_b128 v[208:211], v166 offset:37888
	ds_read_b128 v[212:215], v166 offset:38912
	ds_read_b128 v[216:219], v166 offset:39936
	ds_read_b128 v[220:223], v166 offset:40960
	ds_read_b128 v[240:243], v166 offset:41984
	ds_read_b128 v[244:247], v166 offset:43008
	ds_read_b128 v[248:251], v166 offset:44032
	global_load_lds_dwordx4 v59, s[14:15]
	s_mov_b32 m0, s33
	s_nop 0
	global_load_lds_dwordx4 v61, s[14:15]
	s_waitcnt vmcnt(8)
	s_waitcnt lgkmcnt(0)
	s_barrier
	s_setprio 1
	s_waitcnt lgkmcnt(0)
	v_mfma_f32_16x16x32_bf16 v[142:145], v[78:81], v[204:207], v[142:145]
	v_mfma_f32_16x16x32_bf16 v[134:137], v[158:161], v[204:207], v[134:137]
	v_mfma_f32_16x16x32_bf16 v[126:129], v[78:81], v[212:215], v[126:129]
	v_mfma_f32_16x16x32_bf16 v[118:121], v[158:161], v[212:215], v[118:121]
	v_mfma_f32_16x16x32_bf16 v[110:113], v[78:81], v[220:223], v[110:113]
	v_mfma_f32_16x16x32_bf16 v[102:105], v[158:161], v[220:223], v[102:105]
	v_mfma_f32_16x16x32_bf16 v[94:97], v[78:81], v[244:247], v[94:97]
	v_mfma_f32_16x16x32_bf16 v[86:89], v[158:161], v[244:247], v[86:89]
	v_mfma_f32_16x16x32_bf16 v[142:145], v[154:157], v[208:211], v[142:145]
	v_mfma_f32_16x16x32_bf16 v[134:137], v[172:175], v[208:211], v[134:137]
	v_mfma_f32_16x16x32_bf16 v[126:129], v[154:157], v[216:219], v[126:129]
	v_mfma_f32_16x16x32_bf16 v[118:121], v[172:175], v[216:219], v[118:121]
	v_mfma_f32_16x16x32_bf16 v[110:113], v[154:157], v[240:243], v[110:113]
	v_mfma_f32_16x16x32_bf16 v[102:105], v[172:175], v[240:243], v[102:105]
	v_mfma_f32_16x16x32_bf16 v[94:97], v[154:157], v[248:251], v[94:97]
	v_mfma_f32_16x16x32_bf16 v[86:89], v[172:175], v[248:251], v[86:89]
	s_setprio 0
	s_setprio 1
	v_mfma_f32_16x16x32_bf16 v[138:141], v[176:179], v[204:207], v[138:141]
	v_mfma_f32_16x16x32_bf16 v[130:133], v[196:199], v[204:207], v[130:133]
	v_mfma_f32_16x16x32_bf16 v[122:125], v[176:179], v[212:215], v[122:125]
	v_mfma_f32_16x16x32_bf16 v[114:117], v[196:199], v[212:215], v[114:117]
	v_mfma_f32_16x16x32_bf16 v[106:109], v[176:179], v[220:223], v[106:109]
	v_mfma_f32_16x16x32_bf16 v[98:101], v[196:199], v[220:223], v[98:101]
	v_mfma_f32_16x16x32_bf16 v[90:93], v[176:179], v[244:247], v[90:93]
	v_mfma_f32_16x16x32_bf16 v[82:85], v[196:199], v[244:247], v[82:85]
	v_mfma_f32_16x16x32_bf16 v[138:141], v[180:183], v[208:211], v[138:141]
	v_mfma_f32_16x16x32_bf16 v[130:133], v[200:203], v[208:211], v[130:133]
	v_mfma_f32_16x16x32_bf16 v[122:125], v[180:183], v[216:219], v[122:125]
	v_mfma_f32_16x16x32_bf16 v[114:117], v[200:203], v[216:219], v[114:117]
	v_mfma_f32_16x16x32_bf16 v[106:109], v[180:183], v[240:243], v[106:109]
	v_mfma_f32_16x16x32_bf16 v[98:101], v[200:203], v[240:243], v[98:101]
	v_mfma_f32_16x16x32_bf16 v[90:93], v[180:183], v[248:251], v[90:93]
	v_mfma_f32_16x16x32_bf16 v[82:85], v[200:203], v[248:251], v[82:85]
	s_setprio 0
	s_barrier
	s_add_i32 s14, s35, s17
	v_lshl_add_u64 v[230:231], v[192:193], 0, s[92:93]
	s_mov_b32 m0, s14
	global_load_lds_dwordx4 v[230:231], off
	v_lshl_add_u64 v[230:231], v[192:193], 0, s[4:5]
	s_add_i32 m0, s14, 0x2000
	s_add_i32 s14, s55, s17
	global_load_lds_dwordx4 v[230:231], off
	v_lshl_add_u64 v[230:231], v[192:193], 0, s[6:7]
	s_mov_b32 m0, s14
	v_lshl_add_u64 v[192:193], v[192:193], 0, s[8:9]
	global_load_lds_dwordx4 v[230:231], off
	s_add_i32 m0, s14, 0x2000
	v_lshl_add_u64 v[184:185], v[184:185], 0, s[92:93]
	global_load_lds_dwordx4 v[192:193], off
	v_lshl_add_u64 v[192:193], v[224:225], 0, s[92:93]
	s_mov_b32 m0, s80
	s_nop 0
	global_load_lds_dwordx4 v[192:193], off
	s_mov_b32 m0, s81
	s_nop 0
	global_load_lds_dwordx4 v[184:185], off
	ds_read_b128 v[204:207], v166 offset:53248
	ds_read_b128 v[208:211], v166 offset:54272
	ds_read_b128 v[212:215], v166 offset:55296
	ds_read_b128 v[216:219], v166 offset:56320
	ds_read_b128 v[220:223], v166 offset:57344
	ds_read_b128 v[240:243], v166 offset:58368
	ds_read_b128 v[244:247], v166 offset:59392
	ds_read_b128 v[248:251], v166 offset:60416
	s_waitcnt vmcnt(8)
	s_waitcnt lgkmcnt(0)
	s_barrier
	s_setprio 1
	s_waitcnt lgkmcnt(0)
	v_mfma_f32_16x16x32_bf16 v[70:73], v[78:81], v[204:207], v[70:73]
	v_mfma_f32_16x16x32_bf16 v[54:57], v[158:161], v[204:207], v[54:57]
	v_mfma_f32_16x16x32_bf16 v[46:49], v[78:81], v[212:215], v[46:49]
	v_mfma_f32_16x16x32_bf16 v[38:41], v[158:161], v[212:215], v[38:41]
	v_mfma_f32_16x16x32_bf16 v[30:33], v[78:81], v[220:223], v[30:33]
	v_mfma_f32_16x16x32_bf16 v[22:25], v[158:161], v[220:223], v[22:25]
	v_mfma_f32_16x16x32_bf16 v[14:17], v[78:81], v[244:247], v[14:17]
	v_mfma_f32_16x16x32_bf16 v[6:9], v[158:161], v[244:247], v[6:9]
	v_mfma_f32_16x16x32_bf16 v[70:73], v[154:157], v[208:211], v[70:73]
	v_mfma_f32_16x16x32_bf16 v[54:57], v[172:175], v[208:211], v[54:57]
	v_mfma_f32_16x16x32_bf16 v[46:49], v[154:157], v[216:219], v[46:49]
	v_mfma_f32_16x16x32_bf16 v[38:41], v[172:175], v[216:219], v[38:41]
	v_mfma_f32_16x16x32_bf16 v[30:33], v[154:157], v[240:243], v[30:33]
	v_mfma_f32_16x16x32_bf16 v[22:25], v[172:175], v[240:243], v[22:25]
	v_mfma_f32_16x16x32_bf16 v[14:17], v[154:157], v[248:251], v[14:17]
	v_mfma_f32_16x16x32_bf16 v[6:9], v[172:175], v[248:251], v[6:9]
	s_setprio 0
	s_setprio 1
	v_mfma_f32_16x16x32_bf16 v[66:69], v[176:179], v[204:207], v[66:69]
	v_mfma_f32_16x16x32_bf16 v[50:53], v[196:199], v[204:207], v[50:53]
	v_mfma_f32_16x16x32_bf16 v[42:45], v[176:179], v[212:215], v[42:45]
	v_mfma_f32_16x16x32_bf16 v[34:37], v[196:199], v[212:215], v[34:37]
	v_mfma_f32_16x16x32_bf16 v[26:29], v[176:179], v[220:223], v[26:29]
	v_mfma_f32_16x16x32_bf16 v[18:21], v[196:199], v[220:223], v[18:21]
	v_mfma_f32_16x16x32_bf16 v[10:13], v[176:179], v[244:247], v[10:13]
	v_mfma_f32_16x16x32_bf16 v[2:5], v[196:199], v[244:247], v[2:5]
	v_mfma_f32_16x16x32_bf16 v[66:69], v[180:183], v[208:211], v[66:69]
	v_mfma_f32_16x16x32_bf16 v[50:53], v[200:203], v[208:211], v[50:53]
	v_mfma_f32_16x16x32_bf16 v[42:45], v[180:183], v[216:219], v[42:45]
	v_mfma_f32_16x16x32_bf16 v[34:37], v[200:203], v[216:219], v[34:37]
	v_mfma_f32_16x16x32_bf16 v[26:29], v[180:183], v[240:243], v[26:29]
	v_mfma_f32_16x16x32_bf16 v[18:21], v[200:203], v[240:243], v[18:21]
	v_mfma_f32_16x16x32_bf16 v[10:13], v[180:183], v[248:251], v[10:13]
	v_mfma_f32_16x16x32_bf16 v[2:5], v[200:203], v[248:251], v[2:5]
	s_setprio 0
	s_barrier
	s_add_i32 s34, s34, 2
	s_add_u32 s40, s40, 0x100
	s_addc_u32 s41, s41, 0
.LBB0_1339:
	s_add_u32 s14, s70, s40
	s_addc_u32 s15, s71, s41
	s_add_u32 s35, s14, 0x100
	s_addc_u32 s55, s15, 0
	s_add_u32 s61, s1, s40
	s_addc_u32 s69, s2, s41
	s_cmpk_eq_i32 s40, 0x700
	s_cselect_b64 vcc, -1, 0
	s_and_b64 s[14:15], vcc, exec
	s_cselect_b32 s15, s59, s55
	s_cselect_b32 s14, s58, s35
	s_cselect_b32 s73, s57, s69
	s_cselect_b32 s72, s56, s61
	s_add_i32 s35, 0, 0x11000
	v_add_u32_e32 v63, s35, v165
	s_add_i32 s55, 0, 0x15000
	ds_read_b128 v[78:81], v63
	ds_read_b128 v[154:157], v63 offset:1024
	ds_read_b128 v[158:161], v63 offset:2048
	ds_read_b128 v[172:175], v63 offset:3072
	v_add_u32_e32 v63, s55, v165
	ds_read_b128 v[176:179], v63
	ds_read_b128 v[180:183], v63 offset:1024
	ds_read_b128 v[196:199], v63 offset:2048
	ds_read_b128 v[200:203], v63 offset:3072
	v_cndmask_b32_e32 v186, v62, v171, vcc
	v_cndmask_b32_e32 v184, v60, v170, vcc
	v_cndmask_b32_e32 v59, v58, v168, vcc
	v_cndmask_b32_e32 v61, v64, v169, vcc
	v_lshl_add_u64 v[192:193], v[76:77], 0, s[40:41]
	s_add_i32 m0, s24, 0xd000
	ds_read_b128 v[204:207], v166 offset:4096
	ds_read_b128 v[208:211], v166 offset:5120
	ds_read_b128 v[212:215], v166 offset:6144
	ds_read_b128 v[216:219], v166 offset:7168
	ds_read_b128 v[220:223], v166 offset:8192
	ds_read_b128 v[240:243], v166 offset:9216
	ds_read_b128 v[244:247], v166 offset:10240
	ds_read_b128 v[248:251], v166 offset:11264
	global_load_lds_dwordx4 v[192:193], off
	v_lshl_add_u64 v[192:193], v[74:75], 0, s[40:41]
	s_add_i32 m0, s24, 0xf000
	s_nop 0
	global_load_lds_dwordx4 v[192:193], off
	s_waitcnt vmcnt(8)
	s_waitcnt lgkmcnt(0)
	s_barrier
	s_setprio 1
	s_waitcnt lgkmcnt(0)
	v_mfma_f32_16x16x32_bf16 v[142:145], v[78:81], v[204:207], v[142:145]
	v_mfma_f32_16x16x32_bf16 v[134:137], v[158:161], v[204:207], v[134:137]
	v_mfma_f32_16x16x32_bf16 v[126:129], v[78:81], v[212:215], v[126:129]
	v_mfma_f32_16x16x32_bf16 v[118:121], v[158:161], v[212:215], v[118:121]
	v_mfma_f32_16x16x32_bf16 v[110:113], v[78:81], v[220:223], v[110:113]
	v_mfma_f32_16x16x32_bf16 v[102:105], v[158:161], v[220:223], v[102:105]
	v_mfma_f32_16x16x32_bf16 v[94:97], v[78:81], v[244:247], v[94:97]
	v_mfma_f32_16x16x32_bf16 v[86:89], v[158:161], v[244:247], v[86:89]
	v_mfma_f32_16x16x32_bf16 v[142:145], v[154:157], v[208:211], v[142:145]
	v_mfma_f32_16x16x32_bf16 v[134:137], v[172:175], v[208:211], v[134:137]
	v_mfma_f32_16x16x32_bf16 v[126:129], v[154:157], v[216:219], v[126:129]
	v_mfma_f32_16x16x32_bf16 v[118:121], v[172:175], v[216:219], v[118:121]
	v_mfma_f32_16x16x32_bf16 v[110:113], v[154:157], v[240:243], v[110:113]
	v_mfma_f32_16x16x32_bf16 v[102:105], v[172:175], v[240:243], v[102:105]
	v_mfma_f32_16x16x32_bf16 v[94:97], v[154:157], v[248:251], v[94:97]
	v_mfma_f32_16x16x32_bf16 v[86:89], v[172:175], v[248:251], v[86:89]
	s_setprio 0
	s_setprio 1
	v_mfma_f32_16x16x32_bf16 v[138:141], v[176:179], v[204:207], v[138:141]
	v_mfma_f32_16x16x32_bf16 v[130:133], v[196:199], v[204:207], v[130:133]
	v_mfma_f32_16x16x32_bf16 v[122:125], v[176:179], v[212:215], v[122:125]
	v_mfma_f32_16x16x32_bf16 v[114:117], v[196:199], v[212:215], v[114:117]
	v_mfma_f32_16x16x32_bf16 v[106:109], v[176:179], v[220:223], v[106:109]
	v_mfma_f32_16x16x32_bf16 v[98:101], v[196:199], v[220:223], v[98:101]
	v_mfma_f32_16x16x32_bf16 v[90:93], v[176:179], v[244:247], v[90:93]
	v_mfma_f32_16x16x32_bf16 v[82:85], v[196:199], v[244:247], v[82:85]
	v_mfma_f32_16x16x32_bf16 v[138:141], v[180:183], v[208:211], v[138:141]
	v_mfma_f32_16x16x32_bf16 v[130:133], v[200:203], v[208:211], v[130:133]
	v_mfma_f32_16x16x32_bf16 v[122:125], v[180:183], v[216:219], v[122:125]
	v_mfma_f32_16x16x32_bf16 v[114:117], v[200:203], v[216:219], v[114:117]
	v_mfma_f32_16x16x32_bf16 v[106:109], v[180:183], v[240:243], v[106:109]
	v_mfma_f32_16x16x32_bf16 v[98:101], v[200:203], v[240:243], v[98:101]
	v_mfma_f32_16x16x32_bf16 v[90:93], v[180:183], v[248:251], v[90:93]
	v_mfma_f32_16x16x32_bf16 v[82:85], v[200:203], v[248:251], v[82:85]
	s_setprio 0
	s_barrier
	s_add_i32 s35, s35, s17
	v_lshl_add_u64 v[192:193], s[72:73], 0, v[148:149]
	s_mov_b32 m0, s35
	global_load_lds_dwordx4 v[192:193], off
	v_lshl_add_u64 v[224:225], v[192:193], 0, s[82:83]
	s_add_i32 m0, s35, 0x2000
	s_add_i32 s35, s55, s17
	global_load_lds_dwordx4 v[224:225], off
	v_lshl_add_u64 v[224:225], v[192:193], 0, s[64:65]
	s_mov_b32 m0, s35
	v_mov_b32_e32 v185, v187
	global_load_lds_dwordx4 v[224:225], off
	v_lshl_add_u64 v[224:225], v[192:193], 0, s[86:87]
	s_add_i32 m0, s35, 0x2000
	s_nop 0
	global_load_lds_dwordx4 v[224:225], off
	s_mov_b32 m0, s25
	v_lshl_add_u64 v[224:225], s[14:15], 0, v[186:187]
	global_load_lds_dwordx4 v186, s[14:15]
	s_mov_b32 m0, s28
	s_nop 0
	global_load_lds_dwordx4 v184, s[14:15]
	ds_read_b128 v[204:207], v166 offset:20480
	ds_read_b128 v[208:211], v166 offset:21504
	ds_read_b128 v[212:215], v166 offset:22528
	ds_read_b128 v[216:219], v166 offset:23552
	ds_read_b128 v[220:223], v166 offset:24576
	ds_read_b128 v[240:243], v166 offset:25600
	ds_read_b128 v[244:247], v166 offset:26624
	ds_read_b128 v[248:251], v166 offset:27648
	s_waitcnt vmcnt(8)
	s_waitcnt lgkmcnt(0)
	v_lshl_add_u64 v[184:185], s[14:15], 0, v[184:185]
	s_barrier
	s_setprio 1
	s_waitcnt lgkmcnt(0)
	v_mfma_f32_16x16x32_bf16 v[70:73], v[78:81], v[204:207], v[70:73]
	v_mfma_f32_16x16x32_bf16 v[54:57], v[158:161], v[204:207], v[54:57]
	v_mfma_f32_16x16x32_bf16 v[46:49], v[78:81], v[212:215], v[46:49]
	v_mfma_f32_16x16x32_bf16 v[38:41], v[158:161], v[212:215], v[38:41]
	v_mfma_f32_16x16x32_bf16 v[30:33], v[78:81], v[220:223], v[30:33]
	v_mfma_f32_16x16x32_bf16 v[22:25], v[158:161], v[220:223], v[22:25]
	v_mfma_f32_16x16x32_bf16 v[14:17], v[78:81], v[244:247], v[14:17]
	v_mfma_f32_16x16x32_bf16 v[6:9], v[158:161], v[244:247], v[6:9]
	v_mfma_f32_16x16x32_bf16 v[70:73], v[154:157], v[208:211], v[70:73]
	v_mfma_f32_16x16x32_bf16 v[54:57], v[172:175], v[208:211], v[54:57]
	v_mfma_f32_16x16x32_bf16 v[46:49], v[154:157], v[216:219], v[46:49]
	v_mfma_f32_16x16x32_bf16 v[38:41], v[172:175], v[216:219], v[38:41]
	v_mfma_f32_16x16x32_bf16 v[30:33], v[154:157], v[240:243], v[30:33]
	v_mfma_f32_16x16x32_bf16 v[22:25], v[172:175], v[240:243], v[22:25]
	v_mfma_f32_16x16x32_bf16 v[14:17], v[154:157], v[248:251], v[14:17]
	v_mfma_f32_16x16x32_bf16 v[6:9], v[172:175], v[248:251], v[6:9]
	s_setprio 0
	s_setprio 1
	v_mfma_f32_16x16x32_bf16 v[66:69], v[176:179], v[204:207], v[66:69]
	v_mfma_f32_16x16x32_bf16 v[50:53], v[196:199], v[204:207], v[50:53]
	v_mfma_f32_16x16x32_bf16 v[42:45], v[176:179], v[212:215], v[42:45]
	v_mfma_f32_16x16x32_bf16 v[34:37], v[196:199], v[212:215], v[34:37]
	v_mfma_f32_16x16x32_bf16 v[26:29], v[176:179], v[220:223], v[26:29]
	v_mfma_f32_16x16x32_bf16 v[18:21], v[196:199], v[220:223], v[18:21]
	v_mfma_f32_16x16x32_bf16 v[10:13], v[176:179], v[244:247], v[10:13]
	v_mfma_f32_16x16x32_bf16 v[2:5], v[196:199], v[244:247], v[2:5]
	v_mfma_f32_16x16x32_bf16 v[66:69], v[180:183], v[208:211], v[66:69]
	v_mfma_f32_16x16x32_bf16 v[50:53], v[200:203], v[208:211], v[50:53]
	v_mfma_f32_16x16x32_bf16 v[42:45], v[180:183], v[216:219], v[42:45]
	v_mfma_f32_16x16x32_bf16 v[34:37], v[200:203], v[216:219], v[34:37]
	v_mfma_f32_16x16x32_bf16 v[26:29], v[180:183], v[240:243], v[26:29]
	v_mfma_f32_16x16x32_bf16 v[18:21], v[200:203], v[240:243], v[18:21]
	v_mfma_f32_16x16x32_bf16 v[10:13], v[180:183], v[248:251], v[10:13]
	v_mfma_f32_16x16x32_bf16 v[2:5], v[200:203], v[248:251], v[2:5]
	s_setprio 0
	s_barrier
	s_add_i32 s35, 0, 0x19000
	v_add_u32_e32 v63, s35, v165
	s_add_i32 s55, 0, 0x1d000
	ds_read_b128 v[78:81], v63
	ds_read_b128 v[154:157], v63 offset:1024
	ds_read_b128 v[158:161], v63 offset:2048
	ds_read_b128 v[172:175], v63 offset:3072
	v_add_u32_e32 v63, s55, v165
	ds_read_b128 v[176:179], v63
	ds_read_b128 v[180:183], v63 offset:1024
	ds_read_b128 v[196:199], v63 offset:2048
	ds_read_b128 v[200:203], v63 offset:3072
	s_mov_b32 m0, s29
	ds_read_b128 v[204:207], v166 offset:36864
	ds_read_b128 v[208:211], v166 offset:37888
	ds_read_b128 v[212:215], v166 offset:38912
	ds_read_b128 v[216:219], v166 offset:39936
	ds_read_b128 v[220:223], v166 offset:40960
	ds_read_b128 v[240:243], v166 offset:41984
	ds_read_b128 v[244:247], v166 offset:43008
	ds_read_b128 v[248:251], v166 offset:44032
	global_load_lds_dwordx4 v59, s[14:15]
	s_mov_b32 m0, s33
	s_nop 0
	global_load_lds_dwordx4 v61, s[14:15]
	s_waitcnt vmcnt(8)
	s_waitcnt lgkmcnt(0)
	s_barrier
	s_setprio 1
	s_waitcnt lgkmcnt(0)
	v_mfma_f32_16x16x32_bf16 v[142:145], v[78:81], v[204:207], v[142:145]
	v_mfma_f32_16x16x32_bf16 v[134:137], v[158:161], v[204:207], v[134:137]
	v_mfma_f32_16x16x32_bf16 v[126:129], v[78:81], v[212:215], v[126:129]
	v_mfma_f32_16x16x32_bf16 v[118:121], v[158:161], v[212:215], v[118:121]
	v_mfma_f32_16x16x32_bf16 v[110:113], v[78:81], v[220:223], v[110:113]
	v_mfma_f32_16x16x32_bf16 v[102:105], v[158:161], v[220:223], v[102:105]
	v_mfma_f32_16x16x32_bf16 v[94:97], v[78:81], v[244:247], v[94:97]
	v_mfma_f32_16x16x32_bf16 v[86:89], v[158:161], v[244:247], v[86:89]
	v_mfma_f32_16x16x32_bf16 v[142:145], v[154:157], v[208:211], v[142:145]
	v_mfma_f32_16x16x32_bf16 v[134:137], v[172:175], v[208:211], v[134:137]
	v_mfma_f32_16x16x32_bf16 v[126:129], v[154:157], v[216:219], v[126:129]
	v_mfma_f32_16x16x32_bf16 v[118:121], v[172:175], v[216:219], v[118:121]
	v_mfma_f32_16x16x32_bf16 v[110:113], v[154:157], v[240:243], v[110:113]
	v_mfma_f32_16x16x32_bf16 v[102:105], v[172:175], v[240:243], v[102:105]
	v_mfma_f32_16x16x32_bf16 v[94:97], v[154:157], v[248:251], v[94:97]
	v_mfma_f32_16x16x32_bf16 v[86:89], v[172:175], v[248:251], v[86:89]
	s_setprio 0
	s_setprio 1
	v_mfma_f32_16x16x32_bf16 v[138:141], v[176:179], v[204:207], v[138:141]
	v_mfma_f32_16x16x32_bf16 v[130:133], v[196:199], v[204:207], v[130:133]
	v_mfma_f32_16x16x32_bf16 v[122:125], v[176:179], v[212:215], v[122:125]
	v_mfma_f32_16x16x32_bf16 v[114:117], v[196:199], v[212:215], v[114:117]
	v_mfma_f32_16x16x32_bf16 v[106:109], v[176:179], v[220:223], v[106:109]
	v_mfma_f32_16x16x32_bf16 v[98:101], v[196:199], v[220:223], v[98:101]
	v_mfma_f32_16x16x32_bf16 v[90:93], v[176:179], v[244:247], v[90:93]
	v_mfma_f32_16x16x32_bf16 v[82:85], v[196:199], v[244:247], v[82:85]
	v_mfma_f32_16x16x32_bf16 v[138:141], v[180:183], v[208:211], v[138:141]
	v_mfma_f32_16x16x32_bf16 v[130:133], v[200:203], v[208:211], v[130:133]
	v_mfma_f32_16x16x32_bf16 v[122:125], v[180:183], v[216:219], v[122:125]
	v_mfma_f32_16x16x32_bf16 v[114:117], v[200:203], v[216:219], v[114:117]
	v_mfma_f32_16x16x32_bf16 v[106:109], v[180:183], v[240:243], v[106:109]
	v_mfma_f32_16x16x32_bf16 v[98:101], v[200:203], v[240:243], v[98:101]
	v_mfma_f32_16x16x32_bf16 v[90:93], v[180:183], v[248:251], v[90:93]
	v_mfma_f32_16x16x32_bf16 v[82:85], v[200:203], v[248:251], v[82:85]
	s_setprio 0
	s_barrier
	s_add_i32 s14, s35, s17
	v_lshl_add_u64 v[230:231], v[192:193], 0, s[92:93]
	s_mov_b32 m0, s14
	global_load_lds_dwordx4 v[230:231], off
	v_lshl_add_u64 v[230:231], v[192:193], 0, s[4:5]
	s_add_i32 m0, s14, 0x2000
	s_add_i32 s14, s55, s17
	global_load_lds_dwordx4 v[230:231], off
	v_lshl_add_u64 v[230:231], v[192:193], 0, s[6:7]
	s_mov_b32 m0, s14
	v_lshl_add_u64 v[192:193], v[192:193], 0, s[8:9]
	global_load_lds_dwordx4 v[230:231], off
	s_add_i32 m0, s14, 0x2000
	v_lshl_add_u64 v[184:185], v[184:185], 0, s[92:93]
	global_load_lds_dwordx4 v[192:193], off
	v_lshl_add_u64 v[192:193], v[224:225], 0, s[92:93]
	s_mov_b32 m0, s80
	s_nop 0
	global_load_lds_dwordx4 v[192:193], off
	s_mov_b32 m0, s81
	s_nop 0
	global_load_lds_dwordx4 v[184:185], off
	ds_read_b128 v[204:207], v166 offset:53248
	ds_read_b128 v[208:211], v166 offset:54272
	ds_read_b128 v[212:215], v166 offset:55296
	ds_read_b128 v[216:219], v166 offset:56320
	ds_read_b128 v[220:223], v166 offset:57344
	ds_read_b128 v[240:243], v166 offset:58368
	ds_read_b128 v[244:247], v166 offset:59392
	ds_read_b128 v[248:251], v166 offset:60416
	s_waitcnt vmcnt(8)
	s_waitcnt lgkmcnt(0)
	s_barrier
	s_setprio 1
	s_waitcnt lgkmcnt(0)
	v_mfma_f32_16x16x32_bf16 v[70:73], v[78:81], v[204:207], v[70:73]
	v_mfma_f32_16x16x32_bf16 v[54:57], v[158:161], v[204:207], v[54:57]
	v_mfma_f32_16x16x32_bf16 v[46:49], v[78:81], v[212:215], v[46:49]
	v_mfma_f32_16x16x32_bf16 v[38:41], v[158:161], v[212:215], v[38:41]
	v_mfma_f32_16x16x32_bf16 v[30:33], v[78:81], v[220:223], v[30:33]
	v_mfma_f32_16x16x32_bf16 v[22:25], v[158:161], v[220:223], v[22:25]
	v_mfma_f32_16x16x32_bf16 v[14:17], v[78:81], v[244:247], v[14:17]
	v_mfma_f32_16x16x32_bf16 v[6:9], v[158:161], v[244:247], v[6:9]
	v_mfma_f32_16x16x32_bf16 v[70:73], v[154:157], v[208:211], v[70:73]
	v_mfma_f32_16x16x32_bf16 v[54:57], v[172:175], v[208:211], v[54:57]
	v_mfma_f32_16x16x32_bf16 v[46:49], v[154:157], v[216:219], v[46:49]
	v_mfma_f32_16x16x32_bf16 v[38:41], v[172:175], v[216:219], v[38:41]
	v_mfma_f32_16x16x32_bf16 v[30:33], v[154:157], v[240:243], v[30:33]
	v_mfma_f32_16x16x32_bf16 v[22:25], v[172:175], v[240:243], v[22:25]
	v_mfma_f32_16x16x32_bf16 v[14:17], v[154:157], v[248:251], v[14:17]
	v_mfma_f32_16x16x32_bf16 v[6:9], v[172:175], v[248:251], v[6:9]
	s_setprio 0
	s_setprio 1
	v_mfma_f32_16x16x32_bf16 v[66:69], v[176:179], v[204:207], v[66:69]
	v_mfma_f32_16x16x32_bf16 v[50:53], v[196:199], v[204:207], v[50:53]
	v_mfma_f32_16x16x32_bf16 v[42:45], v[176:179], v[212:215], v[42:45]
	v_mfma_f32_16x16x32_bf16 v[34:37], v[196:199], v[212:215], v[34:37]
	v_mfma_f32_16x16x32_bf16 v[26:29], v[176:179], v[220:223], v[26:29]
	v_mfma_f32_16x16x32_bf16 v[18:21], v[196:199], v[220:223], v[18:21]
	v_mfma_f32_16x16x32_bf16 v[10:13], v[176:179], v[244:247], v[10:13]
	v_mfma_f32_16x16x32_bf16 v[2:5], v[196:199], v[244:247], v[2:5]
	v_mfma_f32_16x16x32_bf16 v[66:69], v[180:183], v[208:211], v[66:69]
	v_mfma_f32_16x16x32_bf16 v[50:53], v[200:203], v[208:211], v[50:53]
	v_mfma_f32_16x16x32_bf16 v[42:45], v[180:183], v[216:219], v[42:45]
	v_mfma_f32_16x16x32_bf16 v[34:37], v[200:203], v[216:219], v[34:37]
	v_mfma_f32_16x16x32_bf16 v[26:29], v[180:183], v[240:243], v[26:29]
	v_mfma_f32_16x16x32_bf16 v[18:21], v[200:203], v[240:243], v[18:21]
	v_mfma_f32_16x16x32_bf16 v[10:13], v[180:183], v[248:251], v[10:13]
	v_mfma_f32_16x16x32_bf16 v[2:5], v[200:203], v[248:251], v[2:5]
	s_setprio 0
	s_barrier
	s_add_i32 s34, s34, 2
	s_add_u32 s40, s40, 0x100
	s_addc_u32 s41, s41, 0
	s_cmp_gt_u32 s34, 13
	s_cbranch_scc0 .LBB0_1339
	s_lshl_b32 s1, s60, 8
	s_or_b32 s14, s1, s84
	s_ashr_i32 s15, s14, 31
	s_lshl_b64 s[14:15], s[14:15], 2
	s_add_u32 s1, s74, s14
	s_addc_u32 s2, s75, s15
	s_ashr_i32 s69, s68, 31
	s_lshl_b64 s[14:15], s[68:69], 13
	s_add_u32 s14, s1, s14
	s_addc_u32 s15, s2, s15
	v_lshl_add_u64 v[78:79], s[14:15], 0, v[150:151]
	global_load_dwordx4 v[58:61], v[78:79], off offset:48
	global_load_dwordx4 v[62:65], v[78:79], off offset:32
	global_load_dwordx4 v[74:77], v[78:79], off offset:16
	s_nop 0
	global_load_dwordx4 v[78:81], v[78:79], off
	s_and_b64 vcc, exec, s[50:51]
	s_cbranch_vccz .LBB0_1342
	s_barrier

.LBB0_1369:
	s_add_u32 s48, s46, 0x100
	s_addc_u32 s49, s47, 0
	s_cmp_lg_u32 s24, 12
	s_cselect_b32 s25, s48, 0
	s_add_u32 s14, s40, s25
	s_addc_u32 s15, s41, 0
	s_add_i32 s43, 0, 0x11000
	s_add_u32 s44, s0, s25
	v_add_u32_e32 v153, s43, v151
	s_addc_u32 s45, s1, 0
	s_add_i32 s25, 0, 0x15000
	ds_read_b128 v[154:157], v153
	ds_read_b128 v[158:161], v153 offset:1024
	ds_read_b128 v[162:165], v153 offset:2048
	ds_read_b128 v[166:169], v153 offset:3072
	v_add_u32_e32 v153, s25, v151
	ds_read_b128 v[170:173], v153
	ds_read_b128 v[174:177], v153 offset:1024
	ds_read_b128 v[178:181], v153 offset:2048
	ds_read_b128 v[182:185], v153 offset:3072
	v_lshl_add_u64 v[192:193], v[148:149], 0, s[46:47]
	s_mov_b64 s[46:47], 0x6e040080
	v_lshl_add_u64 v[224:225], v[192:193], 0, s[46:47]
	s_add_i32 m0, s16, 0xd000
	s_mov_b64 s[46:47], 0x6e060080
	ds_read_b128 v[196:199], v152 offset:4096
	ds_read_b128 v[200:203], v152 offset:5120
	ds_read_b128 v[204:207], v152 offset:6144
	ds_read_b128 v[208:211], v152 offset:7168
	ds_read_b128 v[212:215], v152 offset:8192
	ds_read_b128 v[216:219], v152 offset:9216
	ds_read_b128 v[220:223], v152 offset:10240
	ds_read_b128 v[240:243], v152 offset:11264
	global_load_lds_dwordx4 v[224:225], off
	v_lshl_add_u64 v[192:193], v[192:193], 0, s[46:47]
	s_add_i32 m0, s16, 0xf000
	s_nop 0
	global_load_lds_dwordx4 v[192:193], off
	s_waitcnt vmcnt(8)
	s_waitcnt lgkmcnt(0)
	s_barrier
	s_setprio 1
	s_waitcnt lgkmcnt(0)
	v_mfma_f32_16x16x32_bf16 v[142:145], v[154:157], v[196:199], v[142:145]
	v_mfma_f32_16x16x32_bf16 v[138:141], v[162:165], v[196:199], v[138:141]
	v_mfma_f32_16x16x32_bf16 v[126:129], v[154:157], v[204:207], v[126:129]
	v_mfma_f32_16x16x32_bf16 v[122:125], v[162:165], v[204:207], v[122:125]
	v_mfma_f32_16x16x32_bf16 v[110:113], v[154:157], v[212:215], v[110:113]
	v_mfma_f32_16x16x32_bf16 v[106:109], v[162:165], v[212:215], v[106:109]
	v_mfma_f32_16x16x32_bf16 v[94:97], v[154:157], v[220:223], v[94:97]
	v_mfma_f32_16x16x32_bf16 v[90:93], v[162:165], v[220:223], v[90:93]
	v_mfma_f32_16x16x32_bf16 v[142:145], v[158:161], v[200:203], v[142:145]
	v_mfma_f32_16x16x32_bf16 v[138:141], v[166:169], v[200:203], v[138:141]
	v_mfma_f32_16x16x32_bf16 v[126:129], v[158:161], v[208:211], v[126:129]
	v_mfma_f32_16x16x32_bf16 v[122:125], v[166:169], v[208:211], v[122:125]
	v_mfma_f32_16x16x32_bf16 v[110:113], v[158:161], v[216:219], v[110:113]
	v_mfma_f32_16x16x32_bf16 v[106:109], v[166:169], v[216:219], v[106:109]
	v_mfma_f32_16x16x32_bf16 v[94:97], v[158:161], v[240:243], v[94:97]
	v_mfma_f32_16x16x32_bf16 v[90:93], v[166:169], v[240:243], v[90:93]
	s_setprio 0
	s_setprio 1
	v_mfma_f32_16x16x32_bf16 v[134:137], v[170:173], v[196:199], v[134:137]
	v_mfma_f32_16x16x32_bf16 v[130:133], v[178:181], v[196:199], v[130:133]
	v_mfma_f32_16x16x32_bf16 v[118:121], v[170:173], v[204:207], v[118:121]
	v_mfma_f32_16x16x32_bf16 v[114:117], v[178:181], v[204:207], v[114:117]
	v_mfma_f32_16x16x32_bf16 v[102:105], v[170:173], v[212:215], v[102:105]
	v_mfma_f32_16x16x32_bf16 v[98:101], v[178:181], v[212:215], v[98:101]
	v_mfma_f32_16x16x32_bf16 v[86:89], v[170:173], v[220:223], v[86:89]
	v_mfma_f32_16x16x32_bf16 v[82:85], v[178:181], v[220:223], v[82:85]
	v_mfma_f32_16x16x32_bf16 v[134:137], v[174:177], v[200:203], v[134:137]
	v_mfma_f32_16x16x32_bf16 v[130:133], v[182:185], v[200:203], v[130:133]
	v_mfma_f32_16x16x32_bf16 v[118:121], v[174:177], v[208:211], v[118:121]
	v_mfma_f32_16x16x32_bf16 v[114:117], v[182:185], v[208:211], v[114:117]
	v_mfma_f32_16x16x32_bf16 v[102:105], v[174:177], v[216:219], v[102:105]
	v_mfma_f32_16x16x32_bf16 v[98:101], v[182:185], v[216:219], v[98:101]
	v_mfma_f32_16x16x32_bf16 v[86:89], v[174:177], v[240:243], v[86:89]
	v_mfma_f32_16x16x32_bf16 v[82:85], v[182:185], v[240:243], v[82:85]
	s_setprio 0
	s_barrier
	s_add_i32 s43, s43, s13
	v_lshl_add_u64 v[192:193], s[44:45], 0, v[186:187]
	s_mov_b32 m0, s43
	global_load_lds_dwordx4 v[192:193], off
	v_lshl_add_u64 v[224:225], v[192:193], 0, s[82:83]
	s_add_i32 m0, s43, 0x2000
	s_add_i32 s25, s25, s13
	global_load_lds_dwordx4 v[224:225], off
	v_lshl_add_u64 v[224:225], v[192:193], 0, s[64:65]
	s_mov_b32 m0, s25
	s_nop 0
	global_load_lds_dwordx4 v[224:225], off
	v_lshl_add_u64 v[224:225], v[192:193], 0, s[86:87]
	s_add_i32 m0, s25, 0x2000
	s_nop 0
	global_load_lds_dwordx4 v[224:225], off
	v_lshl_add_u64 v[224:225], s[14:15], 0, v[146:147]
	s_mov_b32 m0, s17
	v_lshl_add_u64 v[230:231], v[224:225], 0, s[82:83]
	global_load_lds_dwordx4 v[224:225], off
	s_mov_b32 m0, s28
	s_nop 0
	global_load_lds_dwordx4 v[230:231], off
	ds_read_b128 v[196:199], v152 offset:20480
	ds_read_b128 v[200:203], v152 offset:21504
	ds_read_b128 v[204:207], v152 offset:22528
	ds_read_b128 v[208:211], v152 offset:23552
	ds_read_b128 v[212:215], v152 offset:24576
	ds_read_b128 v[216:219], v152 offset:25600
	ds_read_b128 v[220:223], v152 offset:26624
	ds_read_b128 v[240:243], v152 offset:27648
	s_waitcnt vmcnt(8)
	s_waitcnt lgkmcnt(0)
	s_barrier
	s_setprio 1
	s_waitcnt lgkmcnt(0)
	v_mfma_f32_16x16x32_bf16 v[78:81], v[154:157], v[196:199], v[78:81]
	v_mfma_f32_16x16x32_bf16 v[74:77], v[162:165], v[196:199], v[74:77]
	v_mfma_f32_16x16x32_bf16 v[62:65], v[154:157], v[204:207], v[62:65]
	v_mfma_f32_16x16x32_bf16 v[58:61], v[162:165], v[204:207], v[58:61]
	v_mfma_f32_16x16x32_bf16 v[46:49], v[154:157], v[212:215], v[46:49]
	v_mfma_f32_16x16x32_bf16 v[42:45], v[162:165], v[212:215], v[42:45]
	v_mfma_f32_16x16x32_bf16 v[30:33], v[154:157], v[220:223], v[30:33]
	v_mfma_f32_16x16x32_bf16 v[26:29], v[162:165], v[220:223], v[26:29]
	v_mfma_f32_16x16x32_bf16 v[78:81], v[158:161], v[200:203], v[78:81]
	v_mfma_f32_16x16x32_bf16 v[74:77], v[166:169], v[200:203], v[74:77]
	v_mfma_f32_16x16x32_bf16 v[62:65], v[158:161], v[208:211], v[62:65]
	v_mfma_f32_16x16x32_bf16 v[58:61], v[166:169], v[208:211], v[58:61]
	v_mfma_f32_16x16x32_bf16 v[46:49], v[158:161], v[216:219], v[46:49]
	v_mfma_f32_16x16x32_bf16 v[42:45], v[166:169], v[216:219], v[42:45]
	v_mfma_f32_16x16x32_bf16 v[30:33], v[158:161], v[240:243], v[30:33]
	v_mfma_f32_16x16x32_bf16 v[26:29], v[166:169], v[240:243], v[26:29]
	s_setprio 0
	s_setprio 1
	v_mfma_f32_16x16x32_bf16 v[70:73], v[170:173], v[196:199], v[70:73]
	v_mfma_f32_16x16x32_bf16 v[66:69], v[178:181], v[196:199], v[66:69]
	v_mfma_f32_16x16x32_bf16 v[54:57], v[170:173], v[204:207], v[54:57]
	v_mfma_f32_16x16x32_bf16 v[50:53], v[178:181], v[204:207], v[50:53]
	v_mfma_f32_16x16x32_bf16 v[38:41], v[170:173], v[212:215], v[38:41]
	v_mfma_f32_16x16x32_bf16 v[34:37], v[178:181], v[212:215], v[34:37]
	v_mfma_f32_16x16x32_bf16 v[22:25], v[170:173], v[220:223], v[22:25]
	v_mfma_f32_16x16x32_bf16 v[18:21], v[178:181], v[220:223], v[18:21]
	v_mfma_f32_16x16x32_bf16 v[70:73], v[174:177], v[200:203], v[70:73]
	v_mfma_f32_16x16x32_bf16 v[66:69], v[182:185], v[200:203], v[66:69]
	v_mfma_f32_16x16x32_bf16 v[54:57], v[174:177], v[208:211], v[54:57]
	v_mfma_f32_16x16x32_bf16 v[50:53], v[182:185], v[208:211], v[50:53]
	v_mfma_f32_16x16x32_bf16 v[38:41], v[174:177], v[216:219], v[38:41]
	v_mfma_f32_16x16x32_bf16 v[34:37], v[182:185], v[216:219], v[34:37]
	v_mfma_f32_16x16x32_bf16 v[22:25], v[174:177], v[240:243], v[22:25]
	v_mfma_f32_16x16x32_bf16 v[18:21], v[182:185], v[240:243], v[18:21]
	s_setprio 0
	s_barrier
	s_add_i32 s14, 0, 0x19000
	v_add_u32_e32 v153, s14, v151
	s_add_i32 s15, 0, 0x1d000
	ds_read_b128 v[154:157], v153
	ds_read_b128 v[158:161], v153 offset:1024
	ds_read_b128 v[162:165], v153 offset:2048
	ds_read_b128 v[166:169], v153 offset:3072
	v_add_u32_e32 v153, s15, v151
	ds_read_b128 v[170:173], v153
	ds_read_b128 v[174:177], v153 offset:1024
	ds_read_b128 v[178:181], v153 offset:2048
	ds_read_b128 v[182:185], v153 offset:3072
	s_mov_b32 m0, s29
	v_lshl_add_u64 v[230:231], v[224:225], 0, s[64:65]
	ds_read_b128 v[196:199], v152 offset:36864
	ds_read_b128 v[200:203], v152 offset:37888
	ds_read_b128 v[204:207], v152 offset:38912
	ds_read_b128 v[208:211], v152 offset:39936
	ds_read_b128 v[212:215], v152 offset:40960
	ds_read_b128 v[216:219], v152 offset:41984
	ds_read_b128 v[220:223], v152 offset:43008
	ds_read_b128 v[240:243], v152 offset:44032
	global_load_lds_dwordx4 v[230:231], off
	v_lshl_add_u64 v[230:231], v[224:225], 0, s[86:87]
	s_mov_b32 m0, s33
	s_nop 0
	global_load_lds_dwordx4 v[230:231], off
	s_waitcnt vmcnt(8)
	s_waitcnt lgkmcnt(0)
	s_barrier
	s_setprio 1
	s_waitcnt lgkmcnt(0)
	v_mfma_f32_16x16x32_bf16 v[142:145], v[154:157], v[196:199], v[142:145]
	v_mfma_f32_16x16x32_bf16 v[138:141], v[162:165], v[196:199], v[138:141]
	v_mfma_f32_16x16x32_bf16 v[126:129], v[154:157], v[204:207], v[126:129]
	v_mfma_f32_16x16x32_bf16 v[122:125], v[162:165], v[204:207], v[122:125]
	v_mfma_f32_16x16x32_bf16 v[110:113], v[154:157], v[212:215], v[110:113]
	v_mfma_f32_16x16x32_bf16 v[106:109], v[162:165], v[212:215], v[106:109]
	v_mfma_f32_16x16x32_bf16 v[94:97], v[154:157], v[220:223], v[94:97]
	v_mfma_f32_16x16x32_bf16 v[90:93], v[162:165], v[220:223], v[90:93]
	v_mfma_f32_16x16x32_bf16 v[142:145], v[158:161], v[200:203], v[142:145]
	v_mfma_f32_16x16x32_bf16 v[138:141], v[166:169], v[200:203], v[138:141]
	v_mfma_f32_16x16x32_bf16 v[126:129], v[158:161], v[208:211], v[126:129]
	v_mfma_f32_16x16x32_bf16 v[122:125], v[166:169], v[208:211], v[122:125]
	v_mfma_f32_16x16x32_bf16 v[110:113], v[158:161], v[216:219], v[110:113]
	v_mfma_f32_16x16x32_bf16 v[106:109], v[166:169], v[216:219], v[106:109]
	v_mfma_f32_16x16x32_bf16 v[94:97], v[158:161], v[240:243], v[94:97]
	v_mfma_f32_16x16x32_bf16 v[90:93], v[166:169], v[240:243], v[90:93]
	s_setprio 0
	s_setprio 1
	v_mfma_f32_16x16x32_bf16 v[134:137], v[170:173], v[196:199], v[134:137]
	v_mfma_f32_16x16x32_bf16 v[130:133], v[178:181], v[196:199], v[130:133]
	v_mfma_f32_16x16x32_bf16 v[118:121], v[170:173], v[204:207], v[118:121]
	v_mfma_f32_16x16x32_bf16 v[114:117], v[178:181], v[204:207], v[114:117]
	v_mfma_f32_16x16x32_bf16 v[102:105], v[170:173], v[212:215], v[102:105]
	v_mfma_f32_16x16x32_bf16 v[98:101], v[178:181], v[212:215], v[98:101]
	v_mfma_f32_16x16x32_bf16 v[86:89], v[170:173], v[220:223], v[86:89]
	v_mfma_f32_16x16x32_bf16 v[82:85], v[178:181], v[220:223], v[82:85]
	v_mfma_f32_16x16x32_bf16 v[134:137], v[174:177], v[200:203], v[134:137]
	v_mfma_f32_16x16x32_bf16 v[130:133], v[182:185], v[200:203], v[130:133]
	v_mfma_f32_16x16x32_bf16 v[118:121], v[174:177], v[208:211], v[118:121]
	v_mfma_f32_16x16x32_bf16 v[114:117], v[182:185], v[208:211], v[114:117]
	v_mfma_f32_16x16x32_bf16 v[102:105], v[174:177], v[216:219], v[102:105]
	v_mfma_f32_16x16x32_bf16 v[98:101], v[182:185], v[216:219], v[98:101]
	v_mfma_f32_16x16x32_bf16 v[86:89], v[174:177], v[240:243], v[86:89]
	v_mfma_f32_16x16x32_bf16 v[82:85], v[182:185], v[240:243], v[82:85]
	s_setprio 0
	s_barrier
	s_add_i32 s14, s14, s13
	v_lshl_add_u64 v[230:231], v[192:193], 0, s[92:93]
	s_mov_b32 m0, s14
	global_load_lds_dwordx4 v[230:231], off
	v_lshl_add_u64 v[230:231], v[192:193], 0, s[4:5]
	s_add_i32 m0, s14, 0x2000
	s_add_i32 s14, s15, s13
	global_load_lds_dwordx4 v[230:231], off
	v_lshl_add_u64 v[230:231], v[192:193], 0, s[6:7]
	s_mov_b32 m0, s14
	v_lshl_add_u64 v[192:193], v[192:193], 0, s[8:9]
	global_load_lds_dwordx4 v[230:231], off
	s_add_i32 m0, s14, 0x2000
	s_nop 0
	global_load_lds_dwordx4 v[192:193], off
	v_lshl_add_u64 v[192:193], v[224:225], 0, s[92:93]
	s_mov_b32 m0, s35
	s_nop 0
	global_load_lds_dwordx4 v[192:193], off
	v_lshl_add_u64 v[192:193], v[224:225], 0, s[4:5]
	s_mov_b32 m0, s42
	s_nop 0
	global_load_lds_dwordx4 v[192:193], off
	ds_read_b128 v[196:199], v152 offset:53248
	ds_read_b128 v[200:203], v152 offset:54272
	ds_read_b128 v[204:207], v152 offset:55296
	ds_read_b128 v[208:211], v152 offset:56320
	ds_read_b128 v[212:215], v152 offset:57344
	ds_read_b128 v[216:219], v152 offset:58368
	ds_read_b128 v[220:223], v152 offset:59392
	ds_read_b128 v[240:243], v152 offset:60416
	s_waitcnt vmcnt(8)
	s_waitcnt lgkmcnt(0)
	s_barrier
	s_setprio 1
	s_waitcnt lgkmcnt(0)
	v_mfma_f32_16x16x32_bf16 v[78:81], v[154:157], v[196:199], v[78:81]
	v_mfma_f32_16x16x32_bf16 v[74:77], v[162:165], v[196:199], v[74:77]
	v_mfma_f32_16x16x32_bf16 v[62:65], v[154:157], v[204:207], v[62:65]
	v_mfma_f32_16x16x32_bf16 v[58:61], v[162:165], v[204:207], v[58:61]
	v_mfma_f32_16x16x32_bf16 v[46:49], v[154:157], v[212:215], v[46:49]
	v_mfma_f32_16x16x32_bf16 v[42:45], v[162:165], v[212:215], v[42:45]
	v_mfma_f32_16x16x32_bf16 v[30:33], v[154:157], v[220:223], v[30:33]
	v_mfma_f32_16x16x32_bf16 v[26:29], v[162:165], v[220:223], v[26:29]
	v_mfma_f32_16x16x32_bf16 v[78:81], v[158:161], v[200:203], v[78:81]
	v_mfma_f32_16x16x32_bf16 v[74:77], v[166:169], v[200:203], v[74:77]
	v_mfma_f32_16x16x32_bf16 v[62:65], v[158:161], v[208:211], v[62:65]
	v_mfma_f32_16x16x32_bf16 v[58:61], v[166:169], v[208:211], v[58:61]
	v_mfma_f32_16x16x32_bf16 v[46:49], v[158:161], v[216:219], v[46:49]
	v_mfma_f32_16x16x32_bf16 v[42:45], v[166:169], v[216:219], v[42:45]
	v_mfma_f32_16x16x32_bf16 v[30:33], v[158:161], v[240:243], v[30:33]
	v_mfma_f32_16x16x32_bf16 v[26:29], v[166:169], v[240:243], v[26:29]
	s_setprio 0
	s_setprio 1
	v_mfma_f32_16x16x32_bf16 v[70:73], v[170:173], v[196:199], v[70:73]
	v_mfma_f32_16x16x32_bf16 v[66:69], v[178:181], v[196:199], v[66:69]
	v_mfma_f32_16x16x32_bf16 v[54:57], v[170:173], v[204:207], v[54:57]
	v_mfma_f32_16x16x32_bf16 v[50:53], v[178:181], v[204:207], v[50:53]
	v_mfma_f32_16x16x32_bf16 v[38:41], v[170:173], v[212:215], v[38:41]
	v_mfma_f32_16x16x32_bf16 v[34:37], v[178:181], v[212:215], v[34:37]
	v_mfma_f32_16x16x32_bf16 v[22:25], v[170:173], v[220:223], v[22:25]
	v_mfma_f32_16x16x32_bf16 v[18:21], v[178:181], v[220:223], v[18:21]
	v_mfma_f32_16x16x32_bf16 v[70:73], v[174:177], v[200:203], v[70:73]
	v_mfma_f32_16x16x32_bf16 v[66:69], v[182:185], v[200:203], v[66:69]
	v_mfma_f32_16x16x32_bf16 v[54:57], v[174:177], v[208:211], v[54:57]
	v_mfma_f32_16x16x32_bf16 v[50:53], v[182:185], v[208:211], v[50:53]
	v_mfma_f32_16x16x32_bf16 v[38:41], v[174:177], v[216:219], v[38:41]
	v_mfma_f32_16x16x32_bf16 v[34:37], v[182:185], v[216:219], v[34:37]
	v_mfma_f32_16x16x32_bf16 v[22:25], v[174:177], v[240:243], v[22:25]
	v_mfma_f32_16x16x32_bf16 v[18:21], v[182:185], v[240:243], v[18:21]
	s_setprio 0
	s_barrier
	s_add_i32 s24, s24, 2
	s_cmp_gt_u32 s24, 13
	s_mov_b64 s[46:47], s[48:49]
	s_cbranch_scc0 .LBB0_1369
	s_cmpk_lt_u32 s2, 0x100
	s_cbranch_scc0 .LBB0_1372
	s_barrier

.LBB0_1462:
	s_add_u32 s2, s56, 0x100
	s_addc_u32 s24, s57, 0
	s_add_u32 s56, s58, 0x40080
	s_waitcnt lgkmcnt(0)
	s_addc_u32 s57, s59, 0
	s_mov_b32 s25, -2
	s_add_u32 s14, s56, 0xfffc0080
	s_addc_u32 s15, s57, -1
	s_add_i32 s49, 0, 0x11000
	s_cmp_eq_u32 s25, 12
	s_cselect_b32 s15, s53, s15
	s_cselect_b32 s14, s52, s14
	v_add_u32_e32 v155, s49, v1
	s_cselect_b32 s35, s51, s24
	s_cselect_b32 s34, s50, s2
	s_add_i32 s55, 0, 0x15000
	ds_read_b128 v[156:159], v155
	ds_read_b128 v[160:163], v155 offset:1024
	ds_read_b128 v[164:167], v155 offset:2048
	ds_read_b128 v[168:171], v155 offset:3072
	v_add_u32_e32 v155, s55, v1
	ds_read_b128 v[172:175], v155
	ds_read_b128 v[176:179], v155 offset:1024
	ds_read_b128 v[180:183], v155 offset:2048
	ds_read_b128 v[196:199], v155 offset:3072
	v_lshl_add_u64 v[184:185], s[56:57], 0, v[152:153]
	s_add_i32 m0, s61, 0xd000
	ds_read_b128 v[200:203], v154 offset:4096
	ds_read_b128 v[204:207], v154 offset:5120
	ds_read_b128 v[208:211], v154 offset:6144
	ds_read_b128 v[212:215], v154 offset:7168
	ds_read_b128 v[216:219], v154 offset:8192
	ds_read_b128 v[220:223], v154 offset:9216
	ds_read_b128 v[240:243], v154 offset:10240
	ds_read_b128 v[244:247], v154 offset:11264
	global_load_lds_dwordx4 v[184:185], off
	v_lshl_add_u64 v[184:185], v[184:185], 0, s[82:83]
	s_add_i32 m0, s61, 0xf000
	s_nop 0
	global_load_lds_dwordx4 v[184:185], off
	s_waitcnt vmcnt(8)
	s_waitcnt lgkmcnt(0)
	s_barrier
	s_setprio 1
	s_waitcnt lgkmcnt(0)
	v_mfma_f32_16x16x32_bf16 v[142:145], v[156:159], v[200:203], 0
	v_mfma_f32_16x16x32_bf16 v[138:141], v[164:167], v[200:203], 0
	v_mfma_f32_16x16x32_bf16 v[126:129], v[156:159], v[208:211], 0
	v_mfma_f32_16x16x32_bf16 v[122:125], v[164:167], v[208:211], 0
	v_mfma_f32_16x16x32_bf16 v[110:113], v[156:159], v[216:219], 0
	v_mfma_f32_16x16x32_bf16 v[106:109], v[164:167], v[216:219], 0
	v_mfma_f32_16x16x32_bf16 v[94:97], v[156:159], v[240:243], 0
	v_mfma_f32_16x16x32_bf16 v[90:93], v[164:167], v[240:243], 0
	v_mfma_f32_16x16x32_bf16 v[142:145], v[160:163], v[204:207], v[142:145]
	v_mfma_f32_16x16x32_bf16 v[138:141], v[168:171], v[204:207], v[138:141]
	v_mfma_f32_16x16x32_bf16 v[126:129], v[160:163], v[212:215], v[126:129]
	v_mfma_f32_16x16x32_bf16 v[122:125], v[168:171], v[212:215], v[122:125]
	v_mfma_f32_16x16x32_bf16 v[110:113], v[160:163], v[220:223], v[110:113]
	v_mfma_f32_16x16x32_bf16 v[106:109], v[168:171], v[220:223], v[106:109]
	v_mfma_f32_16x16x32_bf16 v[94:97], v[160:163], v[244:247], v[94:97]
	v_mfma_f32_16x16x32_bf16 v[90:93], v[168:171], v[244:247], v[90:93]
	s_setprio 0
	s_setprio 1
	v_mfma_f32_16x16x32_bf16 v[134:137], v[172:175], v[200:203], 0
	v_mfma_f32_16x16x32_bf16 v[130:133], v[180:183], v[200:203], 0
	v_mfma_f32_16x16x32_bf16 v[118:121], v[172:175], v[208:211], 0
	v_mfma_f32_16x16x32_bf16 v[114:117], v[180:183], v[208:211], 0
	v_mfma_f32_16x16x32_bf16 v[102:105], v[172:175], v[216:219], 0
	v_mfma_f32_16x16x32_bf16 v[98:101], v[180:183], v[216:219], 0
	v_mfma_f32_16x16x32_bf16 v[86:89], v[172:175], v[240:243], 0
	v_mfma_f32_16x16x32_bf16 v[82:85], v[180:183], v[240:243], 0
	v_mfma_f32_16x16x32_bf16 v[134:137], v[176:179], v[204:207], v[134:137]
	v_mfma_f32_16x16x32_bf16 v[130:133], v[196:199], v[204:207], v[130:133]
	v_mfma_f32_16x16x32_bf16 v[118:121], v[176:179], v[212:215], v[118:121]
	v_mfma_f32_16x16x32_bf16 v[114:117], v[196:199], v[212:215], v[114:117]
	v_mfma_f32_16x16x32_bf16 v[102:105], v[176:179], v[220:223], v[102:105]
	v_mfma_f32_16x16x32_bf16 v[98:101], v[196:199], v[220:223], v[98:101]
	v_mfma_f32_16x16x32_bf16 v[86:89], v[176:179], v[244:247], v[86:89]
	v_mfma_f32_16x16x32_bf16 v[82:85], v[196:199], v[244:247], v[82:85]
	s_setprio 0
	s_barrier
	v_lshl_add_u64 v[184:185], s[34:35], 0, v[186:187]
	s_add_i32 s34, s49, s28
	s_mov_b32 m0, s34
	global_load_lds_dwordx4 v[184:185], off
	v_lshl_add_u64 v[192:193], v[184:185], 0, s[82:83]
	s_add_i32 m0, s34, 0x2000
	s_add_i32 s34, s55, s28
	global_load_lds_dwordx4 v[192:193], off
	v_lshl_add_u64 v[192:193], v[184:185], 0, s[64:65]
	s_mov_b32 m0, s34
	s_nop 0
	global_load_lds_dwordx4 v[192:193], off
	v_lshl_add_u64 v[192:193], v[184:185], 0, s[86:87]
	s_add_i32 m0, s34, 0x2000
	s_nop 0
	global_load_lds_dwordx4 v[192:193], off
	v_lshl_add_u64 v[192:193], s[14:15], 0, v[146:147]
	s_mov_b32 m0, s68
	v_lshl_add_u64 v[224:225], v[192:193], 0, s[82:83]
	global_load_lds_dwordx4 v[192:193], off
	s_mov_b32 m0, s69
	s_nop 0
	global_load_lds_dwordx4 v[224:225], off
	ds_read_b128 v[200:203], v154 offset:20480
	ds_read_b128 v[204:207], v154 offset:21504
	ds_read_b128 v[208:211], v154 offset:22528
	ds_read_b128 v[212:215], v154 offset:23552
	ds_read_b128 v[216:219], v154 offset:24576
	ds_read_b128 v[220:223], v154 offset:25600
	ds_read_b128 v[240:243], v154 offset:26624
	ds_read_b128 v[244:247], v154 offset:27648
	s_waitcnt vmcnt(8)
	s_waitcnt lgkmcnt(0)
	s_barrier
	s_setprio 1
	s_waitcnt lgkmcnt(0)
	v_mfma_f32_16x16x32_bf16 v[78:81], v[156:159], v[200:203], 0
	v_mfma_f32_16x16x32_bf16 v[74:77], v[164:167], v[200:203], 0
	v_mfma_f32_16x16x32_bf16 v[62:65], v[156:159], v[208:211], 0
	v_mfma_f32_16x16x32_bf16 v[58:61], v[164:167], v[208:211], 0
	v_mfma_f32_16x16x32_bf16 v[46:49], v[156:159], v[216:219], 0
	v_mfma_f32_16x16x32_bf16 v[42:45], v[164:167], v[216:219], 0
	v_mfma_f32_16x16x32_bf16 v[30:33], v[156:159], v[240:243], 0
	v_mfma_f32_16x16x32_bf16 v[26:29], v[164:167], v[240:243], 0
	v_mfma_f32_16x16x32_bf16 v[78:81], v[160:163], v[204:207], v[78:81]
	v_mfma_f32_16x16x32_bf16 v[74:77], v[168:171], v[204:207], v[74:77]
	v_mfma_f32_16x16x32_bf16 v[62:65], v[160:163], v[212:215], v[62:65]
	v_mfma_f32_16x16x32_bf16 v[58:61], v[168:171], v[212:215], v[58:61]
	v_mfma_f32_16x16x32_bf16 v[46:49], v[160:163], v[220:223], v[46:49]
	v_mfma_f32_16x16x32_bf16 v[42:45], v[168:171], v[220:223], v[42:45]
	v_mfma_f32_16x16x32_bf16 v[30:33], v[160:163], v[244:247], v[30:33]
	v_mfma_f32_16x16x32_bf16 v[26:29], v[168:171], v[244:247], v[26:29]
	s_setprio 0
	s_setprio 1
	v_mfma_f32_16x16x32_bf16 v[70:73], v[172:175], v[200:203], 0
	v_mfma_f32_16x16x32_bf16 v[66:69], v[180:183], v[200:203], 0
	v_mfma_f32_16x16x32_bf16 v[54:57], v[172:175], v[208:211], 0
	v_mfma_f32_16x16x32_bf16 v[50:53], v[180:183], v[208:211], 0
	v_mfma_f32_16x16x32_bf16 v[38:41], v[172:175], v[216:219], 0
	v_mfma_f32_16x16x32_bf16 v[34:37], v[180:183], v[216:219], 0
	v_mfma_f32_16x16x32_bf16 v[22:25], v[172:175], v[240:243], 0
	v_mfma_f32_16x16x32_bf16 v[18:21], v[180:183], v[240:243], 0
	v_mfma_f32_16x16x32_bf16 v[70:73], v[176:179], v[204:207], v[70:73]
	v_mfma_f32_16x16x32_bf16 v[66:69], v[196:199], v[204:207], v[66:69]
	v_mfma_f32_16x16x32_bf16 v[54:57], v[176:179], v[212:215], v[54:57]
	v_mfma_f32_16x16x32_bf16 v[50:53], v[196:199], v[212:215], v[50:53]
	v_mfma_f32_16x16x32_bf16 v[38:41], v[176:179], v[220:223], v[38:41]
	v_mfma_f32_16x16x32_bf16 v[34:37], v[196:199], v[220:223], v[34:37]
	v_mfma_f32_16x16x32_bf16 v[22:25], v[176:179], v[244:247], v[22:25]
	v_mfma_f32_16x16x32_bf16 v[18:21], v[196:199], v[244:247], v[18:21]
	s_setprio 0
	s_barrier
	s_add_i32 s14, 0, 0x19000
	v_add_u32_e32 v155, s14, v1
	s_add_i32 s15, 0, 0x1d000
	ds_read_b128 v[156:159], v155
	ds_read_b128 v[160:163], v155 offset:1024
	ds_read_b128 v[164:167], v155 offset:2048
	ds_read_b128 v[168:171], v155 offset:3072
	v_add_u32_e32 v155, s15, v1
	ds_read_b128 v[172:175], v155
	ds_read_b128 v[176:179], v155 offset:1024
	ds_read_b128 v[180:183], v155 offset:2048
	ds_read_b128 v[196:199], v155 offset:3072
	s_mov_b32 m0, s70
	v_lshl_add_u64 v[224:225], v[192:193], 0, s[64:65]
	ds_read_b128 v[200:203], v154 offset:36864
	ds_read_b128 v[204:207], v154 offset:37888
	ds_read_b128 v[208:211], v154 offset:38912
	ds_read_b128 v[212:215], v154 offset:39936
	ds_read_b128 v[216:219], v154 offset:40960
	ds_read_b128 v[220:223], v154 offset:41984
	ds_read_b128 v[240:243], v154 offset:43008
	ds_read_b128 v[244:247], v154 offset:44032
	global_load_lds_dwordx4 v[224:225], off
	v_lshl_add_u64 v[224:225], v[192:193], 0, s[86:87]
	s_mov_b32 m0, s71
	s_nop 0
	global_load_lds_dwordx4 v[224:225], off
	s_waitcnt vmcnt(8)
	s_waitcnt lgkmcnt(0)
	s_barrier
	s_setprio 1
	s_waitcnt lgkmcnt(0)
	v_mfma_f32_16x16x32_bf16 v[142:145], v[156:159], v[200:203], v[142:145]
	v_mfma_f32_16x16x32_bf16 v[138:141], v[164:167], v[200:203], v[138:141]
	v_mfma_f32_16x16x32_bf16 v[126:129], v[156:159], v[208:211], v[126:129]
	v_mfma_f32_16x16x32_bf16 v[122:125], v[164:167], v[208:211], v[122:125]
	v_mfma_f32_16x16x32_bf16 v[110:113], v[156:159], v[216:219], v[110:113]
	v_mfma_f32_16x16x32_bf16 v[106:109], v[164:167], v[216:219], v[106:109]
	v_mfma_f32_16x16x32_bf16 v[94:97], v[156:159], v[240:243], v[94:97]
	v_mfma_f32_16x16x32_bf16 v[90:93], v[164:167], v[240:243], v[90:93]
	v_mfma_f32_16x16x32_bf16 v[142:145], v[160:163], v[204:207], v[142:145]
	v_mfma_f32_16x16x32_bf16 v[138:141], v[168:171], v[204:207], v[138:141]
	v_mfma_f32_16x16x32_bf16 v[126:129], v[160:163], v[212:215], v[126:129]
	v_mfma_f32_16x16x32_bf16 v[122:125], v[168:171], v[212:215], v[122:125]
	v_mfma_f32_16x16x32_bf16 v[110:113], v[160:163], v[220:223], v[110:113]
	v_mfma_f32_16x16x32_bf16 v[106:109], v[168:171], v[220:223], v[106:109]
	v_mfma_f32_16x16x32_bf16 v[94:97], v[160:163], v[244:247], v[94:97]
	v_mfma_f32_16x16x32_bf16 v[90:93], v[168:171], v[244:247], v[90:93]
	s_setprio 0
	s_setprio 1
	v_mfma_f32_16x16x32_bf16 v[134:137], v[172:175], v[200:203], v[134:137]
	v_mfma_f32_16x16x32_bf16 v[130:133], v[180:183], v[200:203], v[130:133]
	v_mfma_f32_16x16x32_bf16 v[118:121], v[172:175], v[208:211], v[118:121]
	v_mfma_f32_16x16x32_bf16 v[114:117], v[180:183], v[208:211], v[114:117]
	v_mfma_f32_16x16x32_bf16 v[102:105], v[172:175], v[216:219], v[102:105]
	v_mfma_f32_16x16x32_bf16 v[98:101], v[180:183], v[216:219], v[98:101]
	v_mfma_f32_16x16x32_bf16 v[86:89], v[172:175], v[240:243], v[86:89]
	v_mfma_f32_16x16x32_bf16 v[82:85], v[180:183], v[240:243], v[82:85]
	v_mfma_f32_16x16x32_bf16 v[134:137], v[176:179], v[204:207], v[134:137]
	v_mfma_f32_16x16x32_bf16 v[130:133], v[196:199], v[204:207], v[130:133]
	v_mfma_f32_16x16x32_bf16 v[118:121], v[176:179], v[212:215], v[118:121]
	v_mfma_f32_16x16x32_bf16 v[114:117], v[196:199], v[212:215], v[114:117]
	v_mfma_f32_16x16x32_bf16 v[102:105], v[176:179], v[220:223], v[102:105]
	v_mfma_f32_16x16x32_bf16 v[98:101], v[196:199], v[220:223], v[98:101]
	v_mfma_f32_16x16x32_bf16 v[86:89], v[176:179], v[244:247], v[86:89]
	v_mfma_f32_16x16x32_bf16 v[82:85], v[196:199], v[244:247], v[82:85]
	s_setprio 0
	s_barrier
	s_add_i32 s14, s14, s28
	v_lshl_add_u64 v[224:225], v[184:185], 0, s[92:93]
	s_mov_b32 m0, s14
	global_load_lds_dwordx4 v[224:225], off
	v_lshl_add_u64 v[224:225], v[184:185], 0, s[4:5]
	s_add_i32 m0, s14, 0x2000
	s_add_i32 s14, s15, s28
	global_load_lds_dwordx4 v[224:225], off
	v_lshl_add_u64 v[224:225], v[184:185], 0, s[6:7]
	s_mov_b32 m0, s14
	v_lshl_add_u64 v[184:185], v[184:185], 0, s[8:9]
	global_load_lds_dwordx4 v[224:225], off
	s_add_i32 m0, s14, 0x2000
	s_nop 0
	global_load_lds_dwordx4 v[184:185], off
	v_lshl_add_u64 v[184:185], v[192:193], 0, s[92:93]
	s_mov_b32 m0, s75
	s_nop 0
	global_load_lds_dwordx4 v[184:185], off
	v_lshl_add_u64 v[184:185], v[192:193], 0, s[4:5]
	s_mov_b32 m0, s76
	s_nop 0
	global_load_lds_dwordx4 v[184:185], off
	ds_read_b128 v[200:203], v154 offset:53248
	ds_read_b128 v[204:207], v154 offset:54272
	ds_read_b128 v[208:211], v154 offset:55296
	ds_read_b128 v[212:215], v154 offset:56320
	ds_read_b128 v[216:219], v154 offset:57344
	ds_read_b128 v[220:223], v154 offset:58368
	ds_read_b128 v[240:243], v154 offset:59392
	ds_read_b128 v[244:247], v154 offset:60416
	s_waitcnt vmcnt(8)
	s_waitcnt lgkmcnt(0)
	s_barrier
	s_setprio 1
	s_waitcnt lgkmcnt(0)
	v_mfma_f32_16x16x32_bf16 v[78:81], v[156:159], v[200:203], v[78:81]
	v_mfma_f32_16x16x32_bf16 v[74:77], v[164:167], v[200:203], v[74:77]
	v_mfma_f32_16x16x32_bf16 v[62:65], v[156:159], v[208:211], v[62:65]
	v_mfma_f32_16x16x32_bf16 v[58:61], v[164:167], v[208:211], v[58:61]
	v_mfma_f32_16x16x32_bf16 v[46:49], v[156:159], v[216:219], v[46:49]
	v_mfma_f32_16x16x32_bf16 v[42:45], v[164:167], v[216:219], v[42:45]
	v_mfma_f32_16x16x32_bf16 v[30:33], v[156:159], v[240:243], v[30:33]
	v_mfma_f32_16x16x32_bf16 v[26:29], v[164:167], v[240:243], v[26:29]
	v_mfma_f32_16x16x32_bf16 v[78:81], v[160:163], v[204:207], v[78:81]
	v_mfma_f32_16x16x32_bf16 v[74:77], v[168:171], v[204:207], v[74:77]
	v_mfma_f32_16x16x32_bf16 v[62:65], v[160:163], v[212:215], v[62:65]
	v_mfma_f32_16x16x32_bf16 v[58:61], v[168:171], v[212:215], v[58:61]
	v_mfma_f32_16x16x32_bf16 v[46:49], v[160:163], v[220:223], v[46:49]
	v_mfma_f32_16x16x32_bf16 v[42:45], v[168:171], v[220:223], v[42:45]
	v_mfma_f32_16x16x32_bf16 v[30:33], v[160:163], v[244:247], v[30:33]
	v_mfma_f32_16x16x32_bf16 v[26:29], v[168:171], v[244:247], v[26:29]
	s_setprio 0
	s_setprio 1
	v_mfma_f32_16x16x32_bf16 v[70:73], v[172:175], v[200:203], v[70:73]
	v_mfma_f32_16x16x32_bf16 v[66:69], v[180:183], v[200:203], v[66:69]
	v_mfma_f32_16x16x32_bf16 v[54:57], v[172:175], v[208:211], v[54:57]
	v_mfma_f32_16x16x32_bf16 v[50:53], v[180:183], v[208:211], v[50:53]
	v_mfma_f32_16x16x32_bf16 v[38:41], v[172:175], v[216:219], v[38:41]
	v_mfma_f32_16x16x32_bf16 v[34:37], v[180:183], v[216:219], v[34:37]
	v_mfma_f32_16x16x32_bf16 v[22:25], v[172:175], v[240:243], v[22:25]
	v_mfma_f32_16x16x32_bf16 v[18:21], v[180:183], v[240:243], v[18:21]
	v_mfma_f32_16x16x32_bf16 v[70:73], v[176:179], v[204:207], v[70:73]
	v_mfma_f32_16x16x32_bf16 v[66:69], v[196:199], v[204:207], v[66:69]
	v_mfma_f32_16x16x32_bf16 v[54:57], v[176:179], v[212:215], v[54:57]
	v_mfma_f32_16x16x32_bf16 v[50:53], v[196:199], v[212:215], v[50:53]
	v_mfma_f32_16x16x32_bf16 v[38:41], v[176:179], v[220:223], v[38:41]
	v_mfma_f32_16x16x32_bf16 v[34:37], v[196:199], v[220:223], v[34:37]
	v_mfma_f32_16x16x32_bf16 v[22:25], v[176:179], v[244:247], v[22:25]
	v_mfma_f32_16x16x32_bf16 v[18:21], v[196:199], v[244:247], v[18:21]
	s_setprio 0
	s_barrier
	s_add_i32 s25, s25, 2
	s_add_u32 s2, s2, 0x100
	s_addc_u32 s24, s24, 0
	s_add_u32 s56, s56, 0x100
	s_addc_u32 s57, s57, 0
.LBB0_1463:
	s_add_u32 s14, s56, 0xfffc0080
	s_addc_u32 s15, s57, -1
	s_add_i32 s49, 0, 0x11000
	s_cmp_eq_u32 s25, 12
	s_cselect_b32 s15, s53, s15
	s_cselect_b32 s14, s52, s14
	v_add_u32_e32 v155, s49, v1
	s_cselect_b32 s35, s51, s24
	s_cselect_b32 s34, s50, s2
	s_add_i32 s55, 0, 0x15000
	ds_read_b128 v[156:159], v155
	ds_read_b128 v[160:163], v155 offset:1024
	ds_read_b128 v[164:167], v155 offset:2048
	ds_read_b128 v[168:171], v155 offset:3072
	v_add_u32_e32 v155, s55, v1
	ds_read_b128 v[172:175], v155
	ds_read_b128 v[176:179], v155 offset:1024
	ds_read_b128 v[180:183], v155 offset:2048
	ds_read_b128 v[196:199], v155 offset:3072
	v_lshl_add_u64 v[184:185], s[56:57], 0, v[152:153]
	s_add_i32 m0, s61, 0xd000
	ds_read_b128 v[200:203], v154 offset:4096
	ds_read_b128 v[204:207], v154 offset:5120
	ds_read_b128 v[208:211], v154 offset:6144
	ds_read_b128 v[212:215], v154 offset:7168
	ds_read_b128 v[216:219], v154 offset:8192
	ds_read_b128 v[220:223], v154 offset:9216
	ds_read_b128 v[240:243], v154 offset:10240
	ds_read_b128 v[244:247], v154 offset:11264
	global_load_lds_dwordx4 v[184:185], off
	v_lshl_add_u64 v[184:185], v[184:185], 0, s[82:83]
	s_add_i32 m0, s61, 0xf000
	s_nop 0
	global_load_lds_dwordx4 v[184:185], off
	s_waitcnt vmcnt(8)
	s_waitcnt lgkmcnt(0)
	s_barrier
	s_setprio 1
	s_waitcnt lgkmcnt(0)
	v_mfma_f32_16x16x32_bf16 v[142:145], v[156:159], v[200:203], v[142:145]
	v_mfma_f32_16x16x32_bf16 v[138:141], v[164:167], v[200:203], v[138:141]
	v_mfma_f32_16x16x32_bf16 v[126:129], v[156:159], v[208:211], v[126:129]
	v_mfma_f32_16x16x32_bf16 v[122:125], v[164:167], v[208:211], v[122:125]
	v_mfma_f32_16x16x32_bf16 v[110:113], v[156:159], v[216:219], v[110:113]
	v_mfma_f32_16x16x32_bf16 v[106:109], v[164:167], v[216:219], v[106:109]
	v_mfma_f32_16x16x32_bf16 v[94:97], v[156:159], v[240:243], v[94:97]
	v_mfma_f32_16x16x32_bf16 v[90:93], v[164:167], v[240:243], v[90:93]
	v_mfma_f32_16x16x32_bf16 v[142:145], v[160:163], v[204:207], v[142:145]
	v_mfma_f32_16x16x32_bf16 v[138:141], v[168:171], v[204:207], v[138:141]
	v_mfma_f32_16x16x32_bf16 v[126:129], v[160:163], v[212:215], v[126:129]
	v_mfma_f32_16x16x32_bf16 v[122:125], v[168:171], v[212:215], v[122:125]
	v_mfma_f32_16x16x32_bf16 v[110:113], v[160:163], v[220:223], v[110:113]
	v_mfma_f32_16x16x32_bf16 v[106:109], v[168:171], v[220:223], v[106:109]
	v_mfma_f32_16x16x32_bf16 v[94:97], v[160:163], v[244:247], v[94:97]
	v_mfma_f32_16x16x32_bf16 v[90:93], v[168:171], v[244:247], v[90:93]
	s_setprio 0
	s_setprio 1
	v_mfma_f32_16x16x32_bf16 v[134:137], v[172:175], v[200:203], v[134:137]
	v_mfma_f32_16x16x32_bf16 v[130:133], v[180:183], v[200:203], v[130:133]
	v_mfma_f32_16x16x32_bf16 v[118:121], v[172:175], v[208:211], v[118:121]
	v_mfma_f32_16x16x32_bf16 v[114:117], v[180:183], v[208:211], v[114:117]
	v_mfma_f32_16x16x32_bf16 v[102:105], v[172:175], v[216:219], v[102:105]
	v_mfma_f32_16x16x32_bf16 v[98:101], v[180:183], v[216:219], v[98:101]
	v_mfma_f32_16x16x32_bf16 v[86:89], v[172:175], v[240:243], v[86:89]
	v_mfma_f32_16x16x32_bf16 v[82:85], v[180:183], v[240:243], v[82:85]
	v_mfma_f32_16x16x32_bf16 v[134:137], v[176:179], v[204:207], v[134:137]
	v_mfma_f32_16x16x32_bf16 v[130:133], v[196:199], v[204:207], v[130:133]
	v_mfma_f32_16x16x32_bf16 v[118:121], v[176:179], v[212:215], v[118:121]
	v_mfma_f32_16x16x32_bf16 v[114:117], v[196:199], v[212:215], v[114:117]
	v_mfma_f32_16x16x32_bf16 v[102:105], v[176:179], v[220:223], v[102:105]
	v_mfma_f32_16x16x32_bf16 v[98:101], v[196:199], v[220:223], v[98:101]
	v_mfma_f32_16x16x32_bf16 v[86:89], v[176:179], v[244:247], v[86:89]
	v_mfma_f32_16x16x32_bf16 v[82:85], v[196:199], v[244:247], v[82:85]
	s_setprio 0
	s_barrier
	v_lshl_add_u64 v[184:185], s[34:35], 0, v[186:187]
	s_add_i32 s34, s49, s28
	s_mov_b32 m0, s34
	global_load_lds_dwordx4 v[184:185], off
	v_lshl_add_u64 v[192:193], v[184:185], 0, s[82:83]
	s_add_i32 m0, s34, 0x2000
	s_add_i32 s34, s55, s28
	global_load_lds_dwordx4 v[192:193], off
	v_lshl_add_u64 v[192:193], v[184:185], 0, s[64:65]
	s_mov_b32 m0, s34
	s_nop 0
	global_load_lds_dwordx4 v[192:193], off
	v_lshl_add_u64 v[192:193], v[184:185], 0, s[86:87]
	s_add_i32 m0, s34, 0x2000
	s_nop 0
	global_load_lds_dwordx4 v[192:193], off
	v_lshl_add_u64 v[192:193], s[14:15], 0, v[146:147]
	s_mov_b32 m0, s68
	v_lshl_add_u64 v[224:225], v[192:193], 0, s[82:83]
	global_load_lds_dwordx4 v[192:193], off
	s_mov_b32 m0, s69
	s_nop 0
	global_load_lds_dwordx4 v[224:225], off
	ds_read_b128 v[200:203], v154 offset:20480
	ds_read_b128 v[204:207], v154 offset:21504
	ds_read_b128 v[208:211], v154 offset:22528
	ds_read_b128 v[212:215], v154 offset:23552
	ds_read_b128 v[216:219], v154 offset:24576
	ds_read_b128 v[220:223], v154 offset:25600
	ds_read_b128 v[240:243], v154 offset:26624
	ds_read_b128 v[244:247], v154 offset:27648
	s_waitcnt vmcnt(8)
	s_waitcnt lgkmcnt(0)
	s_barrier
	s_setprio 1
	s_waitcnt lgkmcnt(0)
	v_mfma_f32_16x16x32_bf16 v[78:81], v[156:159], v[200:203], v[78:81]
	v_mfma_f32_16x16x32_bf16 v[74:77], v[164:167], v[200:203], v[74:77]
	v_mfma_f32_16x16x32_bf16 v[62:65], v[156:159], v[208:211], v[62:65]
	v_mfma_f32_16x16x32_bf16 v[58:61], v[164:167], v[208:211], v[58:61]
	v_mfma_f32_16x16x32_bf16 v[46:49], v[156:159], v[216:219], v[46:49]
	v_mfma_f32_16x16x32_bf16 v[42:45], v[164:167], v[216:219], v[42:45]
	v_mfma_f32_16x16x32_bf16 v[30:33], v[156:159], v[240:243], v[30:33]
	v_mfma_f32_16x16x32_bf16 v[26:29], v[164:167], v[240:243], v[26:29]
	v_mfma_f32_16x16x32_bf16 v[78:81], v[160:163], v[204:207], v[78:81]
	v_mfma_f32_16x16x32_bf16 v[74:77], v[168:171], v[204:207], v[74:77]
	v_mfma_f32_16x16x32_bf16 v[62:65], v[160:163], v[212:215], v[62:65]
	v_mfma_f32_16x16x32_bf16 v[58:61], v[168:171], v[212:215], v[58:61]
	v_mfma_f32_16x16x32_bf16 v[46:49], v[160:163], v[220:223], v[46:49]
	v_mfma_f32_16x16x32_bf16 v[42:45], v[168:171], v[220:223], v[42:45]
	v_mfma_f32_16x16x32_bf16 v[30:33], v[160:163], v[244:247], v[30:33]
	v_mfma_f32_16x16x32_bf16 v[26:29], v[168:171], v[244:247], v[26:29]
	s_setprio 0
	s_setprio 1
	v_mfma_f32_16x16x32_bf16 v[70:73], v[172:175], v[200:203], v[70:73]
	v_mfma_f32_16x16x32_bf16 v[66:69], v[180:183], v[200:203], v[66:69]
	v_mfma_f32_16x16x32_bf16 v[54:57], v[172:175], v[208:211], v[54:57]
	v_mfma_f32_16x16x32_bf16 v[50:53], v[180:183], v[208:211], v[50:53]
	v_mfma_f32_16x16x32_bf16 v[38:41], v[172:175], v[216:219], v[38:41]
	v_mfma_f32_16x16x32_bf16 v[34:37], v[180:183], v[216:219], v[34:37]
	v_mfma_f32_16x16x32_bf16 v[22:25], v[172:175], v[240:243], v[22:25]
	v_mfma_f32_16x16x32_bf16 v[18:21], v[180:183], v[240:243], v[18:21]
	v_mfma_f32_16x16x32_bf16 v[70:73], v[176:179], v[204:207], v[70:73]
	v_mfma_f32_16x16x32_bf16 v[66:69], v[196:199], v[204:207], v[66:69]
	v_mfma_f32_16x16x32_bf16 v[54:57], v[176:179], v[212:215], v[54:57]
	v_mfma_f32_16x16x32_bf16 v[50:53], v[196:199], v[212:215], v[50:53]
	v_mfma_f32_16x16x32_bf16 v[38:41], v[176:179], v[220:223], v[38:41]
	v_mfma_f32_16x16x32_bf16 v[34:37], v[196:199], v[220:223], v[34:37]
	v_mfma_f32_16x16x32_bf16 v[22:25], v[176:179], v[244:247], v[22:25]
	v_mfma_f32_16x16x32_bf16 v[18:21], v[196:199], v[244:247], v[18:21]
	s_setprio 0
	s_barrier
	s_add_i32 s14, 0, 0x19000
	v_add_u32_e32 v155, s14, v1
	s_add_i32 s15, 0, 0x1d000
	ds_read_b128 v[156:159], v155
	ds_read_b128 v[160:163], v155 offset:1024
	ds_read_b128 v[164:167], v155 offset:2048
	ds_read_b128 v[168:171], v155 offset:3072
	v_add_u32_e32 v155, s15, v1
	ds_read_b128 v[172:175], v155
	ds_read_b128 v[176:179], v155 offset:1024
	ds_read_b128 v[180:183], v155 offset:2048
	ds_read_b128 v[196:199], v155 offset:3072
	s_mov_b32 m0, s70
	v_lshl_add_u64 v[224:225], v[192:193], 0, s[64:65]
	ds_read_b128 v[200:203], v154 offset:36864
	ds_read_b128 v[204:207], v154 offset:37888
	ds_read_b128 v[208:211], v154 offset:38912
	ds_read_b128 v[212:215], v154 offset:39936
	ds_read_b128 v[216:219], v154 offset:40960
	ds_read_b128 v[220:223], v154 offset:41984
	ds_read_b128 v[240:243], v154 offset:43008
	ds_read_b128 v[244:247], v154 offset:44032
	global_load_lds_dwordx4 v[224:225], off
	v_lshl_add_u64 v[224:225], v[192:193], 0, s[86:87]
	s_mov_b32 m0, s71
	s_nop 0
	global_load_lds_dwordx4 v[224:225], off
	s_waitcnt vmcnt(8)
	s_waitcnt lgkmcnt(0)
	s_barrier
	s_setprio 1
	s_waitcnt lgkmcnt(0)
	v_mfma_f32_16x16x32_bf16 v[142:145], v[156:159], v[200:203], v[142:145]
	v_mfma_f32_16x16x32_bf16 v[138:141], v[164:167], v[200:203], v[138:141]
	v_mfma_f32_16x16x32_bf16 v[126:129], v[156:159], v[208:211], v[126:129]
	v_mfma_f32_16x16x32_bf16 v[122:125], v[164:167], v[208:211], v[122:125]
	v_mfma_f32_16x16x32_bf16 v[110:113], v[156:159], v[216:219], v[110:113]
	v_mfma_f32_16x16x32_bf16 v[106:109], v[164:167], v[216:219], v[106:109]
	v_mfma_f32_16x16x32_bf16 v[94:97], v[156:159], v[240:243], v[94:97]
	v_mfma_f32_16x16x32_bf16 v[90:93], v[164:167], v[240:243], v[90:93]
	v_mfma_f32_16x16x32_bf16 v[142:145], v[160:163], v[204:207], v[142:145]
	v_mfma_f32_16x16x32_bf16 v[138:141], v[168:171], v[204:207], v[138:141]
	v_mfma_f32_16x16x32_bf16 v[126:129], v[160:163], v[212:215], v[126:129]
	v_mfma_f32_16x16x32_bf16 v[122:125], v[168:171], v[212:215], v[122:125]
	v_mfma_f32_16x16x32_bf16 v[110:113], v[160:163], v[220:223], v[110:113]
	v_mfma_f32_16x16x32_bf16 v[106:109], v[168:171], v[220:223], v[106:109]
	v_mfma_f32_16x16x32_bf16 v[94:97], v[160:163], v[244:247], v[94:97]
	v_mfma_f32_16x16x32_bf16 v[90:93], v[168:171], v[244:247], v[90:93]
	s_setprio 0
	s_setprio 1
	v_mfma_f32_16x16x32_bf16 v[134:137], v[172:175], v[200:203], v[134:137]
	v_mfma_f32_16x16x32_bf16 v[130:133], v[180:183], v[200:203], v[130:133]
	v_mfma_f32_16x16x32_bf16 v[118:121], v[172:175], v[208:211], v[118:121]
	v_mfma_f32_16x16x32_bf16 v[114:117], v[180:183], v[208:211], v[114:117]
	v_mfma_f32_16x16x32_bf16 v[102:105], v[172:175], v[216:219], v[102:105]
	v_mfma_f32_16x16x32_bf16 v[98:101], v[180:183], v[216:219], v[98:101]
	v_mfma_f32_16x16x32_bf16 v[86:89], v[172:175], v[240:243], v[86:89]
	v_mfma_f32_16x16x32_bf16 v[82:85], v[180:183], v[240:243], v[82:85]
	v_mfma_f32_16x16x32_bf16 v[134:137], v[176:179], v[204:207], v[134:137]
	v_mfma_f32_16x16x32_bf16 v[130:133], v[196:199], v[204:207], v[130:133]
	v_mfma_f32_16x16x32_bf16 v[118:121], v[176:179], v[212:215], v[118:121]
	v_mfma_f32_16x16x32_bf16 v[114:117], v[196:199], v[212:215], v[114:117]
	v_mfma_f32_16x16x32_bf16 v[102:105], v[176:179], v[220:223], v[102:105]
	v_mfma_f32_16x16x32_bf16 v[98:101], v[196:199], v[220:223], v[98:101]
	v_mfma_f32_16x16x32_bf16 v[86:89], v[176:179], v[244:247], v[86:89]
	v_mfma_f32_16x16x32_bf16 v[82:85], v[196:199], v[244:247], v[82:85]
	s_setprio 0
	s_barrier
	s_add_i32 s14, s14, s28
	v_lshl_add_u64 v[224:225], v[184:185], 0, s[92:93]
	s_mov_b32 m0, s14
	global_load_lds_dwordx4 v[224:225], off
	v_lshl_add_u64 v[224:225], v[184:185], 0, s[4:5]
	s_add_i32 m0, s14, 0x2000
	s_add_i32 s14, s15, s28
	global_load_lds_dwordx4 v[224:225], off
	v_lshl_add_u64 v[224:225], v[184:185], 0, s[6:7]
	s_mov_b32 m0, s14
	v_lshl_add_u64 v[184:185], v[184:185], 0, s[8:9]
	global_load_lds_dwordx4 v[224:225], off
	s_add_i32 m0, s14, 0x2000
	s_nop 0
	global_load_lds_dwordx4 v[184:185], off
	v_lshl_add_u64 v[184:185], v[192:193], 0, s[92:93]
	s_mov_b32 m0, s75
	s_nop 0
	global_load_lds_dwordx4 v[184:185], off
	v_lshl_add_u64 v[184:185], v[192:193], 0, s[4:5]
	s_mov_b32 m0, s76
	s_nop 0
	global_load_lds_dwordx4 v[184:185], off
	ds_read_b128 v[200:203], v154 offset:53248
	ds_read_b128 v[204:207], v154 offset:54272
	ds_read_b128 v[208:211], v154 offset:55296
	ds_read_b128 v[212:215], v154 offset:56320
	ds_read_b128 v[216:219], v154 offset:57344
	ds_read_b128 v[220:223], v154 offset:58368
	ds_read_b128 v[240:243], v154 offset:59392
	ds_read_b128 v[244:247], v154 offset:60416
	s_waitcnt vmcnt(8)
	s_waitcnt lgkmcnt(0)
	s_barrier
	s_setprio 1
	s_waitcnt lgkmcnt(0)
	v_mfma_f32_16x16x32_bf16 v[78:81], v[156:159], v[200:203], v[78:81]
	v_mfma_f32_16x16x32_bf16 v[74:77], v[164:167], v[200:203], v[74:77]
	v_mfma_f32_16x16x32_bf16 v[62:65], v[156:159], v[208:211], v[62:65]
	v_mfma_f32_16x16x32_bf16 v[58:61], v[164:167], v[208:211], v[58:61]
	v_mfma_f32_16x16x32_bf16 v[46:49], v[156:159], v[216:219], v[46:49]
	v_mfma_f32_16x16x32_bf16 v[42:45], v[164:167], v[216:219], v[42:45]
	v_mfma_f32_16x16x32_bf16 v[30:33], v[156:159], v[240:243], v[30:33]
	v_mfma_f32_16x16x32_bf16 v[26:29], v[164:167], v[240:243], v[26:29]
	v_mfma_f32_16x16x32_bf16 v[78:81], v[160:163], v[204:207], v[78:81]
	v_mfma_f32_16x16x32_bf16 v[74:77], v[168:171], v[204:207], v[74:77]
	v_mfma_f32_16x16x32_bf16 v[62:65], v[160:163], v[212:215], v[62:65]
	v_mfma_f32_16x16x32_bf16 v[58:61], v[168:171], v[212:215], v[58:61]
	v_mfma_f32_16x16x32_bf16 v[46:49], v[160:163], v[220:223], v[46:49]
	v_mfma_f32_16x16x32_bf16 v[42:45], v[168:171], v[220:223], v[42:45]
	v_mfma_f32_16x16x32_bf16 v[30:33], v[160:163], v[244:247], v[30:33]
	v_mfma_f32_16x16x32_bf16 v[26:29], v[168:171], v[244:247], v[26:29]
	s_setprio 0
	s_setprio 1
	v_mfma_f32_16x16x32_bf16 v[70:73], v[172:175], v[200:203], v[70:73]
	v_mfma_f32_16x16x32_bf16 v[66:69], v[180:183], v[200:203], v[66:69]
	v_mfma_f32_16x16x32_bf16 v[54:57], v[172:175], v[208:211], v[54:57]
	v_mfma_f32_16x16x32_bf16 v[50:53], v[180:183], v[208:211], v[50:53]
	v_mfma_f32_16x16x32_bf16 v[38:41], v[172:175], v[216:219], v[38:41]
	v_mfma_f32_16x16x32_bf16 v[34:37], v[180:183], v[216:219], v[34:37]
	v_mfma_f32_16x16x32_bf16 v[22:25], v[172:175], v[240:243], v[22:25]
	v_mfma_f32_16x16x32_bf16 v[18:21], v[180:183], v[240:243], v[18:21]
	v_mfma_f32_16x16x32_bf16 v[70:73], v[176:179], v[204:207], v[70:73]
	v_mfma_f32_16x16x32_bf16 v[66:69], v[196:199], v[204:207], v[66:69]
	v_mfma_f32_16x16x32_bf16 v[54:57], v[176:179], v[212:215], v[54:57]
	v_mfma_f32_16x16x32_bf16 v[50:53], v[196:199], v[212:215], v[50:53]
	v_mfma_f32_16x16x32_bf16 v[38:41], v[176:179], v[220:223], v[38:41]
	v_mfma_f32_16x16x32_bf16 v[34:37], v[196:199], v[220:223], v[34:37]
	v_mfma_f32_16x16x32_bf16 v[22:25], v[176:179], v[244:247], v[22:25]
	v_mfma_f32_16x16x32_bf16 v[18:21], v[196:199], v[244:247], v[18:21]
	s_setprio 0
	s_barrier
	s_add_i32 s25, s25, 2
	s_add_u32 s2, s2, 0x100
	s_addc_u32 s24, s24, 0
	s_add_u32 s56, s56, 0x100
	s_addc_u32 s57, s57, 0
	s_cmp_gt_u32 s25, 13
	s_cbranch_scc0 .LBB0_1463
	s_and_b64 vcc, exec, s[46:47]
	s_cbranch_vccz .LBB0_1466
	s_barrier
